# gate epilogues rewritten with 2-row-ahead loads and rcp sigmoid; moe m-tiles interleaved across waves with a no-third-tile loop copy; first seam dropped; barrier set-up loads batched
# speedup vs baseline: 1.0198x; 1.0025x over previous
; #define IN(k) (((PHMASK >> PHBIT(k)) & 1u) && lo <= (k) && (k) < hi)
; #define SEAM(k) do { if (IN(k) && IN((k) + 1)) xcd_barrier(bar); } while (0)
; #define DUP(bit) if constexpr (((PROBE_DUP >> (bit)) & 1u) != 0u)
; __device__ __forceinline__ void xcd_barrier(const XcdBarrier& b) {
;     asm volatile("s_waitcnt vmcnt(0)" ::: "memory");
;     __syncthreads();
;     if (threadIdx.x == 0) {
;         unsigned* bar = b.bar;
;         __builtin_amdgcn_s_waitcnt(0);
;         unsigned nloc = b.st[0], nx = b.st[1];
;         if (nloc == 0u) { xcd_barrier_complete(bar, b.x, nloc, nx); b.st[0] = nloc; b.st[1] = nx; }
; __global__ void __launch_bounds__(NTHR, 2) mk_fwd(ArgsV argsv) {
;     ...
;     if (IN(0)) { { PH_BEGIN(); phase_convert<2>(a, 0, lds, gw, NGW, wave, lane); } DUP(PB_CONVERT) { PH_BEGIN(); phase_convert<2>(a, 0, lds, gw, NGW, wave, lane); } } SEAM(0);
.LBB0_139:
	s_cmp_lt_i32 s77, 2
	s_cselect_b64 s[2:3], -1, 0
	s_mov_b64 s[4:5], -1
	s_xor_b64 s[0:1], s[0:1], -1
	v_writelane_b32 v254, s4, 1
	s_or_b64 s[0:1], s[0:1], s[2:3]
	s_and_b64 vcc, exec, s[0:1]
	v_writelane_b32 v254, s5, 2
	s_branch .LBB0_189
	s_waitcnt vmcnt(0)
	v_cmp_eq_u32_e32 vcc, 0, v0
	s_barrier
	s_and_saveexec_b64 s[0:1], vcc
	s_cbranch_execz .LBB0_188
	v_readlane_b32 s2, v254, 0
	s_waitcnt vmcnt(0) expcnt(0) lgkmcnt(0)
	s_nop 0
	v_mov_b32_e32 v1, s2
	ds_read_b32 v3, v1
	ds_read_b32 v1, v1 offset:4
	s_waitcnt lgkmcnt(1)
	v_cmp_ne_u32_e32 vcc, 0, v3
	s_cbranch_vccnz .LBB0_156
	s_load_dwordx2 s[4:5], s[74:75], 0x120
	s_load_dword s9, s[74:75], 0x128
	s_load_dwordx4 s[40:43], s[74:75], 0x108
	v_mov_b32_e32 v17, 0
	s_waitcnt lgkmcnt(0)
	s_mul_i32 s4, s5, s4
	s_mul_i32 s4, s4, s9
	s_add_u32 s2, s42, 0x4200
	s_addc_u32 s3, s43, 0
	s_add_u32 s8, s42, 0x4400
	s_addc_u32 s9, s43, 0
	s_add_u32 s10, s42, 0x4500
	s_addc_u32 s11, s43, 0
	s_add_u32 s12, s42, 0x4600
	s_addc_u32 s13, s43, 0
	s_add_u32 s14, s42, 0x4700
	s_addc_u32 s15, s43, 0
	s_add_u32 s16, s42, 0x4800
	s_addc_u32 s17, s43, 0
	s_add_u32 s18, s42, 0x4900
	s_addc_u32 s19, s43, 0
	s_add_u32 s20, s42, 0x4a00
	s_addc_u32 s21, s43, 0
	s_add_u32 s22, s42, 0x4b00
	s_addc_u32 s23, s43, 0
	s_add_u32 s24, s42, 0x4c00
	s_addc_u32 s25, s43, 0
	s_add_u32 s26, s42, 0x4d00
	s_addc_u32 s27, s43, 0
	s_add_u32 s28, s42, 0x4e00
	s_addc_u32 s29, s43, 0
	s_add_u32 s30, s42, 0x4f00
	s_addc_u32 s31, s43, 0
	s_add_u32 s34, s42, 0x5000
	s_addc_u32 s35, s43, 0
	s_add_u32 s36, s42, 0x5100
	s_addc_u32 s37, s43, 0
	s_add_u32 s38, s42, 0x5200
	s_addc_u32 s39, s43, 0
	s_add_u32 s40, s42, 0x5300
	s_addc_u32 s41, s43, 0
	s_mov_b32 s5, 1
	s_branch .LBB0_144

; __device__ __forceinline__ unsigned xb_ld(unsigned* p)              { return __hip_atomic_load(p, __ATOMIC_RELAXED, __HIP_MEMORY_SCOPE_AGENT); }
; __device__ __forceinline__ void xcd_barrier_complete(unsigned* bar, unsigned x, unsigned& nloc, unsigned& nx) {
;     const unsigned G = gridDim.x * gridDim.y * gridDim.z;
;     unsigned sum, cnt, mine, sp = 0u;
;     for (;;) {
;         sum = 0u; cnt = 0u; mine = 0u;
; #pragma unroll
;         for (unsigned j = 0; j < 16; ++j) { const unsigned c = xb_ld(&bar[XB_XCNT(j)]); sum += c; cnt += (c > 0u) ? 1u : 0u; mine = (j == x) ? c : mine; }
;         if (sum == G) break;
;         __builtin_amdgcn_s_sleep(1);
;         if ((++sp & 255u) == 0u) { if (xb_ld(&bar[XB_TMO])) break; if (sp > XB_SPIN_CAP) { atomicAdd(&bar[XB_TMO], 1u); break; } }
;     }
.LBB0_261:
	v_readlane_b32 s2, v254, 5
	v_readlane_b32 s3, v254, 6
	s_mov_b64 s[12:13], -1
	s_nop 3
	global_load_dword v2, v91, s[2:3] sc1
	global_load_dword v3, v91, s[2:3] offset:256 sc1
	global_load_dword v4, v91, s[2:3] offset:512 sc1
	global_load_dword v5, v91, s[2:3] offset:768 sc1
	global_load_dword v6, v91, s[2:3] offset:1024 sc1
	global_load_dword v7, v91, s[2:3] offset:1280 sc1
	global_load_dword v8, v91, s[2:3] offset:1536 sc1
	global_load_dword v9, v91, s[2:3] offset:1792 sc1
	global_load_dword v10, v91, s[2:3] offset:2048 sc1
	global_load_dword v11, v91, s[2:3] offset:2304 sc1
	global_load_dword v12, v91, s[2:3] offset:2560 sc1
	global_load_dword v13, v91, s[2:3] offset:2816 sc1
	global_load_dword v14, v91, s[2:3] offset:3072 sc1
	global_load_dword v15, v91, s[2:3] offset:3328 sc1
	global_load_dword v16, v91, s[2:3] offset:3584 sc1
	global_load_dword v17, v91, s[2:3] offset:3840 sc1
	s_waitcnt vmcnt(0)
	v_add_u32_e32 v18, v3, v2
	v_add_u32_e32 v18, v18, v4
	v_add_u32_e32 v18, v18, v5
	v_add_u32_e32 v18, v18, v6
	v_add_u32_e32 v18, v18, v7
	v_add_u32_e32 v18, v18, v8
	v_add_u32_e32 v18, v18, v9
	v_add_u32_e32 v18, v18, v10
	v_add_u32_e32 v18, v18, v11
	v_add_u32_e32 v18, v18, v12
	v_add_u32_e32 v18, v18, v13
	v_add_u32_e32 v18, v18, v14
	v_add_u32_e32 v18, v18, v15
	v_add_u32_e32 v18, v18, v16
	v_add_u32_e32 v18, v18, v17
	s_mov_b64 s[2:3], -1
	v_cmp_eq_u32_e32 vcc, s1, v18
	s_cbranch_vccnz .LBB0_260
	s_and_b32 s2, s4, 0xff
	s_cmp_eq_u32 s2, 0
	s_mov_b64 s[2:3], -1
	s_mov_b64 s[24:25], -1
	s_sleep 1
	s_cbranch_scc0 .LBB0_265
	v_readlane_b32 s2, v254, 3
	v_readlane_b32 s3, v254, 4
	s_nop 4
	global_load_dword v18, v91, s[2:3] sc1
	s_waitcnt vmcnt(0)
	v_cmp_eq_u32_e32 vcc, 0, v18
	s_cbranch_vccnz .LBB0_267
	s_mov_b64 s[24:25], 0
	s_mov_b64 s[2:3], -1

; DI unsigned pk2(float a, float b) { f32x2 v = {a, b}; bf16x2_t r = __builtin_convertvector(v, bf16x2_t); return __builtin_bit_cast(unsigned, r); }
; DI float sigmoidf_(float x) { return 1.f / (1.f + __expf(-x)); }
;     DI void operator()(const f32x4 (&acc)[2][2][4][2], const Unit& u, int wr, int wc, int fr, int fq) const {
;         const int row0 = u.pm * BM + wr * 64 + fr, col0 = u.pn * BM + wc * 32 + 8 * fq;
; #pragma unroll
;         for (int ai = 0; ai < 2; ++ai)
; #pragma unroll
;             for (int m = 0; m < 4; ++m) { const size_t row = (size_t)(row0 + ai * HALF + m * 16);
;                 u32x4 gzs[2], ts[2];
; #pragma unroll
;                 for (int bj = 0; bj < 2; ++bj) { const int col = col0 + bj * HALF; gzs[bj] = *(const u32x4*)(Zg + row * NZ + goff + col); if (add) ts[bj] = *(const u32x4*)(add + row * D + col); else ts[bj] = (u32x4){0u, 0u, 0u, 0u}; }
; #pragma unroll
;                 for (int bj = 0; bj < 2; ++bj) {
;                     const int col = col0 + bj * HALF;
;                     const u32x4 gz = gzs[bj];
;                     float a[8] = {0.f, 0.f, 0.f, 0.f, 0.f, 0.f, 0.f, 0.f};
;                     if (add) { const u32x4 t = ts[bj]; a[0] = bflo(t.x); a[1] = bfhi(t.x); a[2] = bflo(t.y); a[3] = bfhi(t.y); a[4] = bflo(t.z); a[5] = bfhi(t.z); a[6] = bflo(t.w); a[7] = bfhi(t.w); }
;                     const f32x4 v0 = acc[ai][bj][m][0], v1 = acc[ai][bj][m][1];
;                     float o[8];
;                     o[0] = a[0] + sigmoidf_(bflo(gz.x)) * v0[0]; o[1] = a[1] + sigmoidf_(bfhi(gz.x)) * v0[1];
;                     o[2] = a[2] + sigmoidf_(bflo(gz.y)) * v0[2]; o[3] = a[3] + sigmoidf_(bfhi(gz.y)) * v0[3];
;                     o[4] = a[4] + sigmoidf_(bflo(gz.z)) * v1[0]; o[5] = a[5] + sigmoidf_(bfhi(gz.z)) * v1[1];
;                     o[6] = a[6] + sigmoidf_(bflo(gz.w)) * v1[2]; o[7] = a[7] + sigmoidf_(bfhi(gz.w)) * v1[3];
;                     u32x4 w; w.x = pk2(o[0], o[1]); w.y = pk2(o[2], o[3]); w.z = pk2(o[4], o[5]); w.w = pk2(o[6], o[7]);
;                     *(u32x4*)(O + row * D + col) = w; } }
.LBB0_1405:
	v_lshl_add_u32 v214, s12, 8, v159
	v_lshl_or_b32 v216, s0, 8, v161
	v_lshlrev_b32_e32 v216, 1, v216
	v_mov_b32_e32 v213, 0
	v_mov_b32_e32 v212, v216
	v_lshl_add_u64 v[208:209], s[8:9], 0, v[212:213]
	v_lshl_add_u64 v[204:205], s[40:41], 0, v[212:213]
	v_add_u32_e32 v215, 0, v214
	v_mad_i64_i32 v[206:207], s[24:25], v215, s15, v[204:205]
	global_load_dwordx4 v[172:175], v[206:207], off offset:3072
	global_load_dwordx4 v[176:179], v[206:207], off offset:3328
	v_add_u32_e32 v215, 16, v214
	v_mad_i64_i32 v[206:207], s[24:25], v215, s15, v[204:205]
	global_load_dwordx4 v[180:183], v[206:207], off offset:3072
	global_load_dwordx4 v[184:187], v[206:207], off offset:3328
	v_add_u32_e32 v215, 32, v214
	v_mad_i64_i32 v[206:207], s[24:25], v215, s15, v[204:205]
	global_load_dwordx4 v[188:191], v[206:207], off offset:3072
	global_load_dwordx4 v[192:195], v[206:207], off offset:3328
	v_add_u32_e32 v215, 0, v214
	v_lshlrev_b32_e32 v212, 12, v215
	v_lshl_add_u64 v[210:211], v[208:209], 0, v[212:213]
	s_waitcnt vmcnt(5)
	v_lshlrev_b32_e32 v200, 16, v172
	v_and_b32_e32 v201, 0xffff0000, v172
	v_lshlrev_b32_e32 v202, 16, v173
	v_and_b32_e32 v203, 0xffff0000, v173
	v_mul_f32_e32 v200, 0xbfb8aa3b, v200
	v_mul_f32_e32 v201, 0xbfb8aa3b, v201
	v_mul_f32_e32 v202, 0xbfb8aa3b, v202
	v_mul_f32_e32 v203, 0xbfb8aa3b, v203
	v_exp_f32_e32 v200, v200
	v_exp_f32_e32 v201, v201
	v_exp_f32_e32 v202, v202
	v_exp_f32_e32 v203, v203
	v_pk_add_f32 v[200:201], v[200:201], 1.0 op_sel_hi:[1,0]
	v_pk_add_f32 v[202:203], v[202:203], 1.0 op_sel_hi:[1,0]
	v_rcp_f32_e32 v200, v200
	v_rcp_f32_e32 v201, v201
	v_rcp_f32_e32 v202, v202
	v_rcp_f32_e32 v203, v203
	v_pk_mul_f32 v[200:201], v[132:133], v[200:201]
	v_pk_mul_f32 v[202:203], v[134:135], v[202:203]
	v_cvt_pk_bf16_f32 v172, v200, v201
	v_cvt_pk_bf16_f32 v173, v202, v203
	v_lshlrev_b32_e32 v200, 16, v174
	v_and_b32_e32 v201, 0xffff0000, v174
	v_lshlrev_b32_e32 v202, 16, v175
	v_and_b32_e32 v203, 0xffff0000, v175
	v_mul_f32_e32 v200, 0xbfb8aa3b, v200
	v_mul_f32_e32 v201, 0xbfb8aa3b, v201
	v_mul_f32_e32 v202, 0xbfb8aa3b, v202
	v_mul_f32_e32 v203, 0xbfb8aa3b, v203
	v_exp_f32_e32 v200, v200
	v_exp_f32_e32 v201, v201
	v_exp_f32_e32 v202, v202
	v_exp_f32_e32 v203, v203
	v_pk_add_f32 v[200:201], v[200:201], 1.0 op_sel_hi:[1,0]
	v_pk_add_f32 v[202:203], v[202:203], 1.0 op_sel_hi:[1,0]
	v_rcp_f32_e32 v200, v200
	v_rcp_f32_e32 v201, v201
	v_rcp_f32_e32 v202, v202
	v_rcp_f32_e32 v203, v203
	v_pk_mul_f32 v[200:201], v[124:125], v[200:201]
	v_pk_mul_f32 v[202:203], v[126:127], v[202:203]
	v_cvt_pk_bf16_f32 v174, v200, v201
	v_cvt_pk_bf16_f32 v175, v202, v203
	global_store_dwordx4 v[210:211], v[172:175], off
	s_waitcnt vmcnt(5)
	v_lshlrev_b32_e32 v200, 16, v176
	v_and_b32_e32 v201, 0xffff0000, v176
	v_lshlrev_b32_e32 v202, 16, v177
	v_and_b32_e32 v203, 0xffff0000, v177
	v_mul_f32_e32 v200, 0xbfb8aa3b, v200
	v_mul_f32_e32 v201, 0xbfb8aa3b, v201
	v_mul_f32_e32 v202, 0xbfb8aa3b, v202
	v_mul_f32_e32 v203, 0xbfb8aa3b, v203
	v_exp_f32_e32 v200, v200
	v_exp_f32_e32 v201, v201
	v_exp_f32_e32 v202, v202
	v_exp_f32_e32 v203, v203
	v_pk_add_f32 v[200:201], v[200:201], 1.0 op_sel_hi:[1,0]
	v_pk_add_f32 v[202:203], v[202:203], 1.0 op_sel_hi:[1,0]
	v_rcp_f32_e32 v200, v200
	v_rcp_f32_e32 v201, v201
	v_rcp_f32_e32 v202, v202
	v_rcp_f32_e32 v203, v203
	v_pk_mul_f32 v[200:201], v[120:121], v[200:201]
	v_pk_mul_f32 v[202:203], v[122:123], v[202:203]
	v_cvt_pk_bf16_f32 v176, v200, v201
	v_cvt_pk_bf16_f32 v177, v202, v203
	v_lshlrev_b32_e32 v200, 16, v178
	v_and_b32_e32 v201, 0xffff0000, v178
	v_lshlrev_b32_e32 v202, 16, v179
	v_and_b32_e32 v203, 0xffff0000, v179
	v_mul_f32_e32 v200, 0xbfb8aa3b, v200
	v_mul_f32_e32 v201, 0xbfb8aa3b, v201
	v_mul_f32_e32 v202, 0xbfb8aa3b, v202
	v_mul_f32_e32 v203, 0xbfb8aa3b, v203
	v_exp_f32_e32 v200, v200
	v_exp_f32_e32 v201, v201
	v_exp_f32_e32 v202, v202
	v_exp_f32_e32 v203, v203
	v_pk_add_f32 v[200:201], v[200:201], 1.0 op_sel_hi:[1,0]
	v_pk_add_f32 v[202:203], v[202:203], 1.0 op_sel_hi:[1,0]
	v_rcp_f32_e32 v200, v200
	v_rcp_f32_e32 v201, v201
	v_rcp_f32_e32 v202, v202
	v_rcp_f32_e32 v203, v203
	v_pk_mul_f32 v[200:201], v[116:117], v[200:201]
	v_pk_mul_f32 v[202:203], v[118:119], v[202:203]
	v_cvt_pk_bf16_f32 v178, v200, v201
	v_cvt_pk_bf16_f32 v179, v202, v203
	global_store_dwordx4 v[210:211], v[176:179], off offset:256
	v_add_u32_e32 v215, 48, v214
	v_mad_i64_i32 v[206:207], s[24:25], v215, s15, v[204:205]
	global_load_dwordx4 v[172:175], v[206:207], off offset:3072
	global_load_dwordx4 v[176:179], v[206:207], off offset:3328
	v_add_u32_e32 v215, 16, v214
	v_lshlrev_b32_e32 v212, 12, v215
	v_lshl_add_u64 v[210:211], v[208:209], 0, v[212:213]
	s_waitcnt vmcnt(7)
	v_lshlrev_b32_e32 v200, 16, v180
	v_and_b32_e32 v201, 0xffff0000, v180
	v_lshlrev_b32_e32 v202, 16, v181
	v_and_b32_e32 v203, 0xffff0000, v181
	v_mul_f32_e32 v200, 0xbfb8aa3b, v200
	v_mul_f32_e32 v201, 0xbfb8aa3b, v201
	v_mul_f32_e32 v202, 0xbfb8aa3b, v202
	v_mul_f32_e32 v203, 0xbfb8aa3b, v203
	v_exp_f32_e32 v200, v200
	v_exp_f32_e32 v201, v201
	v_exp_f32_e32 v202, v202
	v_exp_f32_e32 v203, v203
	v_pk_add_f32 v[200:201], v[200:201], 1.0 op_sel_hi:[1,0]
	v_pk_add_f32 v[202:203], v[202:203], 1.0 op_sel_hi:[1,0]
	v_rcp_f32_e32 v200, v200
	v_rcp_f32_e32 v201, v201
	v_rcp_f32_e32 v202, v202
	v_rcp_f32_e32 v203, v203
	v_pk_mul_f32 v[200:201], v[112:113], v[200:201]
	v_pk_mul_f32 v[202:203], v[114:115], v[202:203]
	v_cvt_pk_bf16_f32 v180, v200, v201
	v_cvt_pk_bf16_f32 v181, v202, v203
	v_lshlrev_b32_e32 v200, 16, v182
	v_and_b32_e32 v201, 0xffff0000, v182
	v_lshlrev_b32_e32 v202, 16, v183
	v_and_b32_e32 v203, 0xffff0000, v183
	v_mul_f32_e32 v200, 0xbfb8aa3b, v200
	v_mul_f32_e32 v201, 0xbfb8aa3b, v201
	v_mul_f32_e32 v202, 0xbfb8aa3b, v202
	v_mul_f32_e32 v203, 0xbfb8aa3b, v203
	v_exp_f32_e32 v200, v200
	v_exp_f32_e32 v201, v201
	v_exp_f32_e32 v202, v202
	v_exp_f32_e32 v203, v203
	v_pk_add_f32 v[200:201], v[200:201], 1.0 op_sel_hi:[1,0]
	v_pk_add_f32 v[202:203], v[202:203], 1.0 op_sel_hi:[1,0]
	v_rcp_f32_e32 v200, v200
	v_rcp_f32_e32 v201, v201
	v_rcp_f32_e32 v202, v202
	v_rcp_f32_e32 v203, v203
	v_pk_mul_f32 v[200:201], v[108:109], v[200:201]
	v_pk_mul_f32 v[202:203], v[110:111], v[202:203]
	v_cvt_pk_bf16_f32 v182, v200, v201
	v_cvt_pk_bf16_f32 v183, v202, v203
	global_store_dwordx4 v[210:211], v[180:183], off
	s_waitcnt vmcnt(7)
; DI unsigned pk2(float a, float b) { f32x2 v = {a, b}; bf16x2_t r = __builtin_convertvector(v, bf16x2_t); return __builtin_bit_cast(unsigned, r); }
; DI float sigmoidf_(float x) { return 1.f / (1.f + __expf(-x)); }
;     DI void operator()(const f32x4 (&acc)[2][2][4][2], const Unit& u, int wr, int wc, int fr, int fq) const {
;         const int row0 = u.pm * BM + wr * 64 + fr, col0 = u.pn * BM + wc * 32 + 8 * fq;
; #pragma unroll
;         for (int ai = 0; ai < 2; ++ai)
; #pragma unroll
;             for (int m = 0; m < 4; ++m) { const size_t row = (size_t)(row0 + ai * HALF + m * 16);
;                 u32x4 gzs[2], ts[2];
; #pragma unroll
;                 for (int bj = 0; bj < 2; ++bj) { const int col = col0 + bj * HALF; gzs[bj] = *(const u32x4*)(Zg + row * NZ + goff + col); if (add) ts[bj] = *(const u32x4*)(add + row * D + col); else ts[bj] = (u32x4){0u, 0u, 0u, 0u}; }
; #pragma unroll
;                 for (int bj = 0; bj < 2; ++bj) {
;                     const int col = col0 + bj * HALF;
;                     const u32x4 gz = gzs[bj];
;                     float a[8] = {0.f, 0.f, 0.f, 0.f, 0.f, 0.f, 0.f, 0.f};
;                     if (add) { const u32x4 t = ts[bj]; a[0] = bflo(t.x); a[1] = bfhi(t.x); a[2] = bflo(t.y); a[3] = bfhi(t.y); a[4] = bflo(t.z); a[5] = bfhi(t.z); a[6] = bflo(t.w); a[7] = bfhi(t.w); }
;                     const f32x4 v0 = acc[ai][bj][m][0], v1 = acc[ai][bj][m][1];
;                     float o[8];
;                     o[0] = a[0] + sigmoidf_(bflo(gz.x)) * v0[0]; o[1] = a[1] + sigmoidf_(bfhi(gz.x)) * v0[1];
;                     o[2] = a[2] + sigmoidf_(bflo(gz.y)) * v0[2]; o[3] = a[3] + sigmoidf_(bfhi(gz.y)) * v0[3];
;                     o[4] = a[4] + sigmoidf_(bflo(gz.z)) * v1[0]; o[5] = a[5] + sigmoidf_(bfhi(gz.z)) * v1[1];
;                     o[6] = a[6] + sigmoidf_(bflo(gz.w)) * v1[2]; o[7] = a[7] + sigmoidf_(bfhi(gz.w)) * v1[3];
;                     u32x4 w; w.x = pk2(o[0], o[1]); w.y = pk2(o[2], o[3]); w.z = pk2(o[4], o[5]); w.w = pk2(o[6], o[7]);
;                     *(u32x4*)(O + row * D + col) = w; } }
	v_lshlrev_b32_e32 v200, 16, v184
	v_and_b32_e32 v201, 0xffff0000, v184
	v_lshlrev_b32_e32 v202, 16, v185
	v_and_b32_e32 v203, 0xffff0000, v185
	v_mul_f32_e32 v200, 0xbfb8aa3b, v200
	v_mul_f32_e32 v201, 0xbfb8aa3b, v201
	v_mul_f32_e32 v202, 0xbfb8aa3b, v202
	v_mul_f32_e32 v203, 0xbfb8aa3b, v203
	v_exp_f32_e32 v200, v200
	v_exp_f32_e32 v201, v201
	v_exp_f32_e32 v202, v202
	v_exp_f32_e32 v203, v203
	v_pk_add_f32 v[200:201], v[200:201], 1.0 op_sel_hi:[1,0]
	v_pk_add_f32 v[202:203], v[202:203], 1.0 op_sel_hi:[1,0]
	v_rcp_f32_e32 v200, v200
	v_rcp_f32_e32 v201, v201
	v_rcp_f32_e32 v202, v202
	v_rcp_f32_e32 v203, v203
	v_pk_mul_f32 v[200:201], v[104:105], v[200:201]
	v_pk_mul_f32 v[202:203], v[106:107], v[202:203]
	v_cvt_pk_bf16_f32 v184, v200, v201
	v_cvt_pk_bf16_f32 v185, v202, v203
	v_lshlrev_b32_e32 v200, 16, v186
	v_and_b32_e32 v201, 0xffff0000, v186
	v_lshlrev_b32_e32 v202, 16, v187
	v_and_b32_e32 v203, 0xffff0000, v187
	v_mul_f32_e32 v200, 0xbfb8aa3b, v200
	v_mul_f32_e32 v201, 0xbfb8aa3b, v201
	v_mul_f32_e32 v202, 0xbfb8aa3b, v202
	v_mul_f32_e32 v203, 0xbfb8aa3b, v203
	v_exp_f32_e32 v200, v200
	v_exp_f32_e32 v201, v201
	v_exp_f32_e32 v202, v202
	v_exp_f32_e32 v203, v203
	v_pk_add_f32 v[200:201], v[200:201], 1.0 op_sel_hi:[1,0]
	v_pk_add_f32 v[202:203], v[202:203], 1.0 op_sel_hi:[1,0]
	v_rcp_f32_e32 v200, v200
	v_rcp_f32_e32 v201, v201
	v_rcp_f32_e32 v202, v202
	v_rcp_f32_e32 v203, v203
	v_pk_mul_f32 v[200:201], v[100:101], v[200:201]
	v_pk_mul_f32 v[202:203], v[102:103], v[202:203]
	v_cvt_pk_bf16_f32 v186, v200, v201
	v_cvt_pk_bf16_f32 v187, v202, v203
	global_store_dwordx4 v[210:211], v[184:187], off offset:256
	v_add_u32_e32 v215, 128, v214
	v_mad_i64_i32 v[206:207], s[24:25], v215, s15, v[204:205]
	global_load_dwordx4 v[180:183], v[206:207], off offset:3072
	global_load_dwordx4 v[184:187], v[206:207], off offset:3328
	v_add_u32_e32 v215, 32, v214
	v_lshlrev_b32_e32 v212, 12, v215
	v_lshl_add_u64 v[210:211], v[208:209], 0, v[212:213]
	s_waitcnt vmcnt(9)
	v_lshlrev_b32_e32 v200, 16, v188
	v_and_b32_e32 v201, 0xffff0000, v188
	v_lshlrev_b32_e32 v202, 16, v189
	v_and_b32_e32 v203, 0xffff0000, v189
	v_mul_f32_e32 v200, 0xbfb8aa3b, v200
	v_mul_f32_e32 v201, 0xbfb8aa3b, v201
	v_mul_f32_e32 v202, 0xbfb8aa3b, v202
	v_mul_f32_e32 v203, 0xbfb8aa3b, v203
	v_exp_f32_e32 v200, v200
	v_exp_f32_e32 v201, v201
	v_exp_f32_e32 v202, v202
	v_exp_f32_e32 v203, v203
	v_pk_add_f32 v[200:201], v[200:201], 1.0 op_sel_hi:[1,0]
	v_pk_add_f32 v[202:203], v[202:203], 1.0 op_sel_hi:[1,0]
	v_rcp_f32_e32 v200, v200
	v_rcp_f32_e32 v201, v201
	v_rcp_f32_e32 v202, v202
	v_rcp_f32_e32 v203, v203
	v_pk_mul_f32 v[200:201], v[96:97], v[200:201]
	v_pk_mul_f32 v[202:203], v[98:99], v[202:203]
	v_cvt_pk_bf16_f32 v188, v200, v201
	v_cvt_pk_bf16_f32 v189, v202, v203
	v_lshlrev_b32_e32 v200, 16, v190
	v_and_b32_e32 v201, 0xffff0000, v190
	v_lshlrev_b32_e32 v202, 16, v191
	v_and_b32_e32 v203, 0xffff0000, v191
	v_mul_f32_e32 v200, 0xbfb8aa3b, v200
	v_mul_f32_e32 v201, 0xbfb8aa3b, v201
	v_mul_f32_e32 v202, 0xbfb8aa3b, v202
	v_mul_f32_e32 v203, 0xbfb8aa3b, v203
	v_exp_f32_e32 v200, v200
	v_exp_f32_e32 v201, v201
	v_exp_f32_e32 v202, v202
	v_exp_f32_e32 v203, v203
	v_pk_add_f32 v[200:201], v[200:201], 1.0 op_sel_hi:[1,0]
	v_pk_add_f32 v[202:203], v[202:203], 1.0 op_sel_hi:[1,0]
	v_rcp_f32_e32 v200, v200
	v_rcp_f32_e32 v201, v201
	v_rcp_f32_e32 v202, v202
	v_rcp_f32_e32 v203, v203
	v_pk_mul_f32 v[200:201], v[92:93], v[200:201]
	v_pk_mul_f32 v[202:203], v[94:95], v[202:203]
	v_cvt_pk_bf16_f32 v190, v200, v201
	v_cvt_pk_bf16_f32 v191, v202, v203
	global_store_dwordx4 v[210:211], v[188:191], off
	s_waitcnt vmcnt(9)
	v_lshlrev_b32_e32 v200, 16, v192
	v_and_b32_e32 v201, 0xffff0000, v192
	v_lshlrev_b32_e32 v202, 16, v193
	v_and_b32_e32 v203, 0xffff0000, v193
	v_mul_f32_e32 v200, 0xbfb8aa3b, v200
	v_mul_f32_e32 v201, 0xbfb8aa3b, v201
	v_mul_f32_e32 v202, 0xbfb8aa3b, v202
	v_mul_f32_e32 v203, 0xbfb8aa3b, v203
	v_exp_f32_e32 v200, v200
	v_exp_f32_e32 v201, v201
	v_exp_f32_e32 v202, v202
	v_exp_f32_e32 v203, v203
	v_pk_add_f32 v[200:201], v[200:201], 1.0 op_sel_hi:[1,0]
	v_pk_add_f32 v[202:203], v[202:203], 1.0 op_sel_hi:[1,0]
	v_rcp_f32_e32 v200, v200
	v_rcp_f32_e32 v201, v201
	v_rcp_f32_e32 v202, v202
	v_rcp_f32_e32 v203, v203
	v_pk_mul_f32 v[200:201], v[86:87], v[200:201]
	v_pk_mul_f32 v[202:203], v[88:89], v[202:203]
	v_cvt_pk_bf16_f32 v192, v200, v201
	v_cvt_pk_bf16_f32 v193, v202, v203
	v_lshlrev_b32_e32 v200, 16, v194
	v_and_b32_e32 v201, 0xffff0000, v194
	v_lshlrev_b32_e32 v202, 16, v195
	v_and_b32_e32 v203, 0xffff0000, v195
	v_mul_f32_e32 v200, 0xbfb8aa3b, v200
	v_mul_f32_e32 v201, 0xbfb8aa3b, v201
	v_mul_f32_e32 v202, 0xbfb8aa3b, v202
	v_mul_f32_e32 v203, 0xbfb8aa3b, v203
	v_exp_f32_e32 v200, v200
	v_exp_f32_e32 v201, v201
	v_exp_f32_e32 v202, v202
	v_exp_f32_e32 v203, v203
	v_pk_add_f32 v[200:201], v[200:201], 1.0 op_sel_hi:[1,0]
	v_pk_add_f32 v[202:203], v[202:203], 1.0 op_sel_hi:[1,0]
	v_rcp_f32_e32 v200, v200
	v_rcp_f32_e32 v201, v201
	v_rcp_f32_e32 v202, v202
	v_rcp_f32_e32 v203, v203
	v_pk_mul_f32 v[200:201], v[82:83], v[200:201]
	v_pk_mul_f32 v[202:203], v[84:85], v[202:203]
	v_cvt_pk_bf16_f32 v194, v200, v201
	v_cvt_pk_bf16_f32 v195, v202, v203
	global_store_dwordx4 v[210:211], v[192:195], off offset:256
	v_add_u32_e32 v215, 144, v214
	v_mad_i64_i32 v[206:207], s[24:25], v215, s15, v[204:205]
	global_load_dwordx4 v[188:191], v[206:207], off offset:3072
	global_load_dwordx4 v[192:195], v[206:207], off offset:3328
	v_add_u32_e32 v215, 48, v214
	v_lshlrev_b32_e32 v212, 12, v215
	v_lshl_add_u64 v[210:211], v[208:209], 0, v[212:213]
	s_waitcnt vmcnt(9)
; DI unsigned pk2(float a, float b) { f32x2 v = {a, b}; bf16x2_t r = __builtin_convertvector(v, bf16x2_t); return __builtin_bit_cast(unsigned, r); }
; DI float sigmoidf_(float x) { return 1.f / (1.f + __expf(-x)); }
;     DI void operator()(const f32x4 (&acc)[2][2][4][2], const Unit& u, int wr, int wc, int fr, int fq) const {
;         const int row0 = u.pm * BM + wr * 64 + fr, col0 = u.pn * BM + wc * 32 + 8 * fq;
; #pragma unroll
;         for (int ai = 0; ai < 2; ++ai)
; #pragma unroll
;             for (int m = 0; m < 4; ++m) { const size_t row = (size_t)(row0 + ai * HALF + m * 16);
;                 u32x4 gzs[2], ts[2];
; #pragma unroll
;                 for (int bj = 0; bj < 2; ++bj) { const int col = col0 + bj * HALF; gzs[bj] = *(const u32x4*)(Zg + row * NZ + goff + col); if (add) ts[bj] = *(const u32x4*)(add + row * D + col); else ts[bj] = (u32x4){0u, 0u, 0u, 0u}; }
; #pragma unroll
;                 for (int bj = 0; bj < 2; ++bj) {
;                     const int col = col0 + bj * HALF;
;                     const u32x4 gz = gzs[bj];
;                     float a[8] = {0.f, 0.f, 0.f, 0.f, 0.f, 0.f, 0.f, 0.f};
;                     if (add) { const u32x4 t = ts[bj]; a[0] = bflo(t.x); a[1] = bfhi(t.x); a[2] = bflo(t.y); a[3] = bfhi(t.y); a[4] = bflo(t.z); a[5] = bfhi(t.z); a[6] = bflo(t.w); a[7] = bfhi(t.w); }
;                     const f32x4 v0 = acc[ai][bj][m][0], v1 = acc[ai][bj][m][1];
;                     float o[8];
;                     o[0] = a[0] + sigmoidf_(bflo(gz.x)) * v0[0]; o[1] = a[1] + sigmoidf_(bfhi(gz.x)) * v0[1];
;                     o[2] = a[2] + sigmoidf_(bflo(gz.y)) * v0[2]; o[3] = a[3] + sigmoidf_(bfhi(gz.y)) * v0[3];
;                     o[4] = a[4] + sigmoidf_(bflo(gz.z)) * v1[0]; o[5] = a[5] + sigmoidf_(bfhi(gz.z)) * v1[1];
;                     o[6] = a[6] + sigmoidf_(bflo(gz.w)) * v1[2]; o[7] = a[7] + sigmoidf_(bfhi(gz.w)) * v1[3];
;                     u32x4 w; w.x = pk2(o[0], o[1]); w.y = pk2(o[2], o[3]); w.z = pk2(o[4], o[5]); w.w = pk2(o[6], o[7]);
;                     *(u32x4*)(O + row * D + col) = w; } }
	v_lshlrev_b32_e32 v200, 16, v172
	v_and_b32_e32 v201, 0xffff0000, v172
	v_lshlrev_b32_e32 v202, 16, v173
	v_and_b32_e32 v203, 0xffff0000, v173
	v_mul_f32_e32 v200, 0xbfb8aa3b, v200
	v_mul_f32_e32 v201, 0xbfb8aa3b, v201
	v_mul_f32_e32 v202, 0xbfb8aa3b, v202
	v_mul_f32_e32 v203, 0xbfb8aa3b, v203
	v_exp_f32_e32 v200, v200
	v_exp_f32_e32 v201, v201
	v_exp_f32_e32 v202, v202
	v_exp_f32_e32 v203, v203
	v_pk_add_f32 v[200:201], v[200:201], 1.0 op_sel_hi:[1,0]
	v_pk_add_f32 v[202:203], v[202:203], 1.0 op_sel_hi:[1,0]
	v_rcp_f32_e32 v200, v200
	v_rcp_f32_e32 v201, v201
	v_rcp_f32_e32 v202, v202
	v_rcp_f32_e32 v203, v203
	v_pk_mul_f32 v[200:201], v[78:79], v[200:201]
	v_pk_mul_f32 v[202:203], v[80:81], v[202:203]
	v_cvt_pk_bf16_f32 v172, v200, v201
	v_cvt_pk_bf16_f32 v173, v202, v203
	v_lshlrev_b32_e32 v200, 16, v174
	v_and_b32_e32 v201, 0xffff0000, v174
	v_lshlrev_b32_e32 v202, 16, v175
	v_and_b32_e32 v203, 0xffff0000, v175
	v_mul_f32_e32 v200, 0xbfb8aa3b, v200
	v_mul_f32_e32 v201, 0xbfb8aa3b, v201
	v_mul_f32_e32 v202, 0xbfb8aa3b, v202
	v_mul_f32_e32 v203, 0xbfb8aa3b, v203
	v_exp_f32_e32 v200, v200
	v_exp_f32_e32 v201, v201
	v_exp_f32_e32 v202, v202
	v_exp_f32_e32 v203, v203
	v_pk_add_f32 v[200:201], v[200:201], 1.0 op_sel_hi:[1,0]
	v_pk_add_f32 v[202:203], v[202:203], 1.0 op_sel_hi:[1,0]
	v_rcp_f32_e32 v200, v200
	v_rcp_f32_e32 v201, v201
	v_rcp_f32_e32 v202, v202
	v_rcp_f32_e32 v203, v203
	v_pk_mul_f32 v[200:201], v[74:75], v[200:201]
	v_pk_mul_f32 v[202:203], v[76:77], v[202:203]
	v_cvt_pk_bf16_f32 v174, v200, v201
	v_cvt_pk_bf16_f32 v175, v202, v203
	global_store_dwordx4 v[210:211], v[172:175], off
	s_waitcnt vmcnt(9)
	v_lshlrev_b32_e32 v200, 16, v176
	v_and_b32_e32 v201, 0xffff0000, v176
	v_lshlrev_b32_e32 v202, 16, v177
	v_and_b32_e32 v203, 0xffff0000, v177
	v_mul_f32_e32 v200, 0xbfb8aa3b, v200
	v_mul_f32_e32 v201, 0xbfb8aa3b, v201
	v_mul_f32_e32 v202, 0xbfb8aa3b, v202
	v_mul_f32_e32 v203, 0xbfb8aa3b, v203
	v_exp_f32_e32 v200, v200
	v_exp_f32_e32 v201, v201
	v_exp_f32_e32 v202, v202
	v_exp_f32_e32 v203, v203
	v_pk_add_f32 v[200:201], v[200:201], 1.0 op_sel_hi:[1,0]
	v_pk_add_f32 v[202:203], v[202:203], 1.0 op_sel_hi:[1,0]
	v_rcp_f32_e32 v200, v200
	v_rcp_f32_e32 v201, v201
	v_rcp_f32_e32 v202, v202
	v_rcp_f32_e32 v203, v203
	v_pk_mul_f32 v[200:201], v[70:71], v[200:201]
	v_pk_mul_f32 v[202:203], v[72:73], v[202:203]
	v_cvt_pk_bf16_f32 v176, v200, v201
	v_cvt_pk_bf16_f32 v177, v202, v203
	v_lshlrev_b32_e32 v200, 16, v178
	v_and_b32_e32 v201, 0xffff0000, v178
	v_lshlrev_b32_e32 v202, 16, v179
	v_and_b32_e32 v203, 0xffff0000, v179
	v_mul_f32_e32 v200, 0xbfb8aa3b, v200
	v_mul_f32_e32 v201, 0xbfb8aa3b, v201
	v_mul_f32_e32 v202, 0xbfb8aa3b, v202
	v_mul_f32_e32 v203, 0xbfb8aa3b, v203
	v_exp_f32_e32 v200, v200
	v_exp_f32_e32 v201, v201
	v_exp_f32_e32 v202, v202
	v_exp_f32_e32 v203, v203
	v_pk_add_f32 v[200:201], v[200:201], 1.0 op_sel_hi:[1,0]
	v_pk_add_f32 v[202:203], v[202:203], 1.0 op_sel_hi:[1,0]
	v_rcp_f32_e32 v200, v200
	v_rcp_f32_e32 v201, v201
	v_rcp_f32_e32 v202, v202
	v_rcp_f32_e32 v203, v203
	v_pk_mul_f32 v[200:201], v[66:67], v[200:201]
	v_pk_mul_f32 v[202:203], v[68:69], v[202:203]
	v_cvt_pk_bf16_f32 v178, v200, v201
	v_cvt_pk_bf16_f32 v179, v202, v203
	global_store_dwordx4 v[210:211], v[176:179], off offset:256
	v_add_u32_e32 v215, 160, v214
	v_mad_i64_i32 v[206:207], s[24:25], v215, s15, v[204:205]
	global_load_dwordx4 v[172:175], v[206:207], off offset:3072
	global_load_dwordx4 v[176:179], v[206:207], off offset:3328
	v_add_u32_e32 v215, 128, v214
	v_lshlrev_b32_e32 v212, 12, v215
	v_lshl_add_u64 v[210:211], v[208:209], 0, v[212:213]
	s_waitcnt vmcnt(9)
	v_lshlrev_b32_e32 v200, 16, v180
	v_and_b32_e32 v201, 0xffff0000, v180
	v_lshlrev_b32_e32 v202, 16, v181
	v_and_b32_e32 v203, 0xffff0000, v181
	v_mul_f32_e32 v200, 0xbfb8aa3b, v200
	v_mul_f32_e32 v201, 0xbfb8aa3b, v201
	v_mul_f32_e32 v202, 0xbfb8aa3b, v202
	v_mul_f32_e32 v203, 0xbfb8aa3b, v203
	v_exp_f32_e32 v200, v200
	v_exp_f32_e32 v201, v201
	v_exp_f32_e32 v202, v202
	v_exp_f32_e32 v203, v203
	v_pk_add_f32 v[200:201], v[200:201], 1.0 op_sel_hi:[1,0]
	v_pk_add_f32 v[202:203], v[202:203], 1.0 op_sel_hi:[1,0]
	v_rcp_f32_e32 v200, v200
	v_rcp_f32_e32 v201, v201
	v_rcp_f32_e32 v202, v202
	v_rcp_f32_e32 v203, v203
	v_pk_mul_f32 v[200:201], v[62:63], v[200:201]
	v_pk_mul_f32 v[202:203], v[64:65], v[202:203]
	v_cvt_pk_bf16_f32 v180, v200, v201
	v_cvt_pk_bf16_f32 v181, v202, v203
	v_lshlrev_b32_e32 v200, 16, v182
	v_and_b32_e32 v201, 0xffff0000, v182
	v_lshlrev_b32_e32 v202, 16, v183
	v_and_b32_e32 v203, 0xffff0000, v183
	v_mul_f32_e32 v200, 0xbfb8aa3b, v200
	v_mul_f32_e32 v201, 0xbfb8aa3b, v201
	v_mul_f32_e32 v202, 0xbfb8aa3b, v202
	v_mul_f32_e32 v203, 0xbfb8aa3b, v203
	v_exp_f32_e32 v200, v200
	v_exp_f32_e32 v201, v201
	v_exp_f32_e32 v202, v202
	v_exp_f32_e32 v203, v203
	v_pk_add_f32 v[200:201], v[200:201], 1.0 op_sel_hi:[1,0]
	v_pk_add_f32 v[202:203], v[202:203], 1.0 op_sel_hi:[1,0]
	v_rcp_f32_e32 v200, v200
	v_rcp_f32_e32 v201, v201
	v_rcp_f32_e32 v202, v202
	v_rcp_f32_e32 v203, v203
	v_pk_mul_f32 v[200:201], v[58:59], v[200:201]
	v_pk_mul_f32 v[202:203], v[60:61], v[202:203]
	v_cvt_pk_bf16_f32 v182, v200, v201
	v_cvt_pk_bf16_f32 v183, v202, v203
	global_store_dwordx4 v[210:211], v[180:183], off
	s_waitcnt vmcnt(9)
; DI unsigned pk2(float a, float b) { f32x2 v = {a, b}; bf16x2_t r = __builtin_convertvector(v, bf16x2_t); return __builtin_bit_cast(unsigned, r); }
; DI float sigmoidf_(float x) { return 1.f / (1.f + __expf(-x)); }
;     DI void operator()(const f32x4 (&acc)[2][2][4][2], const Unit& u, int wr, int wc, int fr, int fq) const {
;         const int row0 = u.pm * BM + wr * 64 + fr, col0 = u.pn * BM + wc * 32 + 8 * fq;
; #pragma unroll
;         for (int ai = 0; ai < 2; ++ai)
; #pragma unroll
;             for (int m = 0; m < 4; ++m) { const size_t row = (size_t)(row0 + ai * HALF + m * 16);
;                 u32x4 gzs[2], ts[2];
; #pragma unroll
;                 for (int bj = 0; bj < 2; ++bj) { const int col = col0 + bj * HALF; gzs[bj] = *(const u32x4*)(Zg + row * NZ + goff + col); if (add) ts[bj] = *(const u32x4*)(add + row * D + col); else ts[bj] = (u32x4){0u, 0u, 0u, 0u}; }
; #pragma unroll
;                 for (int bj = 0; bj < 2; ++bj) {
;                     const int col = col0 + bj * HALF;
;                     const u32x4 gz = gzs[bj];
;                     float a[8] = {0.f, 0.f, 0.f, 0.f, 0.f, 0.f, 0.f, 0.f};
;                     if (add) { const u32x4 t = ts[bj]; a[0] = bflo(t.x); a[1] = bfhi(t.x); a[2] = bflo(t.y); a[3] = bfhi(t.y); a[4] = bflo(t.z); a[5] = bfhi(t.z); a[6] = bflo(t.w); a[7] = bfhi(t.w); }
;                     const f32x4 v0 = acc[ai][bj][m][0], v1 = acc[ai][bj][m][1];
;                     float o[8];
;                     o[0] = a[0] + sigmoidf_(bflo(gz.x)) * v0[0]; o[1] = a[1] + sigmoidf_(bfhi(gz.x)) * v0[1];
;                     o[2] = a[2] + sigmoidf_(bflo(gz.y)) * v0[2]; o[3] = a[3] + sigmoidf_(bfhi(gz.y)) * v0[3];
;                     o[4] = a[4] + sigmoidf_(bflo(gz.z)) * v1[0]; o[5] = a[5] + sigmoidf_(bfhi(gz.z)) * v1[1];
;                     o[6] = a[6] + sigmoidf_(bflo(gz.w)) * v1[2]; o[7] = a[7] + sigmoidf_(bfhi(gz.w)) * v1[3];
;                     u32x4 w; w.x = pk2(o[0], o[1]); w.y = pk2(o[2], o[3]); w.z = pk2(o[4], o[5]); w.w = pk2(o[6], o[7]);
;                     *(u32x4*)(O + row * D + col) = w; } }
	v_lshlrev_b32_e32 v200, 16, v184
	v_and_b32_e32 v201, 0xffff0000, v184
	v_lshlrev_b32_e32 v202, 16, v185
	v_and_b32_e32 v203, 0xffff0000, v185
	v_mul_f32_e32 v200, 0xbfb8aa3b, v200
	v_mul_f32_e32 v201, 0xbfb8aa3b, v201
	v_mul_f32_e32 v202, 0xbfb8aa3b, v202
	v_mul_f32_e32 v203, 0xbfb8aa3b, v203
	v_exp_f32_e32 v200, v200
	v_exp_f32_e32 v201, v201
	v_exp_f32_e32 v202, v202
	v_exp_f32_e32 v203, v203
	v_pk_add_f32 v[200:201], v[200:201], 1.0 op_sel_hi:[1,0]
	v_pk_add_f32 v[202:203], v[202:203], 1.0 op_sel_hi:[1,0]
	v_rcp_f32_e32 v200, v200
	v_rcp_f32_e32 v201, v201
	v_rcp_f32_e32 v202, v202
	v_rcp_f32_e32 v203, v203
	v_pk_mul_f32 v[200:201], v[54:55], v[200:201]
	v_pk_mul_f32 v[202:203], v[56:57], v[202:203]
	v_cvt_pk_bf16_f32 v184, v200, v201
	v_cvt_pk_bf16_f32 v185, v202, v203
	v_lshlrev_b32_e32 v200, 16, v186
	v_and_b32_e32 v201, 0xffff0000, v186
	v_lshlrev_b32_e32 v202, 16, v187
	v_and_b32_e32 v203, 0xffff0000, v187
	v_mul_f32_e32 v200, 0xbfb8aa3b, v200
	v_mul_f32_e32 v201, 0xbfb8aa3b, v201
	v_mul_f32_e32 v202, 0xbfb8aa3b, v202
	v_mul_f32_e32 v203, 0xbfb8aa3b, v203
	v_exp_f32_e32 v200, v200
	v_exp_f32_e32 v201, v201
	v_exp_f32_e32 v202, v202
	v_exp_f32_e32 v203, v203
	v_pk_add_f32 v[200:201], v[200:201], 1.0 op_sel_hi:[1,0]
	v_pk_add_f32 v[202:203], v[202:203], 1.0 op_sel_hi:[1,0]
	v_rcp_f32_e32 v200, v200
	v_rcp_f32_e32 v201, v201
	v_rcp_f32_e32 v202, v202
	v_rcp_f32_e32 v203, v203
	v_pk_mul_f32 v[200:201], v[50:51], v[200:201]
	v_pk_mul_f32 v[202:203], v[52:53], v[202:203]
	v_cvt_pk_bf16_f32 v186, v200, v201
	v_cvt_pk_bf16_f32 v187, v202, v203
	global_store_dwordx4 v[210:211], v[184:187], off offset:256
	v_add_u32_e32 v215, 176, v214
	v_mad_i64_i32 v[206:207], s[24:25], v215, s15, v[204:205]
	global_load_dwordx4 v[180:183], v[206:207], off offset:3072
	global_load_dwordx4 v[184:187], v[206:207], off offset:3328
	v_add_u32_e32 v215, 144, v214
	v_lshlrev_b32_e32 v212, 12, v215
	v_lshl_add_u64 v[210:211], v[208:209], 0, v[212:213]
	s_waitcnt vmcnt(9)
	v_lshlrev_b32_e32 v200, 16, v188
	v_and_b32_e32 v201, 0xffff0000, v188
	v_lshlrev_b32_e32 v202, 16, v189
	v_and_b32_e32 v203, 0xffff0000, v189
	v_mul_f32_e32 v200, 0xbfb8aa3b, v200
	v_mul_f32_e32 v201, 0xbfb8aa3b, v201
	v_mul_f32_e32 v202, 0xbfb8aa3b, v202
	v_mul_f32_e32 v203, 0xbfb8aa3b, v203
	v_exp_f32_e32 v200, v200
	v_exp_f32_e32 v201, v201
	v_exp_f32_e32 v202, v202
	v_exp_f32_e32 v203, v203
	v_pk_add_f32 v[200:201], v[200:201], 1.0 op_sel_hi:[1,0]
	v_pk_add_f32 v[202:203], v[202:203], 1.0 op_sel_hi:[1,0]
	v_rcp_f32_e32 v200, v200
	v_rcp_f32_e32 v201, v201
	v_rcp_f32_e32 v202, v202
	v_rcp_f32_e32 v203, v203
	v_pk_mul_f32 v[200:201], v[46:47], v[200:201]
	v_pk_mul_f32 v[202:203], v[48:49], v[202:203]
	v_cvt_pk_bf16_f32 v188, v200, v201
	v_cvt_pk_bf16_f32 v189, v202, v203
	v_lshlrev_b32_e32 v200, 16, v190
	v_and_b32_e32 v201, 0xffff0000, v190
	v_lshlrev_b32_e32 v202, 16, v191
	v_and_b32_e32 v203, 0xffff0000, v191
	v_mul_f32_e32 v200, 0xbfb8aa3b, v200
	v_mul_f32_e32 v201, 0xbfb8aa3b, v201
	v_mul_f32_e32 v202, 0xbfb8aa3b, v202
	v_mul_f32_e32 v203, 0xbfb8aa3b, v203
	v_exp_f32_e32 v200, v200
	v_exp_f32_e32 v201, v201
	v_exp_f32_e32 v202, v202
	v_exp_f32_e32 v203, v203
	v_pk_add_f32 v[200:201], v[200:201], 1.0 op_sel_hi:[1,0]
	v_pk_add_f32 v[202:203], v[202:203], 1.0 op_sel_hi:[1,0]
	v_rcp_f32_e32 v200, v200
	v_rcp_f32_e32 v201, v201
	v_rcp_f32_e32 v202, v202
	v_rcp_f32_e32 v203, v203
	v_pk_mul_f32 v[200:201], v[42:43], v[200:201]
	v_pk_mul_f32 v[202:203], v[44:45], v[202:203]
	v_cvt_pk_bf16_f32 v190, v200, v201
	v_cvt_pk_bf16_f32 v191, v202, v203
	global_store_dwordx4 v[210:211], v[188:191], off
	s_waitcnt vmcnt(9)
	v_lshlrev_b32_e32 v200, 16, v192
	v_and_b32_e32 v201, 0xffff0000, v192
	v_lshlrev_b32_e32 v202, 16, v193
	v_and_b32_e32 v203, 0xffff0000, v193
	v_mul_f32_e32 v200, 0xbfb8aa3b, v200
	v_mul_f32_e32 v201, 0xbfb8aa3b, v201
	v_mul_f32_e32 v202, 0xbfb8aa3b, v202
	v_mul_f32_e32 v203, 0xbfb8aa3b, v203
	v_exp_f32_e32 v200, v200
	v_exp_f32_e32 v201, v201
	v_exp_f32_e32 v202, v202
	v_exp_f32_e32 v203, v203
	v_pk_add_f32 v[200:201], v[200:201], 1.0 op_sel_hi:[1,0]
	v_pk_add_f32 v[202:203], v[202:203], 1.0 op_sel_hi:[1,0]
	v_rcp_f32_e32 v200, v200
	v_rcp_f32_e32 v201, v201
	v_rcp_f32_e32 v202, v202
	v_rcp_f32_e32 v203, v203
	v_pk_mul_f32 v[200:201], v[38:39], v[200:201]
	v_pk_mul_f32 v[202:203], v[40:41], v[202:203]
	v_cvt_pk_bf16_f32 v192, v200, v201
	v_cvt_pk_bf16_f32 v193, v202, v203
	v_lshlrev_b32_e32 v200, 16, v194
	v_and_b32_e32 v201, 0xffff0000, v194
	v_lshlrev_b32_e32 v202, 16, v195
	v_and_b32_e32 v203, 0xffff0000, v195
	v_mul_f32_e32 v200, 0xbfb8aa3b, v200
	v_mul_f32_e32 v201, 0xbfb8aa3b, v201
	v_mul_f32_e32 v202, 0xbfb8aa3b, v202
	v_mul_f32_e32 v203, 0xbfb8aa3b, v203
	v_exp_f32_e32 v200, v200
	v_exp_f32_e32 v201, v201
	v_exp_f32_e32 v202, v202
	v_exp_f32_e32 v203, v203
	v_pk_add_f32 v[200:201], v[200:201], 1.0 op_sel_hi:[1,0]
	v_pk_add_f32 v[202:203], v[202:203], 1.0 op_sel_hi:[1,0]
	v_rcp_f32_e32 v200, v200
	v_rcp_f32_e32 v201, v201
	v_rcp_f32_e32 v202, v202
	v_rcp_f32_e32 v203, v203
	v_pk_mul_f32 v[200:201], v[34:35], v[200:201]
	v_pk_mul_f32 v[202:203], v[36:37], v[202:203]
	v_cvt_pk_bf16_f32 v194, v200, v201
	v_cvt_pk_bf16_f32 v195, v202, v203
	global_store_dwordx4 v[210:211], v[192:195], off offset:256
	v_add_u32_e32 v215, 160, v214
	v_lshlrev_b32_e32 v212, 12, v215
	v_lshl_add_u64 v[210:211], v[208:209], 0, v[212:213]
	s_waitcnt vmcnt(7)
; template <class Epi, class Sched, bool ALIGN_EPI = true, bool SP2 = true>
; __device__ __forceinline__ void gemm_phase(LAS unsigned char* lds, const Dims g, const Sched& S, const Epi& E) {
;     ...
;         if constexpr (ALIGN_EPI) { if (wr == 0) PG8_BAR; }
;         E(acc, cur, wr, wc, fr, fq);
;         if (!has_next) break;
; #pragma unroll
;         for (int a = 0; a < 2; ++a)
; #pragma unroll
;             for (int b = 0; b < 2; ++b)
; #pragma unroll
;                 for (int m = 0; m < 4; ++m)
; #pragma unroll
;                     for (int n = 0; n < 2; ++n) acc[a][b][m][n] = (f32x4){0.f, 0.f, 0.f, 0.f};
;     DI void operator()(const f32x4 (&acc)[2][2][4][2], const Unit& u, int wr, int wc, int fr, int fq) const {
;     ...
; #pragma unroll
;         for (int ai = 0; ai < 2; ++ai)
; #pragma unroll
;             for (int m = 0; m < 4; ++m) { const size_t row = (size_t)(row0 + ai * HALF + m * 16);
;                 u32x4 gzs[2], ts[2];
; #pragma unroll
;                 for (int bj = 0; bj < 2; ++bj) { const int col = col0 + bj * HALF; gzs[bj] = *(const u32x4*)(Zg + row * NZ + goff + col); if (add) ts[bj] = *(const u32x4*)(add + row * D + col); else ts[bj] = (u32x4){0u, 0u, 0u, 0u}; }
; #pragma unroll
;                 for (int bj = 0; bj < 2; ++bj) {
;                     const int col = col0 + bj * HALF;
;                     const u32x4 gz = gzs[bj];
;                     float a[8] = {0.f, 0.f, 0.f, 0.f, 0.f, 0.f, 0.f, 0.f};
;                     if (add) { const u32x4 t = ts[bj]; a[0] = bflo(t.x); a[1] = bfhi(t.x); a[2] = bflo(t.y); a[3] = bfhi(t.y); a[4] = bflo(t.z); a[5] = bfhi(t.z); a[6] = bflo(t.w); a[7] = bfhi(t.w); }
;                     const f32x4 v0 = acc[ai][bj][m][0], v1 = acc[ai][bj][m][1];
;                     float o[8];
;                     o[0] = a[0] + sigmoidf_(bflo(gz.x)) * v0[0]; o[1] = a[1] + sigmoidf_(bfhi(gz.x)) * v0[1];
;                     o[2] = a[2] + sigmoidf_(bflo(gz.y)) * v0[2]; o[3] = a[3] + sigmoidf_(bfhi(gz.y)) * v0[3];
;                     o[4] = a[4] + sigmoidf_(bflo(gz.z)) * v1[0]; o[5] = a[5] + sigmoidf_(bfhi(gz.z)) * v1[1];
;                     o[6] = a[6] + sigmoidf_(bflo(gz.w)) * v1[2]; o[7] = a[7] + sigmoidf_(bfhi(gz.w)) * v1[3];
;                     u32x4 w; w.x = pk2(o[0], o[1]); w.y = pk2(o[2], o[3]); w.z = pk2(o[4], o[5]); w.w = pk2(o[6], o[7]);
;                     *(u32x4*)(O + row * D + col) = w; } }
	v_lshlrev_b32_e32 v200, 16, v172
	v_and_b32_e32 v201, 0xffff0000, v172
	v_lshlrev_b32_e32 v202, 16, v173
	v_and_b32_e32 v203, 0xffff0000, v173
	v_mul_f32_e32 v200, 0xbfb8aa3b, v200
	v_mul_f32_e32 v201, 0xbfb8aa3b, v201
	v_mul_f32_e32 v202, 0xbfb8aa3b, v202
	v_mul_f32_e32 v203, 0xbfb8aa3b, v203
	v_exp_f32_e32 v200, v200
	v_exp_f32_e32 v201, v201
	v_exp_f32_e32 v202, v202
	v_exp_f32_e32 v203, v203
	v_pk_add_f32 v[200:201], v[200:201], 1.0 op_sel_hi:[1,0]
	v_pk_add_f32 v[202:203], v[202:203], 1.0 op_sel_hi:[1,0]
	v_rcp_f32_e32 v200, v200
	v_rcp_f32_e32 v201, v201
	v_rcp_f32_e32 v202, v202
	v_rcp_f32_e32 v203, v203
	v_pk_mul_f32 v[200:201], v[30:31], v[200:201]
	v_pk_mul_f32 v[202:203], v[32:33], v[202:203]
	v_cvt_pk_bf16_f32 v172, v200, v201
	v_cvt_pk_bf16_f32 v173, v202, v203
	v_lshlrev_b32_e32 v200, 16, v174
	v_and_b32_e32 v201, 0xffff0000, v174
	v_lshlrev_b32_e32 v202, 16, v175
	v_and_b32_e32 v203, 0xffff0000, v175
	v_mul_f32_e32 v200, 0xbfb8aa3b, v200
	v_mul_f32_e32 v201, 0xbfb8aa3b, v201
	v_mul_f32_e32 v202, 0xbfb8aa3b, v202
	v_mul_f32_e32 v203, 0xbfb8aa3b, v203
	v_exp_f32_e32 v200, v200
	v_exp_f32_e32 v201, v201
	v_exp_f32_e32 v202, v202
	v_exp_f32_e32 v203, v203
	v_pk_add_f32 v[200:201], v[200:201], 1.0 op_sel_hi:[1,0]
	v_pk_add_f32 v[202:203], v[202:203], 1.0 op_sel_hi:[1,0]
	v_rcp_f32_e32 v200, v200
	v_rcp_f32_e32 v201, v201
	v_rcp_f32_e32 v202, v202
	v_rcp_f32_e32 v203, v203
	v_pk_mul_f32 v[200:201], v[26:27], v[200:201]
	v_pk_mul_f32 v[202:203], v[28:29], v[202:203]
	v_cvt_pk_bf16_f32 v174, v200, v201
	v_cvt_pk_bf16_f32 v175, v202, v203
	global_store_dwordx4 v[210:211], v[172:175], off
	s_waitcnt vmcnt(7)
	v_lshlrev_b32_e32 v200, 16, v176
	v_and_b32_e32 v201, 0xffff0000, v176
	v_lshlrev_b32_e32 v202, 16, v177
	v_and_b32_e32 v203, 0xffff0000, v177
	v_mul_f32_e32 v200, 0xbfb8aa3b, v200
	v_mul_f32_e32 v201, 0xbfb8aa3b, v201
	v_mul_f32_e32 v202, 0xbfb8aa3b, v202
	v_mul_f32_e32 v203, 0xbfb8aa3b, v203
	v_exp_f32_e32 v200, v200
	v_exp_f32_e32 v201, v201
	v_exp_f32_e32 v202, v202
	v_exp_f32_e32 v203, v203
	v_pk_add_f32 v[200:201], v[200:201], 1.0 op_sel_hi:[1,0]
	v_pk_add_f32 v[202:203], v[202:203], 1.0 op_sel_hi:[1,0]
	v_rcp_f32_e32 v200, v200
	v_rcp_f32_e32 v201, v201
	v_rcp_f32_e32 v202, v202
	v_rcp_f32_e32 v203, v203
	v_pk_mul_f32 v[200:201], v[22:23], v[200:201]
	v_pk_mul_f32 v[202:203], v[24:25], v[202:203]
	v_cvt_pk_bf16_f32 v176, v200, v201
	v_cvt_pk_bf16_f32 v177, v202, v203
	v_lshlrev_b32_e32 v200, 16, v178
	v_and_b32_e32 v201, 0xffff0000, v178
	v_lshlrev_b32_e32 v202, 16, v179
	v_and_b32_e32 v203, 0xffff0000, v179
	v_mul_f32_e32 v200, 0xbfb8aa3b, v200
	v_mul_f32_e32 v201, 0xbfb8aa3b, v201
	v_mul_f32_e32 v202, 0xbfb8aa3b, v202
	v_mul_f32_e32 v203, 0xbfb8aa3b, v203
	v_exp_f32_e32 v200, v200
	v_exp_f32_e32 v201, v201
	v_exp_f32_e32 v202, v202
	v_exp_f32_e32 v203, v203
	v_pk_add_f32 v[200:201], v[200:201], 1.0 op_sel_hi:[1,0]
	v_pk_add_f32 v[202:203], v[202:203], 1.0 op_sel_hi:[1,0]
	v_rcp_f32_e32 v200, v200
	v_rcp_f32_e32 v201, v201
	v_rcp_f32_e32 v202, v202
	v_rcp_f32_e32 v203, v203
	v_pk_mul_f32 v[200:201], v[18:19], v[200:201]
	v_pk_mul_f32 v[202:203], v[20:21], v[202:203]
	v_cvt_pk_bf16_f32 v178, v200, v201
	v_cvt_pk_bf16_f32 v179, v202, v203
	global_store_dwordx4 v[210:211], v[176:179], off offset:256
	v_add_u32_e32 v215, 176, v214
	v_lshlrev_b32_e32 v212, 12, v215
	v_lshl_add_u64 v[210:211], v[208:209], 0, v[212:213]
	s_waitcnt vmcnt(5)
	v_lshlrev_b32_e32 v200, 16, v180
	v_and_b32_e32 v201, 0xffff0000, v180
	v_lshlrev_b32_e32 v202, 16, v181
	v_and_b32_e32 v203, 0xffff0000, v181
	v_mul_f32_e32 v200, 0xbfb8aa3b, v200
	v_mul_f32_e32 v201, 0xbfb8aa3b, v201
	v_mul_f32_e32 v202, 0xbfb8aa3b, v202
	v_mul_f32_e32 v203, 0xbfb8aa3b, v203
	v_exp_f32_e32 v200, v200
	v_exp_f32_e32 v201, v201
	v_exp_f32_e32 v202, v202
	v_exp_f32_e32 v203, v203
	v_pk_add_f32 v[200:201], v[200:201], 1.0 op_sel_hi:[1,0]
	v_pk_add_f32 v[202:203], v[202:203], 1.0 op_sel_hi:[1,0]
	v_rcp_f32_e32 v200, v200
	v_rcp_f32_e32 v201, v201
	v_rcp_f32_e32 v202, v202
	v_rcp_f32_e32 v203, v203
	v_pk_mul_f32 v[200:201], v[14:15], v[200:201]
	v_pk_mul_f32 v[202:203], v[16:17], v[202:203]
	v_cvt_pk_bf16_f32 v180, v200, v201
	v_cvt_pk_bf16_f32 v181, v202, v203
	v_lshlrev_b32_e32 v200, 16, v182
	v_and_b32_e32 v201, 0xffff0000, v182
	v_lshlrev_b32_e32 v202, 16, v183
	v_and_b32_e32 v203, 0xffff0000, v183
	v_mul_f32_e32 v200, 0xbfb8aa3b, v200
	v_mul_f32_e32 v201, 0xbfb8aa3b, v201
	v_mul_f32_e32 v202, 0xbfb8aa3b, v202
	v_mul_f32_e32 v203, 0xbfb8aa3b, v203
	v_exp_f32_e32 v200, v200
	v_exp_f32_e32 v201, v201
	v_exp_f32_e32 v202, v202
	v_exp_f32_e32 v203, v203
	v_pk_add_f32 v[200:201], v[200:201], 1.0 op_sel_hi:[1,0]
	v_pk_add_f32 v[202:203], v[202:203], 1.0 op_sel_hi:[1,0]
	v_rcp_f32_e32 v200, v200
	v_rcp_f32_e32 v201, v201
	v_rcp_f32_e32 v202, v202
	v_rcp_f32_e32 v203, v203
	v_pk_mul_f32 v[200:201], v[10:11], v[200:201]
	v_pk_mul_f32 v[202:203], v[12:13], v[202:203]
	v_cvt_pk_bf16_f32 v182, v200, v201
	v_cvt_pk_bf16_f32 v183, v202, v203
	global_store_dwordx4 v[210:211], v[180:183], off
	s_waitcnt vmcnt(5)
	v_lshlrev_b32_e32 v200, 16, v184
	v_and_b32_e32 v201, 0xffff0000, v184
	v_lshlrev_b32_e32 v202, 16, v185
	v_and_b32_e32 v203, 0xffff0000, v185
	v_mul_f32_e32 v200, 0xbfb8aa3b, v200
	v_mul_f32_e32 v201, 0xbfb8aa3b, v201
	v_mul_f32_e32 v202, 0xbfb8aa3b, v202
	v_mul_f32_e32 v203, 0xbfb8aa3b, v203
	v_exp_f32_e32 v200, v200
	v_exp_f32_e32 v201, v201
	v_exp_f32_e32 v202, v202
	v_exp_f32_e32 v203, v203
	v_pk_add_f32 v[200:201], v[200:201], 1.0 op_sel_hi:[1,0]
	v_pk_add_f32 v[202:203], v[202:203], 1.0 op_sel_hi:[1,0]
	v_rcp_f32_e32 v200, v200
	v_rcp_f32_e32 v201, v201
	v_rcp_f32_e32 v202, v202
	v_rcp_f32_e32 v203, v203
	v_pk_mul_f32 v[200:201], v[6:7], v[200:201]
	v_pk_mul_f32 v[202:203], v[8:9], v[202:203]
	v_cvt_pk_bf16_f32 v184, v200, v201
	v_cvt_pk_bf16_f32 v185, v202, v203
	v_lshlrev_b32_e32 v200, 16, v186
	v_and_b32_e32 v201, 0xffff0000, v186
	v_lshlrev_b32_e32 v202, 16, v187
	v_and_b32_e32 v203, 0xffff0000, v187
	v_mul_f32_e32 v200, 0xbfb8aa3b, v200
	v_mul_f32_e32 v201, 0xbfb8aa3b, v201
	v_mul_f32_e32 v202, 0xbfb8aa3b, v202
	v_mul_f32_e32 v203, 0xbfb8aa3b, v203
	v_exp_f32_e32 v200, v200
	v_exp_f32_e32 v201, v201
	v_exp_f32_e32 v202, v202
	v_exp_f32_e32 v203, v203
	v_pk_add_f32 v[200:201], v[200:201], 1.0 op_sel_hi:[1,0]
	v_pk_add_f32 v[202:203], v[202:203], 1.0 op_sel_hi:[1,0]
	v_rcp_f32_e32 v200, v200
	v_rcp_f32_e32 v201, v201
	v_rcp_f32_e32 v202, v202
	v_rcp_f32_e32 v203, v203
	v_pk_mul_f32 v[200:201], v[2:3], v[200:201]
	v_pk_mul_f32 v[202:203], v[4:5], v[202:203]
	v_cvt_pk_bf16_f32 v186, v200, v201
	v_cvt_pk_bf16_f32 v187, v202, v203
	s_mov_b64 s[2:3], -1
	s_andn2_b64 vcc, exec, s[38:39]
	global_store_dwordx4 v[210:211], v[184:187], off offset:256
	s_cbranch_vccnz .LBB0_1394
	s_andn2_b64 vcc, exec, s[46:47]
	s_cbranch_vccnz .LBB0_1393
	s_barrier
	s_branch .LBB0_1393

; DI unsigned pk2(float a, float b) { f32x2 v = {a, b}; bf16x2_t r = __builtin_convertvector(v, bf16x2_t); return __builtin_bit_cast(unsigned, r); }
; DI float sigmoidf_(float x) { return 1.f / (1.f + __expf(-x)); }
;     DI void operator()(const f32x4 (&acc)[2][2][4][2], const Unit& u, int wr, int wc, int fr, int fq) const {
;         const int row0 = u.pm * BM + wr * 64 + fr, col0 = u.pn * BM + wc * 32 + 8 * fq;
; #pragma unroll
;         for (int ai = 0; ai < 2; ++ai)
; #pragma unroll
;             for (int m = 0; m < 4; ++m) { const size_t row = (size_t)(row0 + ai * HALF + m * 16);
;                 u32x4 gzs[2], ts[2];
; #pragma unroll
;                 for (int bj = 0; bj < 2; ++bj) { const int col = col0 + bj * HALF; gzs[bj] = *(const u32x4*)(Zg + row * NZ + goff + col); if (add) ts[bj] = *(const u32x4*)(add + row * D + col); else ts[bj] = (u32x4){0u, 0u, 0u, 0u}; }
; #pragma unroll
;                 for (int bj = 0; bj < 2; ++bj) {
;                     const int col = col0 + bj * HALF;
;                     const u32x4 gz = gzs[bj];
;                     float a[8] = {0.f, 0.f, 0.f, 0.f, 0.f, 0.f, 0.f, 0.f};
;                     if (add) { const u32x4 t = ts[bj]; a[0] = bflo(t.x); a[1] = bfhi(t.x); a[2] = bflo(t.y); a[3] = bfhi(t.y); a[4] = bflo(t.z); a[5] = bfhi(t.z); a[6] = bflo(t.w); a[7] = bfhi(t.w); }
;                     const f32x4 v0 = acc[ai][bj][m][0], v1 = acc[ai][bj][m][1];
;                     float o[8];
;                     o[0] = a[0] + sigmoidf_(bflo(gz.x)) * v0[0]; o[1] = a[1] + sigmoidf_(bfhi(gz.x)) * v0[1];
;                     o[2] = a[2] + sigmoidf_(bflo(gz.y)) * v0[2]; o[3] = a[3] + sigmoidf_(bfhi(gz.y)) * v0[3];
;                     o[4] = a[4] + sigmoidf_(bflo(gz.z)) * v1[0]; o[5] = a[5] + sigmoidf_(bfhi(gz.z)) * v1[1];
;                     o[6] = a[6] + sigmoidf_(bflo(gz.w)) * v1[2]; o[7] = a[7] + sigmoidf_(bfhi(gz.w)) * v1[3];
;                     u32x4 w; w.x = pk2(o[0], o[1]); w.y = pk2(o[2], o[3]); w.z = pk2(o[4], o[5]); w.w = pk2(o[6], o[7]);
;                     *(u32x4*)(O + row * D + col) = w; } }
;     }
.LBB0_1432:
	v_lshl_add_u32 v181, s12, 8, v177
	v_lshl_or_b32 v183, s0, 8, v179
	v_lshlrev_b32_e32 v183, 1, v183
	v_mov_b32_e32 v175, 0
	v_mov_b32_e32 v174, v183
	v_lshl_add_u64 v[162:163], s[8:9], 0, v[174:175]
	v_lshl_add_u64 v[166:167], s[42:43], 0, v[174:175]
	v_add_u32_e32 v174, 0x1c00, v183
	v_lshl_add_u64 v[158:159], s[40:41], 0, v[174:175]
	v_add_u32_e32 v182, 0, v181
	v_mad_i64_i32 v[160:161], s[24:25], v182, s15, v[158:159]
	v_lshlrev_b32_e32 v174, 12, v182
	v_lshl_add_u64 v[172:173], v[166:167], 0, v[174:175]
	global_load_dwordx4 v[236:239], v[160:161], off offset:0
	global_load_dwordx4 v[240:243], v[160:161], off offset:256
	global_load_dwordx4 v[128:131], v[172:173], off
	global_load_dwordx4 v[132:135], v[172:173], off offset:256
	v_add_u32_e32 v182, 16, v181
	v_mad_i64_i32 v[160:161], s[24:25], v182, s15, v[158:159]
	v_lshlrev_b32_e32 v174, 12, v182
	v_lshl_add_u64 v[172:173], v[166:167], 0, v[174:175]
	global_load_dwordx4 v[244:247], v[160:161], off offset:0
	global_load_dwordx4 v[248:251], v[160:161], off offset:256
	global_load_dwordx4 v[140:143], v[172:173], off
	global_load_dwordx4 v[144:147], v[172:173], off offset:256
	v_add_u32_e32 v182, 32, v181
	v_mad_i64_i32 v[160:161], s[24:25], v182, s15, v[158:159]
	v_lshlrev_b32_e32 v174, 12, v182
	v_lshl_add_u64 v[172:173], v[166:167], 0, v[174:175]
	global_load_dwordx4 v[184:187], v[160:161], off offset:0
	global_load_dwordx4 v[188:191], v[160:161], off offset:256
	global_load_dwordx4 v[200:203], v[172:173], off
	global_load_dwordx4 v[204:207], v[172:173], off offset:256
	v_add_u32_e32 v182, 0, v181
	v_lshlrev_b32_e32 v174, 12, v182
	v_lshl_add_u64 v[164:165], v[162:163], 0, v[174:175]
	s_waitcnt vmcnt(9)
	v_lshlrev_b32_e32 v208, 16, v236
	v_and_b32_e32 v209, 0xffff0000, v236
	v_lshlrev_b32_e32 v210, 16, v237
	v_and_b32_e32 v211, 0xffff0000, v237
	v_mul_f32_e32 v208, 0xbfb8aa3b, v208
	v_mul_f32_e32 v209, 0xbfb8aa3b, v209
	v_mul_f32_e32 v210, 0xbfb8aa3b, v210
	v_mul_f32_e32 v211, 0xbfb8aa3b, v211
	v_exp_f32_e32 v208, v208
	v_exp_f32_e32 v209, v209
	v_exp_f32_e32 v210, v210
	v_exp_f32_e32 v211, v211
	v_lshlrev_b32_e32 v212, 16, v128
	v_and_b32_e32 v213, 0xffff0000, v128
	v_pk_add_f32 v[208:209], v[208:209], 1.0 op_sel_hi:[1,0]
	v_pk_add_f32 v[210:211], v[210:211], 1.0 op_sel_hi:[1,0]
	v_lshlrev_b32_e32 v214, 16, v129
	v_and_b32_e32 v215, 0xffff0000, v129
	v_rcp_f32_e32 v208, v208
	v_rcp_f32_e32 v209, v209
	v_rcp_f32_e32 v210, v210
	v_rcp_f32_e32 v211, v211
	v_pk_fma_f32 v[208:209], v[136:137], v[208:209], v[212:213]
	v_pk_fma_f32 v[210:211], v[138:139], v[210:211], v[214:215]
	v_cvt_pk_bf16_f32 v236, v208, v209
	v_cvt_pk_bf16_f32 v237, v210, v211
	v_lshlrev_b32_e32 v208, 16, v238
	v_and_b32_e32 v209, 0xffff0000, v238
	v_lshlrev_b32_e32 v210, 16, v239
	v_and_b32_e32 v211, 0xffff0000, v239
	v_mul_f32_e32 v208, 0xbfb8aa3b, v208
	v_mul_f32_e32 v209, 0xbfb8aa3b, v209
	v_mul_f32_e32 v210, 0xbfb8aa3b, v210
	v_mul_f32_e32 v211, 0xbfb8aa3b, v211
	v_exp_f32_e32 v208, v208
	v_exp_f32_e32 v209, v209
	v_exp_f32_e32 v210, v210
	v_exp_f32_e32 v211, v211
	v_lshlrev_b32_e32 v212, 16, v130
	v_and_b32_e32 v213, 0xffff0000, v130
	v_pk_add_f32 v[208:209], v[208:209], 1.0 op_sel_hi:[1,0]
	v_pk_add_f32 v[210:211], v[210:211], 1.0 op_sel_hi:[1,0]
	v_lshlrev_b32_e32 v214, 16, v131
	v_and_b32_e32 v215, 0xffff0000, v131
	v_rcp_f32_e32 v208, v208
	v_rcp_f32_e32 v209, v209
	v_rcp_f32_e32 v210, v210
	v_rcp_f32_e32 v211, v211
	v_pk_fma_f32 v[208:209], v[124:125], v[208:209], v[212:213]
	v_pk_fma_f32 v[210:211], v[126:127], v[210:211], v[214:215]
	v_cvt_pk_bf16_f32 v238, v208, v209
	v_cvt_pk_bf16_f32 v239, v210, v211
	global_store_dwordx4 v[164:165], v[236:239], off
	s_waitcnt vmcnt(9)
	v_lshlrev_b32_e32 v208, 16, v240
	v_and_b32_e32 v209, 0xffff0000, v240
	v_lshlrev_b32_e32 v210, 16, v241
	v_and_b32_e32 v211, 0xffff0000, v241
	v_mul_f32_e32 v208, 0xbfb8aa3b, v208
	v_mul_f32_e32 v209, 0xbfb8aa3b, v209
	v_mul_f32_e32 v210, 0xbfb8aa3b, v210
	v_mul_f32_e32 v211, 0xbfb8aa3b, v211
	v_exp_f32_e32 v208, v208
	v_exp_f32_e32 v209, v209
	v_exp_f32_e32 v210, v210
	v_exp_f32_e32 v211, v211
	v_lshlrev_b32_e32 v212, 16, v132
	v_and_b32_e32 v213, 0xffff0000, v132
	v_pk_add_f32 v[208:209], v[208:209], 1.0 op_sel_hi:[1,0]
	v_pk_add_f32 v[210:211], v[210:211], 1.0 op_sel_hi:[1,0]
	v_lshlrev_b32_e32 v214, 16, v133
	v_and_b32_e32 v215, 0xffff0000, v133
	v_rcp_f32_e32 v208, v208
	v_rcp_f32_e32 v209, v209
	v_rcp_f32_e32 v210, v210
	v_rcp_f32_e32 v211, v211
	v_pk_fma_f32 v[208:209], v[120:121], v[208:209], v[212:213]
	v_pk_fma_f32 v[210:211], v[122:123], v[210:211], v[214:215]
	v_cvt_pk_bf16_f32 v240, v208, v209
	v_cvt_pk_bf16_f32 v241, v210, v211
	v_lshlrev_b32_e32 v208, 16, v242
	v_and_b32_e32 v209, 0xffff0000, v242
	v_lshlrev_b32_e32 v210, 16, v243
	v_and_b32_e32 v211, 0xffff0000, v243
	v_mul_f32_e32 v208, 0xbfb8aa3b, v208
	v_mul_f32_e32 v209, 0xbfb8aa3b, v209
	v_mul_f32_e32 v210, 0xbfb8aa3b, v210
	v_mul_f32_e32 v211, 0xbfb8aa3b, v211
	v_exp_f32_e32 v208, v208
	v_exp_f32_e32 v209, v209
	v_exp_f32_e32 v210, v210
	v_exp_f32_e32 v211, v211
	v_lshlrev_b32_e32 v212, 16, v134
	v_and_b32_e32 v213, 0xffff0000, v134
	v_pk_add_f32 v[208:209], v[208:209], 1.0 op_sel_hi:[1,0]
	v_pk_add_f32 v[210:211], v[210:211], 1.0 op_sel_hi:[1,0]
	v_lshlrev_b32_e32 v214, 16, v135
	v_and_b32_e32 v215, 0xffff0000, v135
	v_rcp_f32_e32 v208, v208
	v_rcp_f32_e32 v209, v209
	v_rcp_f32_e32 v210, v210
	v_rcp_f32_e32 v211, v211
	v_pk_fma_f32 v[208:209], v[116:117], v[208:209], v[212:213]
	v_pk_fma_f32 v[210:211], v[118:119], v[210:211], v[214:215]
	v_cvt_pk_bf16_f32 v242, v208, v209
	v_cvt_pk_bf16_f32 v243, v210, v211
	global_store_dwordx4 v[164:165], v[240:243], off offset:256
	v_add_u32_e32 v182, 48, v181
	v_mad_i64_i32 v[160:161], s[24:25], v182, s15, v[158:159]
	v_lshlrev_b32_e32 v174, 12, v182
	v_lshl_add_u64 v[172:173], v[166:167], 0, v[174:175]
	global_load_dwordx4 v[236:239], v[160:161], off offset:0
	global_load_dwordx4 v[240:243], v[160:161], off offset:256
	global_load_dwordx4 v[128:131], v[172:173], off
	global_load_dwordx4 v[132:135], v[172:173], off offset:256
	v_add_u32_e32 v182, 16, v181
	v_lshlrev_b32_e32 v174, 12, v182
	v_lshl_add_u64 v[164:165], v[162:163], 0, v[174:175]
	s_waitcnt vmcnt(11)
; DI unsigned pk2(float a, float b) { f32x2 v = {a, b}; bf16x2_t r = __builtin_convertvector(v, bf16x2_t); return __builtin_bit_cast(unsigned, r); }
; DI float sigmoidf_(float x) { return 1.f / (1.f + __expf(-x)); }
;     DI void operator()(const f32x4 (&acc)[2][2][4][2], const Unit& u, int wr, int wc, int fr, int fq) const {
;         const int row0 = u.pm * BM + wr * 64 + fr, col0 = u.pn * BM + wc * 32 + 8 * fq;
; #pragma unroll
;         for (int ai = 0; ai < 2; ++ai)
; #pragma unroll
;             for (int m = 0; m < 4; ++m) { const size_t row = (size_t)(row0 + ai * HALF + m * 16);
;                 u32x4 gzs[2], ts[2];
; #pragma unroll
;                 for (int bj = 0; bj < 2; ++bj) { const int col = col0 + bj * HALF; gzs[bj] = *(const u32x4*)(Zg + row * NZ + goff + col); if (add) ts[bj] = *(const u32x4*)(add + row * D + col); else ts[bj] = (u32x4){0u, 0u, 0u, 0u}; }
; #pragma unroll
;                 for (int bj = 0; bj < 2; ++bj) {
;                     const int col = col0 + bj * HALF;
;                     const u32x4 gz = gzs[bj];
;                     float a[8] = {0.f, 0.f, 0.f, 0.f, 0.f, 0.f, 0.f, 0.f};
;                     if (add) { const u32x4 t = ts[bj]; a[0] = bflo(t.x); a[1] = bfhi(t.x); a[2] = bflo(t.y); a[3] = bfhi(t.y); a[4] = bflo(t.z); a[5] = bfhi(t.z); a[6] = bflo(t.w); a[7] = bfhi(t.w); }
;                     const f32x4 v0 = acc[ai][bj][m][0], v1 = acc[ai][bj][m][1];
;                     float o[8];
;                     o[0] = a[0] + sigmoidf_(bflo(gz.x)) * v0[0]; o[1] = a[1] + sigmoidf_(bfhi(gz.x)) * v0[1];
;                     o[2] = a[2] + sigmoidf_(bflo(gz.y)) * v0[2]; o[3] = a[3] + sigmoidf_(bfhi(gz.y)) * v0[3];
;                     o[4] = a[4] + sigmoidf_(bflo(gz.z)) * v1[0]; o[5] = a[5] + sigmoidf_(bfhi(gz.z)) * v1[1];
;                     o[6] = a[6] + sigmoidf_(bflo(gz.w)) * v1[2]; o[7] = a[7] + sigmoidf_(bfhi(gz.w)) * v1[3];
;                     u32x4 w; w.x = pk2(o[0], o[1]); w.y = pk2(o[2], o[3]); w.z = pk2(o[4], o[5]); w.w = pk2(o[6], o[7]);
;                     *(u32x4*)(O + row * D + col) = w; } }
;     }
	v_lshlrev_b32_e32 v208, 16, v244
	v_and_b32_e32 v209, 0xffff0000, v244
	v_lshlrev_b32_e32 v210, 16, v245
	v_and_b32_e32 v211, 0xffff0000, v245
	v_mul_f32_e32 v208, 0xbfb8aa3b, v208
	v_mul_f32_e32 v209, 0xbfb8aa3b, v209
	v_mul_f32_e32 v210, 0xbfb8aa3b, v210
	v_mul_f32_e32 v211, 0xbfb8aa3b, v211
	v_exp_f32_e32 v208, v208
	v_exp_f32_e32 v209, v209
	v_exp_f32_e32 v210, v210
	v_exp_f32_e32 v211, v211
	v_lshlrev_b32_e32 v212, 16, v140
	v_and_b32_e32 v213, 0xffff0000, v140
	v_pk_add_f32 v[208:209], v[208:209], 1.0 op_sel_hi:[1,0]
	v_pk_add_f32 v[210:211], v[210:211], 1.0 op_sel_hi:[1,0]
	v_lshlrev_b32_e32 v214, 16, v141
	v_and_b32_e32 v215, 0xffff0000, v141
	v_rcp_f32_e32 v208, v208
	v_rcp_f32_e32 v209, v209
	v_rcp_f32_e32 v210, v210
	v_rcp_f32_e32 v211, v211
	v_pk_fma_f32 v[208:209], v[112:113], v[208:209], v[212:213]
	v_pk_fma_f32 v[210:211], v[114:115], v[210:211], v[214:215]
	v_cvt_pk_bf16_f32 v244, v208, v209
	v_cvt_pk_bf16_f32 v245, v210, v211
	v_lshlrev_b32_e32 v208, 16, v246
	v_and_b32_e32 v209, 0xffff0000, v246
	v_lshlrev_b32_e32 v210, 16, v247
	v_and_b32_e32 v211, 0xffff0000, v247
	v_mul_f32_e32 v208, 0xbfb8aa3b, v208
	v_mul_f32_e32 v209, 0xbfb8aa3b, v209
	v_mul_f32_e32 v210, 0xbfb8aa3b, v210
	v_mul_f32_e32 v211, 0xbfb8aa3b, v211
	v_exp_f32_e32 v208, v208
	v_exp_f32_e32 v209, v209
	v_exp_f32_e32 v210, v210
	v_exp_f32_e32 v211, v211
	v_lshlrev_b32_e32 v212, 16, v142
	v_and_b32_e32 v213, 0xffff0000, v142
	v_pk_add_f32 v[208:209], v[208:209], 1.0 op_sel_hi:[1,0]
	v_pk_add_f32 v[210:211], v[210:211], 1.0 op_sel_hi:[1,0]
	v_lshlrev_b32_e32 v214, 16, v143
	v_and_b32_e32 v215, 0xffff0000, v143
	v_rcp_f32_e32 v208, v208
	v_rcp_f32_e32 v209, v209
	v_rcp_f32_e32 v210, v210
	v_rcp_f32_e32 v211, v211
	v_pk_fma_f32 v[208:209], v[108:109], v[208:209], v[212:213]
	v_pk_fma_f32 v[210:211], v[110:111], v[210:211], v[214:215]
	v_cvt_pk_bf16_f32 v246, v208, v209
	v_cvt_pk_bf16_f32 v247, v210, v211
	global_store_dwordx4 v[164:165], v[244:247], off
	s_waitcnt vmcnt(11)
	v_lshlrev_b32_e32 v208, 16, v248
	v_and_b32_e32 v209, 0xffff0000, v248
	v_lshlrev_b32_e32 v210, 16, v249
	v_and_b32_e32 v211, 0xffff0000, v249
	v_mul_f32_e32 v208, 0xbfb8aa3b, v208
	v_mul_f32_e32 v209, 0xbfb8aa3b, v209
	v_mul_f32_e32 v210, 0xbfb8aa3b, v210
	v_mul_f32_e32 v211, 0xbfb8aa3b, v211
	v_exp_f32_e32 v208, v208
	v_exp_f32_e32 v209, v209
	v_exp_f32_e32 v210, v210
	v_exp_f32_e32 v211, v211
	v_lshlrev_b32_e32 v212, 16, v144
	v_and_b32_e32 v213, 0xffff0000, v144
	v_pk_add_f32 v[208:209], v[208:209], 1.0 op_sel_hi:[1,0]
	v_pk_add_f32 v[210:211], v[210:211], 1.0 op_sel_hi:[1,0]
	v_lshlrev_b32_e32 v214, 16, v145
	v_and_b32_e32 v215, 0xffff0000, v145
	v_rcp_f32_e32 v208, v208
	v_rcp_f32_e32 v209, v209
	v_rcp_f32_e32 v210, v210
	v_rcp_f32_e32 v211, v211
	v_pk_fma_f32 v[208:209], v[104:105], v[208:209], v[212:213]
	v_pk_fma_f32 v[210:211], v[106:107], v[210:211], v[214:215]
	v_cvt_pk_bf16_f32 v248, v208, v209
	v_cvt_pk_bf16_f32 v249, v210, v211
	v_lshlrev_b32_e32 v208, 16, v250
	v_and_b32_e32 v209, 0xffff0000, v250
	v_lshlrev_b32_e32 v210, 16, v251
	v_and_b32_e32 v211, 0xffff0000, v251
	v_mul_f32_e32 v208, 0xbfb8aa3b, v208
	v_mul_f32_e32 v209, 0xbfb8aa3b, v209
	v_mul_f32_e32 v210, 0xbfb8aa3b, v210
	v_mul_f32_e32 v211, 0xbfb8aa3b, v211
	v_exp_f32_e32 v208, v208
	v_exp_f32_e32 v209, v209
	v_exp_f32_e32 v210, v210
	v_exp_f32_e32 v211, v211
	v_lshlrev_b32_e32 v212, 16, v146
	v_and_b32_e32 v213, 0xffff0000, v146
	v_pk_add_f32 v[208:209], v[208:209], 1.0 op_sel_hi:[1,0]
	v_pk_add_f32 v[210:211], v[210:211], 1.0 op_sel_hi:[1,0]
	v_lshlrev_b32_e32 v214, 16, v147
	v_and_b32_e32 v215, 0xffff0000, v147
	v_rcp_f32_e32 v208, v208
	v_rcp_f32_e32 v209, v209
	v_rcp_f32_e32 v210, v210
	v_rcp_f32_e32 v211, v211
	v_pk_fma_f32 v[208:209], v[100:101], v[208:209], v[212:213]
	v_pk_fma_f32 v[210:211], v[102:103], v[210:211], v[214:215]
	v_cvt_pk_bf16_f32 v250, v208, v209
	v_cvt_pk_bf16_f32 v251, v210, v211
	global_store_dwordx4 v[164:165], v[248:251], off offset:256
	v_add_u32_e32 v182, 128, v181
	v_mad_i64_i32 v[160:161], s[24:25], v182, s15, v[158:159]
	v_lshlrev_b32_e32 v174, 12, v182
	v_lshl_add_u64 v[172:173], v[166:167], 0, v[174:175]
	global_load_dwordx4 v[244:247], v[160:161], off offset:0
	global_load_dwordx4 v[248:251], v[160:161], off offset:256
	global_load_dwordx4 v[140:143], v[172:173], off
	global_load_dwordx4 v[144:147], v[172:173], off offset:256
	v_add_u32_e32 v182, 32, v181
	v_lshlrev_b32_e32 v174, 12, v182
	v_lshl_add_u64 v[164:165], v[162:163], 0, v[174:175]
	s_waitcnt vmcnt(13)
	v_lshlrev_b32_e32 v208, 16, v184
	v_and_b32_e32 v209, 0xffff0000, v184
	v_lshlrev_b32_e32 v210, 16, v185
	v_and_b32_e32 v211, 0xffff0000, v185
	v_mul_f32_e32 v208, 0xbfb8aa3b, v208
	v_mul_f32_e32 v209, 0xbfb8aa3b, v209
	v_mul_f32_e32 v210, 0xbfb8aa3b, v210
	v_mul_f32_e32 v211, 0xbfb8aa3b, v211
	v_exp_f32_e32 v208, v208
	v_exp_f32_e32 v209, v209
	v_exp_f32_e32 v210, v210
	v_exp_f32_e32 v211, v211
	v_lshlrev_b32_e32 v212, 16, v200
	v_and_b32_e32 v213, 0xffff0000, v200
	v_pk_add_f32 v[208:209], v[208:209], 1.0 op_sel_hi:[1,0]
	v_pk_add_f32 v[210:211], v[210:211], 1.0 op_sel_hi:[1,0]
	v_lshlrev_b32_e32 v214, 16, v201
	v_and_b32_e32 v215, 0xffff0000, v201
	v_rcp_f32_e32 v208, v208
	v_rcp_f32_e32 v209, v209
	v_rcp_f32_e32 v210, v210
	v_rcp_f32_e32 v211, v211
	v_pk_fma_f32 v[208:209], v[96:97], v[208:209], v[212:213]
	v_pk_fma_f32 v[210:211], v[98:99], v[210:211], v[214:215]
	v_cvt_pk_bf16_f32 v184, v208, v209
	v_cvt_pk_bf16_f32 v185, v210, v211
	v_lshlrev_b32_e32 v208, 16, v186
	v_and_b32_e32 v209, 0xffff0000, v186
	v_lshlrev_b32_e32 v210, 16, v187
	v_and_b32_e32 v211, 0xffff0000, v187
	v_mul_f32_e32 v208, 0xbfb8aa3b, v208
	v_mul_f32_e32 v209, 0xbfb8aa3b, v209
	v_mul_f32_e32 v210, 0xbfb8aa3b, v210
	v_mul_f32_e32 v211, 0xbfb8aa3b, v211
	v_exp_f32_e32 v208, v208
	v_exp_f32_e32 v209, v209
	v_exp_f32_e32 v210, v210
	v_exp_f32_e32 v211, v211
	v_lshlrev_b32_e32 v212, 16, v202
	v_and_b32_e32 v213, 0xffff0000, v202
	v_pk_add_f32 v[208:209], v[208:209], 1.0 op_sel_hi:[1,0]
	v_pk_add_f32 v[210:211], v[210:211], 1.0 op_sel_hi:[1,0]
	v_lshlrev_b32_e32 v214, 16, v203
	v_and_b32_e32 v215, 0xffff0000, v203
	v_rcp_f32_e32 v208, v208
	v_rcp_f32_e32 v209, v209
	v_rcp_f32_e32 v210, v210
	v_rcp_f32_e32 v211, v211
	v_pk_fma_f32 v[208:209], v[92:93], v[208:209], v[212:213]
	v_pk_fma_f32 v[210:211], v[94:95], v[210:211], v[214:215]
	v_cvt_pk_bf16_f32 v186, v208, v209
	v_cvt_pk_bf16_f32 v187, v210, v211
	global_store_dwordx4 v[164:165], v[184:187], off
	s_waitcnt vmcnt(13)
; DI unsigned pk2(float a, float b) { f32x2 v = {a, b}; bf16x2_t r = __builtin_convertvector(v, bf16x2_t); return __builtin_bit_cast(unsigned, r); }
; DI float sigmoidf_(float x) { return 1.f / (1.f + __expf(-x)); }
;     DI void operator()(const f32x4 (&acc)[2][2][4][2], const Unit& u, int wr, int wc, int fr, int fq) const {
;         const int row0 = u.pm * BM + wr * 64 + fr, col0 = u.pn * BM + wc * 32 + 8 * fq;
; #pragma unroll
;         for (int ai = 0; ai < 2; ++ai)
; #pragma unroll
;             for (int m = 0; m < 4; ++m) { const size_t row = (size_t)(row0 + ai * HALF + m * 16);
;                 u32x4 gzs[2], ts[2];
; #pragma unroll
;                 for (int bj = 0; bj < 2; ++bj) { const int col = col0 + bj * HALF; gzs[bj] = *(const u32x4*)(Zg + row * NZ + goff + col); if (add) ts[bj] = *(const u32x4*)(add + row * D + col); else ts[bj] = (u32x4){0u, 0u, 0u, 0u}; }
; #pragma unroll
;                 for (int bj = 0; bj < 2; ++bj) {
;                     const int col = col0 + bj * HALF;
;                     const u32x4 gz = gzs[bj];
;                     float a[8] = {0.f, 0.f, 0.f, 0.f, 0.f, 0.f, 0.f, 0.f};
;                     if (add) { const u32x4 t = ts[bj]; a[0] = bflo(t.x); a[1] = bfhi(t.x); a[2] = bflo(t.y); a[3] = bfhi(t.y); a[4] = bflo(t.z); a[5] = bfhi(t.z); a[6] = bflo(t.w); a[7] = bfhi(t.w); }
;                     const f32x4 v0 = acc[ai][bj][m][0], v1 = acc[ai][bj][m][1];
;                     float o[8];
;                     o[0] = a[0] + sigmoidf_(bflo(gz.x)) * v0[0]; o[1] = a[1] + sigmoidf_(bfhi(gz.x)) * v0[1];
;                     o[2] = a[2] + sigmoidf_(bflo(gz.y)) * v0[2]; o[3] = a[3] + sigmoidf_(bfhi(gz.y)) * v0[3];
;                     o[4] = a[4] + sigmoidf_(bflo(gz.z)) * v1[0]; o[5] = a[5] + sigmoidf_(bfhi(gz.z)) * v1[1];
;                     o[6] = a[6] + sigmoidf_(bflo(gz.w)) * v1[2]; o[7] = a[7] + sigmoidf_(bfhi(gz.w)) * v1[3];
;                     u32x4 w; w.x = pk2(o[0], o[1]); w.y = pk2(o[2], o[3]); w.z = pk2(o[4], o[5]); w.w = pk2(o[6], o[7]);
;                     *(u32x4*)(O + row * D + col) = w; } }
;     }
	v_lshlrev_b32_e32 v208, 16, v188
	v_and_b32_e32 v209, 0xffff0000, v188
	v_lshlrev_b32_e32 v210, 16, v189
	v_and_b32_e32 v211, 0xffff0000, v189
	v_mul_f32_e32 v208, 0xbfb8aa3b, v208
	v_mul_f32_e32 v209, 0xbfb8aa3b, v209
	v_mul_f32_e32 v210, 0xbfb8aa3b, v210
	v_mul_f32_e32 v211, 0xbfb8aa3b, v211
	v_exp_f32_e32 v208, v208
	v_exp_f32_e32 v209, v209
	v_exp_f32_e32 v210, v210
	v_exp_f32_e32 v211, v211
	v_lshlrev_b32_e32 v212, 16, v204
	v_and_b32_e32 v213, 0xffff0000, v204
	v_pk_add_f32 v[208:209], v[208:209], 1.0 op_sel_hi:[1,0]
	v_pk_add_f32 v[210:211], v[210:211], 1.0 op_sel_hi:[1,0]
	v_lshlrev_b32_e32 v214, 16, v205
	v_and_b32_e32 v215, 0xffff0000, v205
	v_rcp_f32_e32 v208, v208
	v_rcp_f32_e32 v209, v209
	v_rcp_f32_e32 v210, v210
	v_rcp_f32_e32 v211, v211
	v_pk_fma_f32 v[208:209], v[86:87], v[208:209], v[212:213]
	v_pk_fma_f32 v[210:211], v[88:89], v[210:211], v[214:215]
	v_cvt_pk_bf16_f32 v188, v208, v209
	v_cvt_pk_bf16_f32 v189, v210, v211
	v_lshlrev_b32_e32 v208, 16, v190
	v_and_b32_e32 v209, 0xffff0000, v190
	v_lshlrev_b32_e32 v210, 16, v191
	v_and_b32_e32 v211, 0xffff0000, v191
	v_mul_f32_e32 v208, 0xbfb8aa3b, v208
	v_mul_f32_e32 v209, 0xbfb8aa3b, v209
	v_mul_f32_e32 v210, 0xbfb8aa3b, v210
	v_mul_f32_e32 v211, 0xbfb8aa3b, v211
	v_exp_f32_e32 v208, v208
	v_exp_f32_e32 v209, v209
	v_exp_f32_e32 v210, v210
	v_exp_f32_e32 v211, v211
	v_lshlrev_b32_e32 v212, 16, v206
	v_and_b32_e32 v213, 0xffff0000, v206
	v_pk_add_f32 v[208:209], v[208:209], 1.0 op_sel_hi:[1,0]
	v_pk_add_f32 v[210:211], v[210:211], 1.0 op_sel_hi:[1,0]
	v_lshlrev_b32_e32 v214, 16, v207
	v_and_b32_e32 v215, 0xffff0000, v207
	v_rcp_f32_e32 v208, v208
	v_rcp_f32_e32 v209, v209
	v_rcp_f32_e32 v210, v210
	v_rcp_f32_e32 v211, v211
	v_pk_fma_f32 v[208:209], v[82:83], v[208:209], v[212:213]
	v_pk_fma_f32 v[210:211], v[84:85], v[210:211], v[214:215]
	v_cvt_pk_bf16_f32 v190, v208, v209
	v_cvt_pk_bf16_f32 v191, v210, v211
	global_store_dwordx4 v[164:165], v[188:191], off offset:256
	v_add_u32_e32 v182, 144, v181
	v_mad_i64_i32 v[160:161], s[24:25], v182, s15, v[158:159]
	v_lshlrev_b32_e32 v174, 12, v182
	v_lshl_add_u64 v[172:173], v[166:167], 0, v[174:175]
	global_load_dwordx4 v[184:187], v[160:161], off offset:0
	global_load_dwordx4 v[188:191], v[160:161], off offset:256
	global_load_dwordx4 v[200:203], v[172:173], off
	global_load_dwordx4 v[204:207], v[172:173], off offset:256
	v_add_u32_e32 v182, 48, v181
	v_lshlrev_b32_e32 v174, 12, v182
	v_lshl_add_u64 v[164:165], v[162:163], 0, v[174:175]
	s_waitcnt vmcnt(13)
	v_lshlrev_b32_e32 v208, 16, v236
	v_and_b32_e32 v209, 0xffff0000, v236
	v_lshlrev_b32_e32 v210, 16, v237
	v_and_b32_e32 v211, 0xffff0000, v237
	v_mul_f32_e32 v208, 0xbfb8aa3b, v208
	v_mul_f32_e32 v209, 0xbfb8aa3b, v209
	v_mul_f32_e32 v210, 0xbfb8aa3b, v210
	v_mul_f32_e32 v211, 0xbfb8aa3b, v211
	v_exp_f32_e32 v208, v208
	v_exp_f32_e32 v209, v209
	v_exp_f32_e32 v210, v210
	v_exp_f32_e32 v211, v211
	v_lshlrev_b32_e32 v212, 16, v128
	v_and_b32_e32 v213, 0xffff0000, v128
	v_pk_add_f32 v[208:209], v[208:209], 1.0 op_sel_hi:[1,0]
	v_pk_add_f32 v[210:211], v[210:211], 1.0 op_sel_hi:[1,0]
	v_lshlrev_b32_e32 v214, 16, v129
	v_and_b32_e32 v215, 0xffff0000, v129
	v_rcp_f32_e32 v208, v208
	v_rcp_f32_e32 v209, v209
	v_rcp_f32_e32 v210, v210
	v_rcp_f32_e32 v211, v211
	v_pk_fma_f32 v[208:209], v[78:79], v[208:209], v[212:213]
	v_pk_fma_f32 v[210:211], v[80:81], v[210:211], v[214:215]
	v_cvt_pk_bf16_f32 v236, v208, v209
	v_cvt_pk_bf16_f32 v237, v210, v211
	v_lshlrev_b32_e32 v208, 16, v238
	v_and_b32_e32 v209, 0xffff0000, v238
	v_lshlrev_b32_e32 v210, 16, v239
	v_and_b32_e32 v211, 0xffff0000, v239
	v_mul_f32_e32 v208, 0xbfb8aa3b, v208
	v_mul_f32_e32 v209, 0xbfb8aa3b, v209
	v_mul_f32_e32 v210, 0xbfb8aa3b, v210
	v_mul_f32_e32 v211, 0xbfb8aa3b, v211
	v_exp_f32_e32 v208, v208
	v_exp_f32_e32 v209, v209
	v_exp_f32_e32 v210, v210
	v_exp_f32_e32 v211, v211
	v_lshlrev_b32_e32 v212, 16, v130
	v_and_b32_e32 v213, 0xffff0000, v130
	v_pk_add_f32 v[208:209], v[208:209], 1.0 op_sel_hi:[1,0]
	v_pk_add_f32 v[210:211], v[210:211], 1.0 op_sel_hi:[1,0]
	v_lshlrev_b32_e32 v214, 16, v131
	v_and_b32_e32 v215, 0xffff0000, v131
	v_rcp_f32_e32 v208, v208
	v_rcp_f32_e32 v209, v209
	v_rcp_f32_e32 v210, v210
	v_rcp_f32_e32 v211, v211
	v_pk_fma_f32 v[208:209], v[74:75], v[208:209], v[212:213]
	v_pk_fma_f32 v[210:211], v[76:77], v[210:211], v[214:215]
	v_cvt_pk_bf16_f32 v238, v208, v209
	v_cvt_pk_bf16_f32 v239, v210, v211
	global_store_dwordx4 v[164:165], v[236:239], off
	s_waitcnt vmcnt(13)
; DI unsigned pk2(float a, float b) { f32x2 v = {a, b}; bf16x2_t r = __builtin_convertvector(v, bf16x2_t); return __builtin_bit_cast(unsigned, r); }
; DI float sigmoidf_(float x) { return 1.f / (1.f + __expf(-x)); }
;     DI void operator()(const f32x4 (&acc)[2][2][4][2], const Unit& u, int wr, int wc, int fr, int fq) const {
;         const int row0 = u.pm * BM + wr * 64 + fr, col0 = u.pn * BM + wc * 32 + 8 * fq;
; #pragma unroll
;         for (int ai = 0; ai < 2; ++ai)
; #pragma unroll
;             for (int m = 0; m < 4; ++m) { const size_t row = (size_t)(row0 + ai * HALF + m * 16);
;                 u32x4 gzs[2], ts[2];
; #pragma unroll
;                 for (int bj = 0; bj < 2; ++bj) { const int col = col0 + bj * HALF; gzs[bj] = *(const u32x4*)(Zg + row * NZ + goff + col); if (add) ts[bj] = *(const u32x4*)(add + row * D + col); else ts[bj] = (u32x4){0u, 0u, 0u, 0u}; }
; #pragma unroll
;                 for (int bj = 0; bj < 2; ++bj) {
;                     const int col = col0 + bj * HALF;
;                     const u32x4 gz = gzs[bj];
;                     float a[8] = {0.f, 0.f, 0.f, 0.f, 0.f, 0.f, 0.f, 0.f};
;                     if (add) { const u32x4 t = ts[bj]; a[0] = bflo(t.x); a[1] = bfhi(t.x); a[2] = bflo(t.y); a[3] = bfhi(t.y); a[4] = bflo(t.z); a[5] = bfhi(t.z); a[6] = bflo(t.w); a[7] = bfhi(t.w); }
;                     const f32x4 v0 = acc[ai][bj][m][0], v1 = acc[ai][bj][m][1];
;                     float o[8];
;                     o[0] = a[0] + sigmoidf_(bflo(gz.x)) * v0[0]; o[1] = a[1] + sigmoidf_(bfhi(gz.x)) * v0[1];
;                     o[2] = a[2] + sigmoidf_(bflo(gz.y)) * v0[2]; o[3] = a[3] + sigmoidf_(bfhi(gz.y)) * v0[3];
;                     o[4] = a[4] + sigmoidf_(bflo(gz.z)) * v1[0]; o[5] = a[5] + sigmoidf_(bfhi(gz.z)) * v1[1];
;                     o[6] = a[6] + sigmoidf_(bflo(gz.w)) * v1[2]; o[7] = a[7] + sigmoidf_(bfhi(gz.w)) * v1[3];
;                     u32x4 w; w.x = pk2(o[0], o[1]); w.y = pk2(o[2], o[3]); w.z = pk2(o[4], o[5]); w.w = pk2(o[6], o[7]);
;                     *(u32x4*)(O + row * D + col) = w; } }
;     }
	v_lshlrev_b32_e32 v208, 16, v240
	v_and_b32_e32 v209, 0xffff0000, v240
	v_lshlrev_b32_e32 v210, 16, v241
	v_and_b32_e32 v211, 0xffff0000, v241
	v_mul_f32_e32 v208, 0xbfb8aa3b, v208
	v_mul_f32_e32 v209, 0xbfb8aa3b, v209
	v_mul_f32_e32 v210, 0xbfb8aa3b, v210
	v_mul_f32_e32 v211, 0xbfb8aa3b, v211
	v_exp_f32_e32 v208, v208
	v_exp_f32_e32 v209, v209
	v_exp_f32_e32 v210, v210
	v_exp_f32_e32 v211, v211
	v_lshlrev_b32_e32 v212, 16, v132
	v_and_b32_e32 v213, 0xffff0000, v132
	v_pk_add_f32 v[208:209], v[208:209], 1.0 op_sel_hi:[1,0]
	v_pk_add_f32 v[210:211], v[210:211], 1.0 op_sel_hi:[1,0]
	v_lshlrev_b32_e32 v214, 16, v133
	v_and_b32_e32 v215, 0xffff0000, v133
	v_rcp_f32_e32 v208, v208
	v_rcp_f32_e32 v209, v209
	v_rcp_f32_e32 v210, v210
	v_rcp_f32_e32 v211, v211
	v_pk_fma_f32 v[208:209], v[70:71], v[208:209], v[212:213]
	v_pk_fma_f32 v[210:211], v[72:73], v[210:211], v[214:215]
	v_cvt_pk_bf16_f32 v240, v208, v209
	v_cvt_pk_bf16_f32 v241, v210, v211
	v_lshlrev_b32_e32 v208, 16, v242
	v_and_b32_e32 v209, 0xffff0000, v242
	v_lshlrev_b32_e32 v210, 16, v243
	v_and_b32_e32 v211, 0xffff0000, v243
	v_mul_f32_e32 v208, 0xbfb8aa3b, v208
	v_mul_f32_e32 v209, 0xbfb8aa3b, v209
	v_mul_f32_e32 v210, 0xbfb8aa3b, v210
	v_mul_f32_e32 v211, 0xbfb8aa3b, v211
	v_exp_f32_e32 v208, v208
	v_exp_f32_e32 v209, v209
	v_exp_f32_e32 v210, v210
	v_exp_f32_e32 v211, v211
	v_lshlrev_b32_e32 v212, 16, v134
	v_and_b32_e32 v213, 0xffff0000, v134
	v_pk_add_f32 v[208:209], v[208:209], 1.0 op_sel_hi:[1,0]
	v_pk_add_f32 v[210:211], v[210:211], 1.0 op_sel_hi:[1,0]
	v_lshlrev_b32_e32 v214, 16, v135
	v_and_b32_e32 v215, 0xffff0000, v135
	v_rcp_f32_e32 v208, v208
	v_rcp_f32_e32 v209, v209
	v_rcp_f32_e32 v210, v210
	v_rcp_f32_e32 v211, v211
	v_pk_fma_f32 v[208:209], v[66:67], v[208:209], v[212:213]
	v_pk_fma_f32 v[210:211], v[68:69], v[210:211], v[214:215]
	v_cvt_pk_bf16_f32 v242, v208, v209
	v_cvt_pk_bf16_f32 v243, v210, v211
	global_store_dwordx4 v[164:165], v[240:243], off offset:256
	v_add_u32_e32 v182, 160, v181
	v_mad_i64_i32 v[160:161], s[24:25], v182, s15, v[158:159]
	v_lshlrev_b32_e32 v174, 12, v182
	v_lshl_add_u64 v[172:173], v[166:167], 0, v[174:175]
	global_load_dwordx4 v[236:239], v[160:161], off offset:0
	global_load_dwordx4 v[240:243], v[160:161], off offset:256
	global_load_dwordx4 v[128:131], v[172:173], off
	global_load_dwordx4 v[132:135], v[172:173], off offset:256
	v_add_u32_e32 v182, 128, v181
	v_lshlrev_b32_e32 v174, 12, v182
	v_lshl_add_u64 v[164:165], v[162:163], 0, v[174:175]
	s_waitcnt vmcnt(13)
	v_lshlrev_b32_e32 v208, 16, v244
	v_and_b32_e32 v209, 0xffff0000, v244
	v_lshlrev_b32_e32 v210, 16, v245
	v_and_b32_e32 v211, 0xffff0000, v245
	v_mul_f32_e32 v208, 0xbfb8aa3b, v208
	v_mul_f32_e32 v209, 0xbfb8aa3b, v209
	v_mul_f32_e32 v210, 0xbfb8aa3b, v210
	v_mul_f32_e32 v211, 0xbfb8aa3b, v211
	v_exp_f32_e32 v208, v208
	v_exp_f32_e32 v209, v209
	v_exp_f32_e32 v210, v210
	v_exp_f32_e32 v211, v211
	v_lshlrev_b32_e32 v212, 16, v140
	v_and_b32_e32 v213, 0xffff0000, v140
	v_pk_add_f32 v[208:209], v[208:209], 1.0 op_sel_hi:[1,0]
	v_pk_add_f32 v[210:211], v[210:211], 1.0 op_sel_hi:[1,0]
	v_lshlrev_b32_e32 v214, 16, v141
	v_and_b32_e32 v215, 0xffff0000, v141
	v_rcp_f32_e32 v208, v208
	v_rcp_f32_e32 v209, v209
	v_rcp_f32_e32 v210, v210
	v_rcp_f32_e32 v211, v211
	v_pk_fma_f32 v[208:209], v[62:63], v[208:209], v[212:213]
	v_pk_fma_f32 v[210:211], v[64:65], v[210:211], v[214:215]
	v_cvt_pk_bf16_f32 v244, v208, v209
	v_cvt_pk_bf16_f32 v245, v210, v211
	v_lshlrev_b32_e32 v208, 16, v246
	v_and_b32_e32 v209, 0xffff0000, v246
	v_lshlrev_b32_e32 v210, 16, v247
	v_and_b32_e32 v211, 0xffff0000, v247
	v_mul_f32_e32 v208, 0xbfb8aa3b, v208
	v_mul_f32_e32 v209, 0xbfb8aa3b, v209
	v_mul_f32_e32 v210, 0xbfb8aa3b, v210
	v_mul_f32_e32 v211, 0xbfb8aa3b, v211
	v_exp_f32_e32 v208, v208
	v_exp_f32_e32 v209, v209
	v_exp_f32_e32 v210, v210
	v_exp_f32_e32 v211, v211
	v_lshlrev_b32_e32 v212, 16, v142
	v_and_b32_e32 v213, 0xffff0000, v142
	v_pk_add_f32 v[208:209], v[208:209], 1.0 op_sel_hi:[1,0]
	v_pk_add_f32 v[210:211], v[210:211], 1.0 op_sel_hi:[1,0]
	v_lshlrev_b32_e32 v214, 16, v143
	v_and_b32_e32 v215, 0xffff0000, v143
	v_rcp_f32_e32 v208, v208
	v_rcp_f32_e32 v209, v209
	v_rcp_f32_e32 v210, v210
	v_rcp_f32_e32 v211, v211
	v_pk_fma_f32 v[208:209], v[58:59], v[208:209], v[212:213]
	v_pk_fma_f32 v[210:211], v[60:61], v[210:211], v[214:215]
	v_cvt_pk_bf16_f32 v246, v208, v209
	v_cvt_pk_bf16_f32 v247, v210, v211
	global_store_dwordx4 v[164:165], v[244:247], off
	s_waitcnt vmcnt(13)
; DI unsigned pk2(float a, float b) { f32x2 v = {a, b}; bf16x2_t r = __builtin_convertvector(v, bf16x2_t); return __builtin_bit_cast(unsigned, r); }
; DI float sigmoidf_(float x) { return 1.f / (1.f + __expf(-x)); }
;     DI void operator()(const f32x4 (&acc)[2][2][4][2], const Unit& u, int wr, int wc, int fr, int fq) const {
;         const int row0 = u.pm * BM + wr * 64 + fr, col0 = u.pn * BM + wc * 32 + 8 * fq;
; #pragma unroll
;         for (int ai = 0; ai < 2; ++ai)
; #pragma unroll
;             for (int m = 0; m < 4; ++m) { const size_t row = (size_t)(row0 + ai * HALF + m * 16);
;                 u32x4 gzs[2], ts[2];
; #pragma unroll
;                 for (int bj = 0; bj < 2; ++bj) { const int col = col0 + bj * HALF; gzs[bj] = *(const u32x4*)(Zg + row * NZ + goff + col); if (add) ts[bj] = *(const u32x4*)(add + row * D + col); else ts[bj] = (u32x4){0u, 0u, 0u, 0u}; }
; #pragma unroll
;                 for (int bj = 0; bj < 2; ++bj) {
;                     const int col = col0 + bj * HALF;
;                     const u32x4 gz = gzs[bj];
;                     float a[8] = {0.f, 0.f, 0.f, 0.f, 0.f, 0.f, 0.f, 0.f};
;                     if (add) { const u32x4 t = ts[bj]; a[0] = bflo(t.x); a[1] = bfhi(t.x); a[2] = bflo(t.y); a[3] = bfhi(t.y); a[4] = bflo(t.z); a[5] = bfhi(t.z); a[6] = bflo(t.w); a[7] = bfhi(t.w); }
;                     const f32x4 v0 = acc[ai][bj][m][0], v1 = acc[ai][bj][m][1];
;                     float o[8];
;                     o[0] = a[0] + sigmoidf_(bflo(gz.x)) * v0[0]; o[1] = a[1] + sigmoidf_(bfhi(gz.x)) * v0[1];
;                     o[2] = a[2] + sigmoidf_(bflo(gz.y)) * v0[2]; o[3] = a[3] + sigmoidf_(bfhi(gz.y)) * v0[3];
;                     o[4] = a[4] + sigmoidf_(bflo(gz.z)) * v1[0]; o[5] = a[5] + sigmoidf_(bfhi(gz.z)) * v1[1];
;                     o[6] = a[6] + sigmoidf_(bflo(gz.w)) * v1[2]; o[7] = a[7] + sigmoidf_(bfhi(gz.w)) * v1[3];
;                     u32x4 w; w.x = pk2(o[0], o[1]); w.y = pk2(o[2], o[3]); w.z = pk2(o[4], o[5]); w.w = pk2(o[6], o[7]);
;                     *(u32x4*)(O + row * D + col) = w; } }
;     }
	v_lshlrev_b32_e32 v208, 16, v248
	v_and_b32_e32 v209, 0xffff0000, v248
	v_lshlrev_b32_e32 v210, 16, v249
	v_and_b32_e32 v211, 0xffff0000, v249
	v_mul_f32_e32 v208, 0xbfb8aa3b, v208
	v_mul_f32_e32 v209, 0xbfb8aa3b, v209
	v_mul_f32_e32 v210, 0xbfb8aa3b, v210
	v_mul_f32_e32 v211, 0xbfb8aa3b, v211
	v_exp_f32_e32 v208, v208
	v_exp_f32_e32 v209, v209
	v_exp_f32_e32 v210, v210
	v_exp_f32_e32 v211, v211
	v_lshlrev_b32_e32 v212, 16, v144
	v_and_b32_e32 v213, 0xffff0000, v144
	v_pk_add_f32 v[208:209], v[208:209], 1.0 op_sel_hi:[1,0]
	v_pk_add_f32 v[210:211], v[210:211], 1.0 op_sel_hi:[1,0]
	v_lshlrev_b32_e32 v214, 16, v145
	v_and_b32_e32 v215, 0xffff0000, v145
	v_rcp_f32_e32 v208, v208
	v_rcp_f32_e32 v209, v209
	v_rcp_f32_e32 v210, v210
	v_rcp_f32_e32 v211, v211
	v_pk_fma_f32 v[208:209], v[54:55], v[208:209], v[212:213]
	v_pk_fma_f32 v[210:211], v[56:57], v[210:211], v[214:215]
	v_cvt_pk_bf16_f32 v248, v208, v209
	v_cvt_pk_bf16_f32 v249, v210, v211
	v_lshlrev_b32_e32 v208, 16, v250
	v_and_b32_e32 v209, 0xffff0000, v250
	v_lshlrev_b32_e32 v210, 16, v251
	v_and_b32_e32 v211, 0xffff0000, v251
	v_mul_f32_e32 v208, 0xbfb8aa3b, v208
	v_mul_f32_e32 v209, 0xbfb8aa3b, v209
	v_mul_f32_e32 v210, 0xbfb8aa3b, v210
	v_mul_f32_e32 v211, 0xbfb8aa3b, v211
	v_exp_f32_e32 v208, v208
	v_exp_f32_e32 v209, v209
	v_exp_f32_e32 v210, v210
	v_exp_f32_e32 v211, v211
	v_lshlrev_b32_e32 v212, 16, v146
	v_and_b32_e32 v213, 0xffff0000, v146
	v_pk_add_f32 v[208:209], v[208:209], 1.0 op_sel_hi:[1,0]
	v_pk_add_f32 v[210:211], v[210:211], 1.0 op_sel_hi:[1,0]
	v_lshlrev_b32_e32 v214, 16, v147
	v_and_b32_e32 v215, 0xffff0000, v147
	v_rcp_f32_e32 v208, v208
	v_rcp_f32_e32 v209, v209
	v_rcp_f32_e32 v210, v210
	v_rcp_f32_e32 v211, v211
	v_pk_fma_f32 v[208:209], v[50:51], v[208:209], v[212:213]
	v_pk_fma_f32 v[210:211], v[52:53], v[210:211], v[214:215]
	v_cvt_pk_bf16_f32 v250, v208, v209
	v_cvt_pk_bf16_f32 v251, v210, v211
	global_store_dwordx4 v[164:165], v[248:251], off offset:256
	v_add_u32_e32 v182, 176, v181
	v_mad_i64_i32 v[160:161], s[24:25], v182, s15, v[158:159]
	v_lshlrev_b32_e32 v174, 12, v182
	v_lshl_add_u64 v[172:173], v[166:167], 0, v[174:175]
	global_load_dwordx4 v[244:247], v[160:161], off offset:0
	global_load_dwordx4 v[248:251], v[160:161], off offset:256
	global_load_dwordx4 v[140:143], v[172:173], off
	global_load_dwordx4 v[144:147], v[172:173], off offset:256
	v_add_u32_e32 v182, 144, v181
	v_lshlrev_b32_e32 v174, 12, v182
	v_lshl_add_u64 v[164:165], v[162:163], 0, v[174:175]
	s_waitcnt vmcnt(13)
	v_lshlrev_b32_e32 v208, 16, v184
	v_and_b32_e32 v209, 0xffff0000, v184
	v_lshlrev_b32_e32 v210, 16, v185
	v_and_b32_e32 v211, 0xffff0000, v185
	v_mul_f32_e32 v208, 0xbfb8aa3b, v208
	v_mul_f32_e32 v209, 0xbfb8aa3b, v209
	v_mul_f32_e32 v210, 0xbfb8aa3b, v210
	v_mul_f32_e32 v211, 0xbfb8aa3b, v211
	v_exp_f32_e32 v208, v208
	v_exp_f32_e32 v209, v209
	v_exp_f32_e32 v210, v210
	v_exp_f32_e32 v211, v211
	v_lshlrev_b32_e32 v212, 16, v200
	v_and_b32_e32 v213, 0xffff0000, v200
	v_pk_add_f32 v[208:209], v[208:209], 1.0 op_sel_hi:[1,0]
	v_pk_add_f32 v[210:211], v[210:211], 1.0 op_sel_hi:[1,0]
	v_lshlrev_b32_e32 v214, 16, v201
	v_and_b32_e32 v215, 0xffff0000, v201
	v_rcp_f32_e32 v208, v208
	v_rcp_f32_e32 v209, v209
	v_rcp_f32_e32 v210, v210
	v_rcp_f32_e32 v211, v211
	v_pk_fma_f32 v[208:209], v[46:47], v[208:209], v[212:213]
	v_pk_fma_f32 v[210:211], v[48:49], v[210:211], v[214:215]
	v_cvt_pk_bf16_f32 v184, v208, v209
	v_cvt_pk_bf16_f32 v185, v210, v211
	v_lshlrev_b32_e32 v208, 16, v186
	v_and_b32_e32 v209, 0xffff0000, v186
	v_lshlrev_b32_e32 v210, 16, v187
	v_and_b32_e32 v211, 0xffff0000, v187
	v_mul_f32_e32 v208, 0xbfb8aa3b, v208
	v_mul_f32_e32 v209, 0xbfb8aa3b, v209
	v_mul_f32_e32 v210, 0xbfb8aa3b, v210
	v_mul_f32_e32 v211, 0xbfb8aa3b, v211
	v_exp_f32_e32 v208, v208
	v_exp_f32_e32 v209, v209
	v_exp_f32_e32 v210, v210
	v_exp_f32_e32 v211, v211
	v_lshlrev_b32_e32 v212, 16, v202
	v_and_b32_e32 v213, 0xffff0000, v202
	v_pk_add_f32 v[208:209], v[208:209], 1.0 op_sel_hi:[1,0]
	v_pk_add_f32 v[210:211], v[210:211], 1.0 op_sel_hi:[1,0]
	v_lshlrev_b32_e32 v214, 16, v203
	v_and_b32_e32 v215, 0xffff0000, v203
	v_rcp_f32_e32 v208, v208
	v_rcp_f32_e32 v209, v209
	v_rcp_f32_e32 v210, v210
	v_rcp_f32_e32 v211, v211
	v_pk_fma_f32 v[208:209], v[42:43], v[208:209], v[212:213]
	v_pk_fma_f32 v[210:211], v[44:45], v[210:211], v[214:215]
	v_cvt_pk_bf16_f32 v186, v208, v209
	v_cvt_pk_bf16_f32 v187, v210, v211
	global_store_dwordx4 v[164:165], v[184:187], off
	s_waitcnt vmcnt(13)
	v_lshlrev_b32_e32 v208, 16, v188
	v_and_b32_e32 v209, 0xffff0000, v188
	v_lshlrev_b32_e32 v210, 16, v189
	v_and_b32_e32 v211, 0xffff0000, v189
	v_mul_f32_e32 v208, 0xbfb8aa3b, v208
	v_mul_f32_e32 v209, 0xbfb8aa3b, v209
	v_mul_f32_e32 v210, 0xbfb8aa3b, v210
	v_mul_f32_e32 v211, 0xbfb8aa3b, v211
	v_exp_f32_e32 v208, v208
	v_exp_f32_e32 v209, v209
	v_exp_f32_e32 v210, v210
	v_exp_f32_e32 v211, v211
	v_lshlrev_b32_e32 v212, 16, v204
	v_and_b32_e32 v213, 0xffff0000, v204
	v_pk_add_f32 v[208:209], v[208:209], 1.0 op_sel_hi:[1,0]
	v_pk_add_f32 v[210:211], v[210:211], 1.0 op_sel_hi:[1,0]
	v_lshlrev_b32_e32 v214, 16, v205
	v_and_b32_e32 v215, 0xffff0000, v205
	v_rcp_f32_e32 v208, v208
	v_rcp_f32_e32 v209, v209
	v_rcp_f32_e32 v210, v210
	v_rcp_f32_e32 v211, v211
	v_pk_fma_f32 v[208:209], v[38:39], v[208:209], v[212:213]
	v_pk_fma_f32 v[210:211], v[40:41], v[210:211], v[214:215]
	v_cvt_pk_bf16_f32 v188, v208, v209
	v_cvt_pk_bf16_f32 v189, v210, v211
	v_lshlrev_b32_e32 v208, 16, v190
	v_and_b32_e32 v209, 0xffff0000, v190
	v_lshlrev_b32_e32 v210, 16, v191
	v_and_b32_e32 v211, 0xffff0000, v191
	v_mul_f32_e32 v208, 0xbfb8aa3b, v208
	v_mul_f32_e32 v209, 0xbfb8aa3b, v209
	v_mul_f32_e32 v210, 0xbfb8aa3b, v210
	v_mul_f32_e32 v211, 0xbfb8aa3b, v211
	v_exp_f32_e32 v208, v208
	v_exp_f32_e32 v209, v209
	v_exp_f32_e32 v210, v210
	v_exp_f32_e32 v211, v211
	v_lshlrev_b32_e32 v212, 16, v206
	v_and_b32_e32 v213, 0xffff0000, v206
	v_pk_add_f32 v[208:209], v[208:209], 1.0 op_sel_hi:[1,0]
	v_pk_add_f32 v[210:211], v[210:211], 1.0 op_sel_hi:[1,0]
	v_lshlrev_b32_e32 v214, 16, v207
	v_and_b32_e32 v215, 0xffff0000, v207
	v_rcp_f32_e32 v208, v208
	v_rcp_f32_e32 v209, v209
	v_rcp_f32_e32 v210, v210
	v_rcp_f32_e32 v211, v211
	v_pk_fma_f32 v[208:209], v[34:35], v[208:209], v[212:213]
	v_pk_fma_f32 v[210:211], v[36:37], v[210:211], v[214:215]
	v_cvt_pk_bf16_f32 v190, v208, v209
	v_cvt_pk_bf16_f32 v191, v210, v211
	global_store_dwordx4 v[164:165], v[188:191], off offset:256
	v_add_u32_e32 v182, 160, v181
	v_lshlrev_b32_e32 v174, 12, v182
	v_lshl_add_u64 v[164:165], v[162:163], 0, v[174:175]
	s_waitcnt vmcnt(9)
; DI unsigned pk2(float a, float b) { f32x2 v = {a, b}; bf16x2_t r = __builtin_convertvector(v, bf16x2_t); return __builtin_bit_cast(unsigned, r); }
; DI float sigmoidf_(float x) { return 1.f / (1.f + __expf(-x)); }
;     DI void operator()(const f32x4 (&acc)[2][2][4][2], const Unit& u, int wr, int wc, int fr, int fq) const {
;         const int row0 = u.pm * BM + wr * 64 + fr, col0 = u.pn * BM + wc * 32 + 8 * fq;
; #pragma unroll
;         for (int ai = 0; ai < 2; ++ai)
; #pragma unroll
;             for (int m = 0; m < 4; ++m) { const size_t row = (size_t)(row0 + ai * HALF + m * 16);
;                 u32x4 gzs[2], ts[2];
; #pragma unroll
;                 for (int bj = 0; bj < 2; ++bj) { const int col = col0 + bj * HALF; gzs[bj] = *(const u32x4*)(Zg + row * NZ + goff + col); if (add) ts[bj] = *(const u32x4*)(add + row * D + col); else ts[bj] = (u32x4){0u, 0u, 0u, 0u}; }
; #pragma unroll
;                 for (int bj = 0; bj < 2; ++bj) {
;                     const int col = col0 + bj * HALF;
;                     const u32x4 gz = gzs[bj];
;                     float a[8] = {0.f, 0.f, 0.f, 0.f, 0.f, 0.f, 0.f, 0.f};
;                     if (add) { const u32x4 t = ts[bj]; a[0] = bflo(t.x); a[1] = bfhi(t.x); a[2] = bflo(t.y); a[3] = bfhi(t.y); a[4] = bflo(t.z); a[5] = bfhi(t.z); a[6] = bflo(t.w); a[7] = bfhi(t.w); }
;                     const f32x4 v0 = acc[ai][bj][m][0], v1 = acc[ai][bj][m][1];
;                     float o[8];
;                     o[0] = a[0] + sigmoidf_(bflo(gz.x)) * v0[0]; o[1] = a[1] + sigmoidf_(bfhi(gz.x)) * v0[1];
;                     o[2] = a[2] + sigmoidf_(bflo(gz.y)) * v0[2]; o[3] = a[3] + sigmoidf_(bfhi(gz.y)) * v0[3];
;                     o[4] = a[4] + sigmoidf_(bflo(gz.z)) * v1[0]; o[5] = a[5] + sigmoidf_(bfhi(gz.z)) * v1[1];
;                     o[6] = a[6] + sigmoidf_(bflo(gz.w)) * v1[2]; o[7] = a[7] + sigmoidf_(bfhi(gz.w)) * v1[3];
;                     u32x4 w; w.x = pk2(o[0], o[1]); w.y = pk2(o[2], o[3]); w.z = pk2(o[4], o[5]); w.w = pk2(o[6], o[7]);
;                     *(u32x4*)(O + row * D + col) = w; } }
;     }
	v_lshlrev_b32_e32 v208, 16, v236
	v_and_b32_e32 v209, 0xffff0000, v236
	v_lshlrev_b32_e32 v210, 16, v237
	v_and_b32_e32 v211, 0xffff0000, v237
	v_mul_f32_e32 v208, 0xbfb8aa3b, v208
	v_mul_f32_e32 v209, 0xbfb8aa3b, v209
	v_mul_f32_e32 v210, 0xbfb8aa3b, v210
	v_mul_f32_e32 v211, 0xbfb8aa3b, v211
	v_exp_f32_e32 v208, v208
	v_exp_f32_e32 v209, v209
	v_exp_f32_e32 v210, v210
	v_exp_f32_e32 v211, v211
	v_lshlrev_b32_e32 v212, 16, v128
	v_and_b32_e32 v213, 0xffff0000, v128
	v_pk_add_f32 v[208:209], v[208:209], 1.0 op_sel_hi:[1,0]
	v_pk_add_f32 v[210:211], v[210:211], 1.0 op_sel_hi:[1,0]
	v_lshlrev_b32_e32 v214, 16, v129
	v_and_b32_e32 v215, 0xffff0000, v129
	v_rcp_f32_e32 v208, v208
	v_rcp_f32_e32 v209, v209
	v_rcp_f32_e32 v210, v210
	v_rcp_f32_e32 v211, v211
	v_pk_fma_f32 v[208:209], v[30:31], v[208:209], v[212:213]
	v_pk_fma_f32 v[210:211], v[32:33], v[210:211], v[214:215]
	v_cvt_pk_bf16_f32 v236, v208, v209
	v_cvt_pk_bf16_f32 v237, v210, v211
	v_lshlrev_b32_e32 v208, 16, v238
	v_and_b32_e32 v209, 0xffff0000, v238
	v_lshlrev_b32_e32 v210, 16, v239
	v_and_b32_e32 v211, 0xffff0000, v239
	v_mul_f32_e32 v208, 0xbfb8aa3b, v208
	v_mul_f32_e32 v209, 0xbfb8aa3b, v209
	v_mul_f32_e32 v210, 0xbfb8aa3b, v210
	v_mul_f32_e32 v211, 0xbfb8aa3b, v211
	v_exp_f32_e32 v208, v208
	v_exp_f32_e32 v209, v209
	v_exp_f32_e32 v210, v210
	v_exp_f32_e32 v211, v211
	v_lshlrev_b32_e32 v212, 16, v130
	v_and_b32_e32 v213, 0xffff0000, v130
	v_pk_add_f32 v[208:209], v[208:209], 1.0 op_sel_hi:[1,0]
	v_pk_add_f32 v[210:211], v[210:211], 1.0 op_sel_hi:[1,0]
	v_lshlrev_b32_e32 v214, 16, v131
	v_and_b32_e32 v215, 0xffff0000, v131
	v_rcp_f32_e32 v208, v208
	v_rcp_f32_e32 v209, v209
	v_rcp_f32_e32 v210, v210
	v_rcp_f32_e32 v211, v211
	v_pk_fma_f32 v[208:209], v[26:27], v[208:209], v[212:213]
	v_pk_fma_f32 v[210:211], v[28:29], v[210:211], v[214:215]
	v_cvt_pk_bf16_f32 v238, v208, v209
	v_cvt_pk_bf16_f32 v239, v210, v211
	global_store_dwordx4 v[164:165], v[236:239], off
	s_waitcnt vmcnt(9)
	v_lshlrev_b32_e32 v208, 16, v240
	v_and_b32_e32 v209, 0xffff0000, v240
	v_lshlrev_b32_e32 v210, 16, v241
	v_and_b32_e32 v211, 0xffff0000, v241
	v_mul_f32_e32 v208, 0xbfb8aa3b, v208
	v_mul_f32_e32 v209, 0xbfb8aa3b, v209
	v_mul_f32_e32 v210, 0xbfb8aa3b, v210
	v_mul_f32_e32 v211, 0xbfb8aa3b, v211
	v_exp_f32_e32 v208, v208
	v_exp_f32_e32 v209, v209
	v_exp_f32_e32 v210, v210
	v_exp_f32_e32 v211, v211
	v_lshlrev_b32_e32 v212, 16, v132
	v_and_b32_e32 v213, 0xffff0000, v132
	v_pk_add_f32 v[208:209], v[208:209], 1.0 op_sel_hi:[1,0]
	v_pk_add_f32 v[210:211], v[210:211], 1.0 op_sel_hi:[1,0]
	v_lshlrev_b32_e32 v214, 16, v133
	v_and_b32_e32 v215, 0xffff0000, v133
	v_rcp_f32_e32 v208, v208
	v_rcp_f32_e32 v209, v209
	v_rcp_f32_e32 v210, v210
	v_rcp_f32_e32 v211, v211
	v_pk_fma_f32 v[208:209], v[22:23], v[208:209], v[212:213]
	v_pk_fma_f32 v[210:211], v[24:25], v[210:211], v[214:215]
	v_cvt_pk_bf16_f32 v240, v208, v209
	v_cvt_pk_bf16_f32 v241, v210, v211
	v_lshlrev_b32_e32 v208, 16, v242
	v_and_b32_e32 v209, 0xffff0000, v242
	v_lshlrev_b32_e32 v210, 16, v243
	v_and_b32_e32 v211, 0xffff0000, v243
	v_mul_f32_e32 v208, 0xbfb8aa3b, v208
	v_mul_f32_e32 v209, 0xbfb8aa3b, v209
	v_mul_f32_e32 v210, 0xbfb8aa3b, v210
	v_mul_f32_e32 v211, 0xbfb8aa3b, v211
	v_exp_f32_e32 v208, v208
	v_exp_f32_e32 v209, v209
	v_exp_f32_e32 v210, v210
	v_exp_f32_e32 v211, v211
	v_lshlrev_b32_e32 v212, 16, v134
	v_and_b32_e32 v213, 0xffff0000, v134
	v_pk_add_f32 v[208:209], v[208:209], 1.0 op_sel_hi:[1,0]
	v_pk_add_f32 v[210:211], v[210:211], 1.0 op_sel_hi:[1,0]
	v_lshlrev_b32_e32 v214, 16, v135
	v_and_b32_e32 v215, 0xffff0000, v135
	v_rcp_f32_e32 v208, v208
	v_rcp_f32_e32 v209, v209
	v_rcp_f32_e32 v210, v210
	v_rcp_f32_e32 v211, v211
	v_pk_fma_f32 v[208:209], v[18:19], v[208:209], v[212:213]
	v_pk_fma_f32 v[210:211], v[20:21], v[210:211], v[214:215]
	v_cvt_pk_bf16_f32 v242, v208, v209
	v_cvt_pk_bf16_f32 v243, v210, v211
	global_store_dwordx4 v[164:165], v[240:243], off offset:256
	v_add_u32_e32 v182, 176, v181
	v_lshlrev_b32_e32 v174, 12, v182
	v_lshl_add_u64 v[164:165], v[162:163], 0, v[174:175]
	s_waitcnt vmcnt(5)
; template <class Epi, class Sched, bool ALIGN_EPI = true, bool SP2 = true>
; __device__ __forceinline__ void gemm_phase(LAS unsigned char* lds, const Dims g, const Sched& S, const Epi& E) {
;     ...
;         if constexpr (ALIGN_EPI) { if (wr == 0) PG8_BAR; }
;         E(acc, cur, wr, wc, fr, fq);
;         if (!has_next) break;
; #pragma unroll
;         for (int a = 0; a < 2; ++a)
; #pragma unroll
;             for (int b = 0; b < 2; ++b)
; #pragma unroll
;                 for (int m = 0; m < 4; ++m)
; #pragma unroll
;     DI void operator()(const f32x4 (&acc)[2][2][4][2], const Unit& u, int wr, int wc, int fr, int fq) const {
;         const int row0 = u.pm * BM + wr * 64 + fr, col0 = u.pn * BM + wc * 32 + 8 * fq;
; #pragma unroll
;         for (int ai = 0; ai < 2; ++ai)
; #pragma unroll
;             for (int m = 0; m < 4; ++m) { const size_t row = (size_t)(row0 + ai * HALF + m * 16);
;                 u32x4 gzs[2], ts[2];
; #pragma unroll
;                 for (int bj = 0; bj < 2; ++bj) { const int col = col0 + bj * HALF; gzs[bj] = *(const u32x4*)(Zg + row * NZ + goff + col); if (add) ts[bj] = *(const u32x4*)(add + row * D + col); else ts[bj] = (u32x4){0u, 0u, 0u, 0u}; }
; #pragma unroll
;                 for (int bj = 0; bj < 2; ++bj) {
;                     const int col = col0 + bj * HALF;
;                     const u32x4 gz = gzs[bj];
;                     float a[8] = {0.f, 0.f, 0.f, 0.f, 0.f, 0.f, 0.f, 0.f};
;                     if (add) { const u32x4 t = ts[bj]; a[0] = bflo(t.x); a[1] = bfhi(t.x); a[2] = bflo(t.y); a[3] = bfhi(t.y); a[4] = bflo(t.z); a[5] = bfhi(t.z); a[6] = bflo(t.w); a[7] = bfhi(t.w); }
;                     const f32x4 v0 = acc[ai][bj][m][0], v1 = acc[ai][bj][m][1];
;                     float o[8];
;                     o[0] = a[0] + sigmoidf_(bflo(gz.x)) * v0[0]; o[1] = a[1] + sigmoidf_(bfhi(gz.x)) * v0[1];
;                     o[2] = a[2] + sigmoidf_(bflo(gz.y)) * v0[2]; o[3] = a[3] + sigmoidf_(bfhi(gz.y)) * v0[3];
;                     o[4] = a[4] + sigmoidf_(bflo(gz.z)) * v1[0]; o[5] = a[5] + sigmoidf_(bfhi(gz.z)) * v1[1];
;                     o[6] = a[6] + sigmoidf_(bflo(gz.w)) * v1[2]; o[7] = a[7] + sigmoidf_(bfhi(gz.w)) * v1[3];
;                     u32x4 w; w.x = pk2(o[0], o[1]); w.y = pk2(o[2], o[3]); w.z = pk2(o[4], o[5]); w.w = pk2(o[6], o[7]);
;                     *(u32x4*)(O + row * D + col) = w; } }
;     }
	v_lshlrev_b32_e32 v208, 16, v244
	v_and_b32_e32 v209, 0xffff0000, v244
	v_lshlrev_b32_e32 v210, 16, v245
	v_and_b32_e32 v211, 0xffff0000, v245
	v_mul_f32_e32 v208, 0xbfb8aa3b, v208
	v_mul_f32_e32 v209, 0xbfb8aa3b, v209
	v_mul_f32_e32 v210, 0xbfb8aa3b, v210
	v_mul_f32_e32 v211, 0xbfb8aa3b, v211
	v_exp_f32_e32 v208, v208
	v_exp_f32_e32 v209, v209
	v_exp_f32_e32 v210, v210
	v_exp_f32_e32 v211, v211
	v_lshlrev_b32_e32 v212, 16, v140
	v_and_b32_e32 v213, 0xffff0000, v140
	v_pk_add_f32 v[208:209], v[208:209], 1.0 op_sel_hi:[1,0]
	v_pk_add_f32 v[210:211], v[210:211], 1.0 op_sel_hi:[1,0]
	v_lshlrev_b32_e32 v214, 16, v141
	v_and_b32_e32 v215, 0xffff0000, v141
	v_rcp_f32_e32 v208, v208
	v_rcp_f32_e32 v209, v209
	v_rcp_f32_e32 v210, v210
	v_rcp_f32_e32 v211, v211
	v_pk_fma_f32 v[208:209], v[14:15], v[208:209], v[212:213]
	v_pk_fma_f32 v[210:211], v[16:17], v[210:211], v[214:215]
	v_cvt_pk_bf16_f32 v244, v208, v209
	v_cvt_pk_bf16_f32 v245, v210, v211
	v_lshlrev_b32_e32 v208, 16, v246
	v_and_b32_e32 v209, 0xffff0000, v246
	v_lshlrev_b32_e32 v210, 16, v247
	v_and_b32_e32 v211, 0xffff0000, v247
	v_mul_f32_e32 v208, 0xbfb8aa3b, v208
	v_mul_f32_e32 v209, 0xbfb8aa3b, v209
	v_mul_f32_e32 v210, 0xbfb8aa3b, v210
	v_mul_f32_e32 v211, 0xbfb8aa3b, v211
	v_exp_f32_e32 v208, v208
	v_exp_f32_e32 v209, v209
	v_exp_f32_e32 v210, v210
	v_exp_f32_e32 v211, v211
	v_lshlrev_b32_e32 v212, 16, v142
	v_and_b32_e32 v213, 0xffff0000, v142
	v_pk_add_f32 v[208:209], v[208:209], 1.0 op_sel_hi:[1,0]
	v_pk_add_f32 v[210:211], v[210:211], 1.0 op_sel_hi:[1,0]
	v_lshlrev_b32_e32 v214, 16, v143
	v_and_b32_e32 v215, 0xffff0000, v143
	v_rcp_f32_e32 v208, v208
	v_rcp_f32_e32 v209, v209
	v_rcp_f32_e32 v210, v210
	v_rcp_f32_e32 v211, v211
	v_pk_fma_f32 v[208:209], v[10:11], v[208:209], v[212:213]
	v_pk_fma_f32 v[210:211], v[12:13], v[210:211], v[214:215]
	v_cvt_pk_bf16_f32 v246, v208, v209
	v_cvt_pk_bf16_f32 v247, v210, v211
	global_store_dwordx4 v[164:165], v[244:247], off
	s_waitcnt vmcnt(5)
	v_lshlrev_b32_e32 v208, 16, v248
	v_and_b32_e32 v209, 0xffff0000, v248
	v_lshlrev_b32_e32 v210, 16, v249
	v_and_b32_e32 v211, 0xffff0000, v249
	v_mul_f32_e32 v208, 0xbfb8aa3b, v208
	v_mul_f32_e32 v209, 0xbfb8aa3b, v209
	v_mul_f32_e32 v210, 0xbfb8aa3b, v210
	v_mul_f32_e32 v211, 0xbfb8aa3b, v211
	v_exp_f32_e32 v208, v208
	v_exp_f32_e32 v209, v209
	v_exp_f32_e32 v210, v210
	v_exp_f32_e32 v211, v211
	v_lshlrev_b32_e32 v212, 16, v144
	v_and_b32_e32 v213, 0xffff0000, v144
	v_pk_add_f32 v[208:209], v[208:209], 1.0 op_sel_hi:[1,0]
	v_pk_add_f32 v[210:211], v[210:211], 1.0 op_sel_hi:[1,0]
	v_lshlrev_b32_e32 v214, 16, v145
	v_and_b32_e32 v215, 0xffff0000, v145
	v_rcp_f32_e32 v208, v208
	v_rcp_f32_e32 v209, v209
	v_rcp_f32_e32 v210, v210
	v_rcp_f32_e32 v211, v211
	v_pk_fma_f32 v[208:209], v[6:7], v[208:209], v[212:213]
	v_pk_fma_f32 v[210:211], v[8:9], v[210:211], v[214:215]
	v_cvt_pk_bf16_f32 v248, v208, v209
	v_cvt_pk_bf16_f32 v249, v210, v211
	v_lshlrev_b32_e32 v208, 16, v250
	v_and_b32_e32 v209, 0xffff0000, v250
	v_lshlrev_b32_e32 v210, 16, v251
	v_and_b32_e32 v211, 0xffff0000, v251
	v_mul_f32_e32 v208, 0xbfb8aa3b, v208
	v_mul_f32_e32 v209, 0xbfb8aa3b, v209
	v_mul_f32_e32 v210, 0xbfb8aa3b, v210
	v_mul_f32_e32 v211, 0xbfb8aa3b, v211
	v_exp_f32_e32 v208, v208
	v_exp_f32_e32 v209, v209
	v_exp_f32_e32 v210, v210
	v_exp_f32_e32 v211, v211
	v_lshlrev_b32_e32 v212, 16, v146
	v_and_b32_e32 v213, 0xffff0000, v146
	v_pk_add_f32 v[208:209], v[208:209], 1.0 op_sel_hi:[1,0]
	v_pk_add_f32 v[210:211], v[210:211], 1.0 op_sel_hi:[1,0]
	v_lshlrev_b32_e32 v214, 16, v147
	v_and_b32_e32 v215, 0xffff0000, v147
	v_rcp_f32_e32 v208, v208
	v_rcp_f32_e32 v209, v209
	v_rcp_f32_e32 v210, v210
	v_rcp_f32_e32 v211, v211
	v_pk_fma_f32 v[208:209], v[2:3], v[208:209], v[212:213]
	v_pk_fma_f32 v[210:211], v[4:5], v[210:211], v[214:215]
	v_cvt_pk_bf16_f32 v250, v208, v209
	v_cvt_pk_bf16_f32 v251, v210, v211
	s_mov_b64 s[2:3], -1
	s_andn2_b64 vcc, exec, s[38:39]
	global_store_dwordx4 v[164:165], v[248:251], off offset:256
	s_cbranch_vccnz .LBB0_1421
	s_andn2_b64 vcc, exec, s[48:49]
	s_cbranch_vccnz .LBB0_1420
	s_barrier
	s_branch .LBB0_1420

; #define GAS __attribute__((address_space(1)))
; #define LAS __attribute__((address_space(3)))
;     ...
;     constexpr int KD = (MODE == 0) ? D : DEXP, NT = KD / 64, NSLAB = (MODE == 0) ? 8 : 16, LDW = (MODE == 0) ? DEXP : D, LDX = KD;
;     const int half = wave & 1, nb16 = lane & 15, kb = 4 * (wave >> 1) + (lane >> 4);
;     const int tk = lane & 15, q = lane >> 4;
;     const GAS char* wmat = (const GAS char*)((MODE == 0) ? (half ? a.inp(I_WEU) : a.inp(I_WEG)) : a.inp(I_WED));
;     const unsigned wvo = (unsigned)((4 * kb * LDW + 4 * nb16) * 4);
;     const int lw0 = (64 * half + 4 * nb16) * 128 + (((kb >> 1) ^ ((2 * nb16) & 7)) << 4) + (kb & 1) * 8, lw1 = lw0 ^ 16;
;     const int rd_g = (tk >> 1) & 7;
;     for (int vb = bid; vb < NEXP * NSLAB; vb += G) {
;         const int xcd = vb & 7, idx = vb >> 3; const int e = xcd * 8 + idx / NSLAB, slab = idx % NSLAB;
;         const int M = __builtin_amdgcn_readfirstlane(lc[LC_CNT / 4 + e]), row0 = __builtin_amdgcn_readfirstlane(lc[LC_PSTART / 4 + e]);
;         const size_t wuo = (MODE == 0) ? ((size_t)(l * NEXP + e) * D * DEXP + slab * 64) * 4 : ((size_t)(l * NEXP + e) * DEXP * D + slab * 128 + 64 * half) * 4;
;         const __amdgpu_buffer_rsrc_t wrs = __builtin_amdgcn_make_buffer_rsrc((void*)(wmat + wuo), 0, KD * LDW * 4, 0x00020000);
;         const __amdgpu_buffer_rsrc_t xrs = __builtin_amdgcn_make_buffer_rsrc((MODE == 0) ? (void*)(ws + WS_U) : (void*)((const GAS char*)(ws + WS_HID) + (size_t)row0 * LDX * 2), 0, 0x7fffffff, 0x00020000);
;         const int* el = (const int*)(ws + WS_ELIST) + (size_t)e * T;
;         for (int rp = 0; rp < M; rp += 384) {
;             unsigned xso[6];
; #pragma unroll
;             for (int i = 0; i < 6; ++i) { int tok = rp + wave * 48 + 8 * i + (lane >> 3); tok = min(tok, M - 1); if (VAR == 5) tok &= 15; if (MODE == 0) tok = el[tok]; xso[i] = (unsigned)(tok * LDX * 2 + (lane & 7) * 16); }
;             LAS unsigned char* xw = lds + MS_XOFF + wave * MS_XWAVE; const int xwo = (lane >> 3) * 128 + (((lane & 7) ^ ((lane >> 4) & 3)) << 4);
;             const LAS unsigned char* xr = lds + MS_XOFF + wave * MS_XWAVE + tk * 128 + ((q ^ rd_g) << 4);
.LBB0_1713:
	s_or_b64 exec, exec, s[12:13]
	s_cmpk_gt_i32 s3, 0x1ff
	s_waitcnt lgkmcnt(0)
	s_barrier
	s_cbranch_scc1 .LBB0_1727
	s_ashr_i32 s12, s0, 6
	s_and_b32 s7, s12, 1
	s_lshl_b32 s0, s12, 1
	v_bfe_u32 v4, v2, 4, 2
	v_and_or_b32 v5, s0, -4, v4
	s_cmp_eq_u32 s7, 0
	s_movk_i32 s0, 0xe8
	s_cselect_b32 s0, s0, 0xf0
	v_and_b32_e32 v3, 15, v2
	s_add_u32 s0, s4, s0
	s_addc_u32 s1, s5, 0
	s_waitcnt vmcnt(0)
	v_lshlrev_b32_e32 v6, 4, v3
	v_lshlrev_b32_e32 v90, 3, v4
	s_load_dwordx2 s[38:39], s[0:1], 0x0
	v_lshl_or_b32 v160, v5, 13, v6
	v_lshlrev_b32_e32 v6, 9, v3
	s_lshl_b32 s0, s7, 13
	v_and_b32_e32 v7, 8, v90
	v_or3_b32 v6, v7, v6, s0
	v_readlane_b32 s0, v255, 30
	s_lshl_b32 s24, s0, 6
	s_add_u32 s4, s8, 0x4300000
	v_lshrrev_b32_e32 v5, 1, v5
	v_lshlrev_b32_e32 v8, 1, v2
	s_addc_u32 s0, s9, 0
	v_bitop3_b32 v5, v5, v8, 6 bitop3:0x78
	s_and_b32 s5, s0, 0xffff
	s_mul_i32 s0, s12, 16
	s_mul_i32 s80, s12, 16
	v_bfe_u32 v8, v2, 3, 3
	v_or_b32_e32 v162, s0, v8
	v_lshlrev_b32_e32 v8, 4, v2
	v_and_b32_e32 v163, 0x70, v8
	v_bitop3_b32 v8, v4, v2, 7 bitop3:0x78
	v_lshl_add_u32 v161, v5, 4, v6
	v_lshrrev_b32_e32 v6, 1, v2
	v_bfe_u32 v7, v2, 1, 3
	s_add_u32 s25, s8, 0x39e61600
	s_mulk_i32 s12, 0x3000
	v_and_or_b32 v2, v2, 56, v8
	v_readlane_b32 s1, v255, 31
	s_addc_u32 s26, s9, 0
	s_add_i32 s27, s12, 0
	v_lshlrev_b32_e32 v172, 4, v2
	v_lshlrev_b32_e32 v2, 7, v3
	v_add_u32_e32 v173, s27, v2
	v_add_u32_e32 v176, 0, v2
	v_or_b32_e32 v177, s0, v3
	v_lshl_add_u64 v[2:3], s[8:9], 0, v[90:91]
	s_mov_b64 s[0:1], 0x2fe31000
	v_xor_b32_e32 v5, 16, v161
	v_bitop3_b32 v6, v6, v4, 7 bitop3:0x6c
	v_bitop3_b32 v4, v4, v7, 4 bitop3:0x36
	v_lshl_add_u64 v[156:157], v[2:3], 0, s[0:1]
	v_xor_b32_e32 v2, 64, v172
	s_mov_b32 s7, s11
	v_lshlrev_b32_e32 v174, 4, v6
	v_lshlrev_b32_e32 v175, 4, v4
	v_or_b32_e32 v90, 0x800, v160
	v_or_b32_e32 v178, 0x1000, v160
	v_or_b32_e32 v179, 0x1800, v160
	v_add_u32_e32 v180, 0, v5
	v_add_u32_e32 v181, s27, v2
	s_branch .LBB0_1716

; #define LAS __attribute__((address_space(3)))
; #define MS_WLOAD(set, t) do { _Pragma("unroll") for (int r_ = 0; r_ < 4; ++r_) wr[set][r_] = __builtin_bit_cast(f32x4, __builtin_amdgcn_raw_buffer_load_b128(wrs, (int)wvo + r_ * LDW * 4, MS_CL(t) * (64 * LDW * 4), 0)); } while (0)
; #define MS_WCOMMIT(set, bufi) do { LAS unsigned char* wb_ = lds + (bufi) * MS_TILE; _Pragma("unroll") for (int i_ = 0; i_ < 4; ++i_) { \
;             u32x2 p_; p_.x = pk2(wr[set][0][i_], wr[set][1][i_]); p_.y = pk2(wr[set][2][i_], wr[set][3][i_]); \
;             *(LAS u32x2*)(wb_ + ((i_ < 2) ? lw0 : lw1) + i_ * 128) = p_; } } while (0)
; #define MS_XSLOAD(t) do { _Pragma("unroll") for (int i_ = 0; i_ < 6; ++i_) xs[i_] = __builtin_bit_cast(bf16x8, __builtin_amdgcn_raw_buffer_load_b128(xrs, (int)xso[i_], MS_CL(t) * 128, 0)); } while (0)
; #define MS_XSWRITE(bufi) do { _Pragma("unroll") for (int i_ = 0; i_ < 6; ++i_) *(LAS bf16x8*)(xw + (bufi) * MS_XBUF + i_ * 1024 + ((i_ & 1) ? (xwo ^ 64) : xwo)) = xs[i_]; } while (0)
;     ...
;         for (int rp = 0; rp < M; rp += 384) {
;             unsigned xso[6];
; #pragma unroll
;             for (int i = 0; i < 6; ++i) { int tok = rp + wave * 48 + 8 * i + (lane >> 3); tok = min(tok, M - 1); if (VAR == 5) tok &= 15; if (MODE == 0) tok = el[tok]; xso[i] = (unsigned)(tok * LDX * 2 + (lane & 7) * 16); }
;             LAS unsigned char* xw = lds + MS_XOFF + wave * MS_XWAVE; const int xwo = (lane >> 3) * 128 + (((lane & 7) ^ ((lane >> 4) & 3)) << 4);
;             const LAS unsigned char* xr = lds + MS_XOFF + wave * MS_XWAVE + tk * 128 + ((q ^ rd_g) << 4);
;             f32x4 acc[3][8];
; #pragma unroll
;             for (int mt = 0; mt < 3; ++mt)
; #pragma unroll
;                 for (int j = 0; j < 8; ++j) acc[mt][j] = (f32x4){0.f, 0.f, 0.f, 0.f};
;             f32x4 wr[2][4];
;             bf16x8 xs[6];
;     ...
;             const LAS unsigned char* xr1 = lds + MS_XOFF + wave * MS_XWAVE + tk * 128 + (((4 + q) ^ rd_g) << 4);
;             __syncthreads();
;             MS_XSLOAD(0); MS_WLOAD(0, 0); MS_WLOAD(1, 1);
;             MS_WCOMMIT(0, 0); MS_WLOAD(0, 2);
;             MS_XSWRITE(0); MS_XSLOAD(1);
;             __syncthreads();
.LBB0_1719:
	v_add_u32_e32 v4, s31, v162
	v_min_i32_e32 v2, s30, v4
	v_ashrrev_i32_e32 v3, 31, v2
	v_lshl_add_u64 v[2:3], v[2:3], 2, s[40:41]
	global_load_dword v182, v[2:3], off
	v_or_b32_e32 v2, 8, v4
	v_min_i32_e32 v2, s30, v2
	v_ashrrev_i32_e32 v3, 31, v2
	v_lshl_add_u64 v[2:3], v[2:3], 2, s[40:41]
	global_load_dword v183, v[2:3], off
	v_add_u32_e32 v2, 0x80, v4
	v_min_i32_e32 v2, s30, v2
	v_ashrrev_i32_e32 v3, 31, v2
	v_lshl_add_u64 v[2:3], v[2:3], 2, s[40:41]
	global_load_dword v184, v[2:3], off
	v_add_u32_e32 v2, 0x88, v4
	v_min_i32_e32 v2, s30, v2
	v_ashrrev_i32_e32 v3, 31, v2
	v_lshl_add_u64 v[2:3], v[2:3], 2, s[40:41]
	global_load_dword v185, v[2:3], off
	v_add_u32_e32 v2, 0x100, v4
	v_min_i32_e32 v2, s30, v2
	v_ashrrev_i32_e32 v3, 31, v2
	v_lshl_add_u64 v[2:3], v[2:3], 2, s[40:41]
	global_load_dword v186, v[2:3], off
	v_add_u32_e32 v2, 0x108, v4
	v_min_i32_e32 v2, s30, v2
	v_ashrrev_i32_e32 v3, 31, v2
	v_lshl_add_u64 v[2:3], v[2:3], 2, s[40:41]
	global_load_dword v187, v[2:3], off
	v_add_u32_e32 v188, 0, v161
	v_add_u32_e32 v189, s27, v172
	s_mov_b32 s0, -2
	s_barrier
	s_waitcnt vmcnt(0)
	v_lshl_or_b32 v182, v182, 12, v163
	v_lshl_or_b32 v183, v183, 12, v163
	v_lshl_or_b32 v184, v184, 12, v163
	v_lshl_or_b32 v185, v185, 12, v163
	v_lshl_or_b32 v186, v186, 12, v163
	v_lshl_or_b32 v187, v187, 12, v163
	buffer_load_dwordx4 v[2:5], v182, s[4:7], 0 offen
	buffer_load_dwordx4 v[6:9], v183, s[4:7], 0 offen
	buffer_load_dwordx4 v[10:13], v184, s[4:7], 0 offen
	buffer_load_dwordx4 v[14:17], v185, s[4:7], 0 offen
	buffer_load_dwordx4 v[18:21], v186, s[4:7], 0 offen
	buffer_load_dwordx4 v[22:25], v187, s[4:7], 0 offen
	buffer_load_dwordx4 v[26:29], v160, s[8:11], 0 offen
	buffer_load_dwordx4 v[30:33], v90, s[8:11], 0 offen
	buffer_load_dwordx4 v[34:37], v178, s[8:11], 0 offen
	buffer_load_dwordx4 v[38:41], v179, s[8:11], 0 offen
	buffer_load_dwordx4 v[74:77], v160, s[8:11], s11 offen
	buffer_load_dwordx4 v[78:81], v90, s[8:11], s11 offen
	buffer_load_dwordx4 v[82:85], v178, s[8:11], s11 offen
	buffer_load_dwordx4 v[86:89], v179, s[8:11], s11 offen
	s_waitcnt vmcnt(6)
	v_cvt_pk_bf16_f32 v42, v26, v30
	v_cvt_pk_bf16_f32 v26, v27, v31
	s_waitcnt vmcnt(4)
	v_cvt_pk_bf16_f32 v43, v34, v38
	v_cvt_pk_bf16_f32 v27, v35, v39
	ds_write2_b64 v188, v[42:43], v[26:27] offset1:16
	v_cvt_pk_bf16_f32 v26, v28, v32
	v_cvt_pk_bf16_f32 v27, v36, v40
	v_cvt_pk_bf16_f32 v28, v29, v33
	v_cvt_pk_bf16_f32 v29, v37, v41
	ds_write2_b64 v180, v[26:27], v[28:29] offset0:32 offset1:48
	buffer_load_dwordx4 v[96:99], v160, s[8:11], s22 offen
	buffer_load_dwordx4 v[100:103], v90, s[8:11], s22 offen
	buffer_load_dwordx4 v[104:107], v178, s[8:11], s22 offen
	buffer_load_dwordx4 v[108:111], v179, s[8:11], s22 offen
	ds_write_b128 v189, v[2:5] offset:32768
	ds_write_b128 v181, v[6:9] offset:33792
	ds_write_b128 v189, v[10:13] offset:34816
	ds_write_b128 v181, v[14:17] offset:35840
	ds_write_b128 v189, v[18:21] offset:36864
	ds_write_b128 v181, v[22:25] offset:37888
	buffer_load_dwordx4 v[132:135], v182, s[4:7], s92 offen
	buffer_load_dwordx4 v[124:127], v183, s[4:7], s92 offen
	buffer_load_dwordx4 v[140:143], v184, s[4:7], s92 offen
	buffer_load_dwordx4 v[144:147], v185, s[4:7], s92 offen
	buffer_load_dwordx4 v[128:131], v186, s[4:7], s92 offen
	buffer_load_dwordx4 v[136:139], v187, s[4:7], s92 offen
	v_mov_b32_e32 v2, 0
	v_mov_b32_e32 v3, v2
	v_mov_b32_e32 v4, v2
	v_mov_b32_e32 v5, v2
	v_mov_b32_e32 v10, v2
	v_mov_b32_e32 v11, v2
	v_mov_b32_e32 v12, v2
	v_mov_b32_e32 v13, v2
	v_mov_b32_e32 v18, v2
	v_mov_b32_e32 v19, v2
	v_mov_b32_e32 v20, v2
	v_mov_b32_e32 v21, v2
	v_mov_b32_e32 v26, v2
	v_mov_b32_e32 v27, v2
	v_mov_b32_e32 v28, v2
	v_mov_b32_e32 v29, v2
	v_mov_b32_e32 v6, v2
	v_mov_b32_e32 v7, v2
	v_mov_b32_e32 v8, v2
	v_mov_b32_e32 v9, v2
	v_mov_b32_e32 v14, v2
	v_mov_b32_e32 v15, v2
	v_mov_b32_e32 v16, v2
	v_mov_b32_e32 v17, v2
	v_mov_b32_e32 v22, v2
	v_mov_b32_e32 v23, v2
	v_mov_b32_e32 v24, v2
	v_mov_b32_e32 v25, v2
	v_mov_b32_e32 v30, v2
	v_mov_b32_e32 v31, v2
	v_mov_b32_e32 v32, v2
	v_mov_b32_e32 v33, v2
	v_mov_b32_e32 v34, v2
	v_mov_b32_e32 v35, v2
	v_mov_b32_e32 v36, v2
	v_mov_b32_e32 v37, v2
	v_mov_b32_e32 v42, v2
	v_mov_b32_e32 v43, v2
	v_mov_b32_e32 v44, v2
	v_mov_b32_e32 v45, v2
	v_mov_b32_e32 v50, v2
	v_mov_b32_e32 v51, v2
	v_mov_b32_e32 v52, v2
	v_mov_b32_e32 v53, v2
	v_mov_b32_e32 v58, v2
	v_mov_b32_e32 v59, v2
	v_mov_b32_e32 v60, v2
	v_mov_b32_e32 v61, v2
	v_mov_b32_e32 v38, v2
	v_mov_b32_e32 v39, v2
	v_mov_b32_e32 v40, v2
	v_mov_b32_e32 v41, v2
	v_mov_b32_e32 v46, v2
	v_mov_b32_e32 v47, v2
	v_mov_b32_e32 v48, v2
	v_mov_b32_e32 v49, v2
	v_mov_b32_e32 v54, v2
	v_mov_b32_e32 v55, v2
	v_mov_b32_e32 v56, v2
	v_mov_b32_e32 v57, v2
	v_mov_b32_e32 v62, v2
	v_mov_b32_e32 v63, v2
	v_mov_b32_e32 v64, v2
	v_mov_b32_e32 v65, v2
	v_mov_b32_e32 v66, v2
	v_mov_b32_e32 v67, v2
	v_mov_b32_e32 v68, v2
	v_mov_b32_e32 v69, v2
	v_mov_b32_e32 v92, v2
	v_mov_b32_e32 v93, v2
	v_mov_b32_e32 v94, v2
	v_mov_b32_e32 v95, v2
	v_mov_b32_e32 v116, v2
	v_mov_b32_e32 v117, v2
	v_mov_b32_e32 v118, v2
	v_mov_b32_e32 v119, v2
	v_mov_b32_e32 v148, v2
	v_mov_b32_e32 v149, v2
	v_mov_b32_e32 v150, v2
	v_mov_b32_e32 v151, v2
	v_mov_b32_e32 v70, v2
	v_mov_b32_e32 v71, v2
	v_mov_b32_e32 v72, v2
	v_mov_b32_e32 v73, v2
	v_mov_b32_e32 v112, v2
	v_mov_b32_e32 v113, v2
	v_mov_b32_e32 v114, v2
	v_mov_b32_e32 v115, v2
	v_mov_b32_e32 v120, v2
	v_mov_b32_e32 v121, v2
	v_mov_b32_e32 v122, v2
	v_mov_b32_e32 v123, v2
	v_mov_b32_e32 v152, v2
	v_mov_b32_e32 v153, v2
	v_mov_b32_e32 v154, v2
	v_mov_b32_e32 v155, v2
	s_waitcnt lgkmcnt(0)
	s_barrier
	s_sub_i32 s81, s28, s31
	s_add_i32 s82, s80, 0x100
	s_cmp_le_i32 s81, s82
	s_cbranch_scc1 .Lmoe_k_b
; #define LAS __attribute__((address_space(3)))
; #define MS_WLOAD(set, t) do { _Pragma("unroll") for (int r_ = 0; r_ < 4; ++r_) wr[set][r_] = __builtin_bit_cast(f32x4, __builtin_amdgcn_raw_buffer_load_b128(wrs, (int)wvo + r_ * LDW * 4, MS_CL(t) * (64 * LDW * 4), 0)); } while (0)
; #define MS_WCOMMIT(set, bufi) do { LAS unsigned char* wb_ = lds + (bufi) * MS_TILE; _Pragma("unroll") for (int i_ = 0; i_ < 4; ++i_) { \
;             u32x2 p_; p_.x = pk2(wr[set][0][i_], wr[set][1][i_]); p_.y = pk2(wr[set][2][i_], wr[set][3][i_]); \
;             *(LAS u32x2*)(wb_ + ((i_ < 2) ? lw0 : lw1) + i_ * 128) = p_; } } while (0)
; #define MS_XSLOAD(t) do { _Pragma("unroll") for (int i_ = 0; i_ < 6; ++i_) xs[i_] = __builtin_bit_cast(bf16x8, __builtin_amdgcn_raw_buffer_load_b128(xrs, (int)xso[i_], MS_CL(t) * 128, 0)); } while (0)
; #define MS_XSWRITE(bufi) do { _Pragma("unroll") for (int i_ = 0; i_ < 6; ++i_) *(LAS bf16x8*)(xw + (bufi) * MS_XBUF + i_ * 1024 + ((i_ & 1) ? (xwo ^ 64) : xwo)) = xs[i_]; } while (0)
; #define MS_STEP(I, J, t) do { MS_WCOMMIT(J, J); MS_WLOAD(J, (t) + 3); MS_COMPUTE(I); MS_XSWRITE(J); MS_XSLOAD((t) + 2); __syncthreads(); } while (0)
;     ...
;             const LAS unsigned char* xr1 = lds + MS_XOFF + wave * MS_XWAVE + tk * 128 + (((4 + q) ^ rd_g) << 4);
;             __syncthreads();
;             MS_XSLOAD(0); MS_WLOAD(0, 0); MS_WLOAD(1, 1);
;             MS_WCOMMIT(0, 0); MS_WLOAD(0, 2);
;             MS_XSWRITE(0); MS_XSLOAD(1);
;             __syncthreads();
; #pragma unroll 1
;             for (int t = 0; t < NT; t += 2) { MS_STEP(0, 1, t); MS_STEP(1, 0, t + 1); }
.LBB0_1720:
	s_add_i32 s0, s0, 2
	s_min_u32 s1, s0, 28
	s_lshl_b32 s12, s1, 17
	s_add_i32 s12, s12, 0x60000
	s_waitcnt vmcnt(12)
	v_cvt_pk_bf16_f32 v164, v74, v78
	s_waitcnt vmcnt(10)
	v_cvt_pk_bf16_f32 v165, v82, v86
	v_cvt_pk_bf16_f32 v166, v75, v79
	v_cvt_pk_bf16_f32 v167, v83, v87
	v_cvt_pk_bf16_f32 v190, v76, v80
	v_cvt_pk_bf16_f32 v191, v84, v88
	v_cvt_pk_bf16_f32 v192, v77, v81
	v_cvt_pk_bf16_f32 v193, v85, v89
	buffer_load_dwordx4 v[74:77], v160, s[8:11], s12 offen
	buffer_load_dwordx4 v[78:81], v90, s[8:11], s12 offen
	buffer_load_dwordx4 v[82:85], v178, s[8:11], s12 offen
	buffer_load_dwordx4 v[86:89], v179, s[8:11], s12 offen
	v_add_u32_e32 v194, 0x4000, v188
	v_add_u32_e32 v195, 0x4000, v180
	v_add_u32_e32 v214, v173, v174
	ds_write2_b64 v194, v[164:165], v[166:167] offset1:16
	ds_write2_b64 v195, v[190:191], v[192:193] offset0:32 offset1:48
	v_add_u32_e32 v215, v176, v174
	ds_read_b128 v[164:167], v214 offset:32768
	ds_read_b128 v[190:193], v214 offset:34816
	ds_read_b128 v[194:197], v214 offset:36864
	ds_read_b128 v[198:201], v215
	ds_read_b128 v[202:205], v215 offset:2048
	ds_read_b128 v[206:209], v215 offset:4096
	ds_read_b128 v[210:213], v215 offset:6144
	s_waitcnt lgkmcnt(3)
	v_mfma_f32_16x16x32_bf16 v[152:155], v[198:201], v[164:167], v[152:155]
	v_mfma_f32_16x16x32_bf16 v[62:65], v[198:201], v[190:193], v[62:65]
	v_mfma_f32_16x16x32_bf16 v[30:33], v[198:201], v[194:197], v[30:33]
	s_waitcnt lgkmcnt(2)
	v_mfma_f32_16x16x32_bf16 v[120:123], v[202:205], v[164:167], v[120:123]
	v_mfma_f32_16x16x32_bf16 v[54:57], v[202:205], v[190:193], v[54:57]
	v_mfma_f32_16x16x32_bf16 v[22:25], v[202:205], v[194:197], v[22:25]
	s_waitcnt lgkmcnt(1)
	v_mfma_f32_16x16x32_bf16 v[112:115], v[206:209], v[164:167], v[112:115]
	v_mfma_f32_16x16x32_bf16 v[46:49], v[206:209], v[190:193], v[46:49]
	v_mfma_f32_16x16x32_bf16 v[14:17], v[206:209], v[194:197], v[14:17]
	s_waitcnt lgkmcnt(0)
	v_mfma_f32_16x16x32_bf16 v[70:73], v[210:213], v[164:167], v[70:73]
	v_mfma_f32_16x16x32_bf16 v[38:41], v[210:213], v[190:193], v[38:41]
	v_mfma_f32_16x16x32_bf16 v[6:9], v[210:213], v[194:197], v[6:9]
	ds_read_b128 v[198:201], v215 offset:8192
	ds_read_b128 v[202:205], v215 offset:10240
	ds_read_b128 v[206:209], v215 offset:12288
	ds_read_b128 v[210:213], v215 offset:14336
	s_waitcnt lgkmcnt(3)
	v_mfma_f32_16x16x32_bf16 v[148:151], v[198:201], v[164:167], v[148:151]
	v_mfma_f32_16x16x32_bf16 v[58:61], v[198:201], v[190:193], v[58:61]
	v_mfma_f32_16x16x32_bf16 v[26:29], v[198:201], v[194:197], v[26:29]
	s_waitcnt lgkmcnt(2)
	v_mfma_f32_16x16x32_bf16 v[116:119], v[202:205], v[164:167], v[116:119]
	v_mfma_f32_16x16x32_bf16 v[50:53], v[202:205], v[190:193], v[50:53]
	v_mfma_f32_16x16x32_bf16 v[18:21], v[202:205], v[194:197], v[18:21]
	s_waitcnt lgkmcnt(1)
	v_mfma_f32_16x16x32_bf16 v[92:95], v[206:209], v[164:167], v[92:95]
	v_mfma_f32_16x16x32_bf16 v[42:45], v[206:209], v[190:193], v[42:45]
	v_mfma_f32_16x16x32_bf16 v[10:13], v[206:209], v[194:197], v[10:13]
	s_waitcnt lgkmcnt(0)
	v_mfma_f32_16x16x32_bf16 v[66:69], v[210:213], v[164:167], v[66:69]
	v_mfma_f32_16x16x32_bf16 v[34:37], v[210:213], v[190:193], v[34:37]
	v_mfma_f32_16x16x32_bf16 v[2:5], v[210:213], v[194:197], v[2:5]
	v_add_u32_e32 v216, v173, v175
	ds_read_b128 v[164:167], v216 offset:32768
	ds_read_b128 v[190:193], v216 offset:34816
	v_add_u32_e32 v217, v176, v175
	ds_read_b128 v[194:197], v216 offset:36864
	ds_read_b128 v[198:201], v217
	ds_read_b128 v[202:205], v217 offset:2048
	ds_read_b128 v[206:209], v217 offset:4096
	ds_read_b128 v[210:213], v217 offset:6144
	s_waitcnt lgkmcnt(3)
	v_mfma_f32_16x16x32_bf16 v[152:155], v[198:201], v[164:167], v[152:155]
	v_mfma_f32_16x16x32_bf16 v[62:65], v[198:201], v[190:193], v[62:65]
	v_mfma_f32_16x16x32_bf16 v[30:33], v[198:201], v[194:197], v[30:33]
	s_waitcnt lgkmcnt(2)
	v_mfma_f32_16x16x32_bf16 v[120:123], v[202:205], v[164:167], v[120:123]
	v_mfma_f32_16x16x32_bf16 v[54:57], v[202:205], v[190:193], v[54:57]
	v_mfma_f32_16x16x32_bf16 v[22:25], v[202:205], v[194:197], v[22:25]
	s_waitcnt lgkmcnt(1)
	v_mfma_f32_16x16x32_bf16 v[112:115], v[206:209], v[164:167], v[112:115]
	v_mfma_f32_16x16x32_bf16 v[46:49], v[206:209], v[190:193], v[46:49]
	v_mfma_f32_16x16x32_bf16 v[14:17], v[206:209], v[194:197], v[14:17]
	s_waitcnt lgkmcnt(0)
	v_mfma_f32_16x16x32_bf16 v[70:73], v[210:213], v[164:167], v[70:73]
	v_mfma_f32_16x16x32_bf16 v[38:41], v[210:213], v[190:193], v[38:41]
	v_mfma_f32_16x16x32_bf16 v[6:9], v[210:213], v[194:197], v[6:9]
	ds_read_b128 v[198:201], v217 offset:8192
	ds_read_b128 v[202:205], v217 offset:10240
	ds_read_b128 v[206:209], v217 offset:12288
	ds_read_b128 v[210:213], v217 offset:14336
	s_min_u32 s12, s0, 29
	s_lshl_b32 s12, s12, 7
	s_waitcnt vmcnt(9)
	ds_write_b128 v189, v[132:135] offset:38912
	s_waitcnt vmcnt(8)
	ds_write_b128 v181, v[124:127] offset:39936
	s_waitcnt vmcnt(7)
	ds_write_b128 v189, v[140:143] offset:40960
	s_waitcnt vmcnt(6)
	ds_write_b128 v181, v[144:147] offset:41984
	s_waitcnt vmcnt(5)
	ds_write_b128 v189, v[128:131] offset:43008
	s_waitcnt vmcnt(4)
	ds_write_b128 v181, v[136:139] offset:44032
	s_addk_i32 s12, 0x100
	s_waitcnt lgkmcnt(9)
	v_mfma_f32_16x16x32_bf16 v[148:151], v[198:201], v[164:167], v[148:151]
	buffer_load_dwordx4 v[124:127], v182, s[4:7], s12 offen
	buffer_load_dwordx4 v[128:131], v183, s[4:7], s12 offen
	buffer_load_dwordx4 v[132:135], v184, s[4:7], s12 offen
	buffer_load_dwordx4 v[136:139], v185, s[4:7], s12 offen
	buffer_load_dwordx4 v[140:143], v186, s[4:7], s12 offen
	buffer_load_dwordx4 v[144:147], v187, s[4:7], s12 offen
	s_min_u32 s12, s0, 27
	s_waitcnt lgkmcnt(0)
	v_mfma_f32_16x16x32_bf16 v[116:119], v[202:205], v[164:167], v[116:119]
	s_barrier
; #define LAS __attribute__((address_space(3)))
; #define MS_WLOAD(set, t) do { _Pragma("unroll") for (int r_ = 0; r_ < 4; ++r_) wr[set][r_] = __builtin_bit_cast(f32x4, __builtin_amdgcn_raw_buffer_load_b128(wrs, (int)wvo + r_ * LDW * 4, MS_CL(t) * (64 * LDW * 4), 0)); } while (0)
; #define MS_WCOMMIT(set, bufi) do { LAS unsigned char* wb_ = lds + (bufi) * MS_TILE; _Pragma("unroll") for (int i_ = 0; i_ < 4; ++i_) { \
;             u32x2 p_; p_.x = pk2(wr[set][0][i_], wr[set][1][i_]); p_.y = pk2(wr[set][2][i_], wr[set][3][i_]); \
;             *(LAS u32x2*)(wb_ + ((i_ < 2) ? lw0 : lw1) + i_ * 128) = p_; } } while (0)
; #define MS_XSLOAD(t) do { _Pragma("unroll") for (int i_ = 0; i_ < 6; ++i_) xs[i_] = __builtin_bit_cast(bf16x8, __builtin_amdgcn_raw_buffer_load_b128(xrs, (int)xso[i_], MS_CL(t) * 128, 0)); } while (0)
; #define MS_XSWRITE(bufi) do { _Pragma("unroll") for (int i_ = 0; i_ < 6; ++i_) *(LAS bf16x8*)(xw + (bufi) * MS_XBUF + i_ * 1024 + ((i_ & 1) ? (xwo ^ 64) : xwo)) = xs[i_]; } while (0)
; #define MS_STEP(I, J, t) do { MS_WCOMMIT(J, J); MS_WLOAD(J, (t) + 3); MS_COMPUTE(I); MS_XSWRITE(J); MS_XSLOAD((t) + 2); __syncthreads(); } while (0)
;     ...
;             const LAS unsigned char* xr1 = lds + MS_XOFF + wave * MS_XWAVE + tk * 128 + (((4 + q) ^ rd_g) << 4);
;             __syncthreads();
;             MS_XSLOAD(0); MS_WLOAD(0, 0); MS_WLOAD(1, 1);
;             MS_WCOMMIT(0, 0); MS_WLOAD(0, 2);
;             MS_XSWRITE(0); MS_XSLOAD(1);
;             __syncthreads();
; #pragma unroll 1
;             for (int t = 0; t < NT; t += 2) { MS_STEP(0, 1, t); MS_STEP(1, 0, t + 1); }
	s_lshl_b32 s12, s12, 17
	v_mfma_f32_16x16x32_bf16 v[92:95], v[206:209], v[164:167], v[92:95]
	s_add_i32 s12, s12, 0x80000
	v_mfma_f32_16x16x32_bf16 v[66:69], v[210:213], v[164:167], v[66:69]
	v_cvt_pk_bf16_f32 v164, v96, v100
	v_cvt_pk_bf16_f32 v165, v104, v108
	v_cvt_pk_bf16_f32 v96, v97, v101
	v_cvt_pk_bf16_f32 v97, v105, v109
	ds_write2_b64 v188, v[164:165], v[96:97] offset1:16
	v_cvt_pk_bf16_f32 v96, v98, v102
	v_cvt_pk_bf16_f32 v97, v106, v110
	v_cvt_pk_bf16_f32 v98, v99, v103
	v_cvt_pk_bf16_f32 v99, v107, v111
	ds_write2_b64 v180, v[96:97], v[98:99] offset0:32 offset1:48
	buffer_load_dwordx4 v[96:99], v160, s[8:11], s12 offen
	buffer_load_dwordx4 v[100:103], v90, s[8:11], s12 offen
	buffer_load_dwordx4 v[104:107], v178, s[8:11], s12 offen
	buffer_load_dwordx4 v[108:111], v179, s[8:11], s12 offen
	v_mfma_f32_16x16x32_bf16 v[58:61], v[198:201], v[190:193], v[58:61]
	v_mfma_f32_16x16x32_bf16 v[26:29], v[198:201], v[194:197], v[26:29]
	v_mfma_f32_16x16x32_bf16 v[50:53], v[202:205], v[190:193], v[50:53]
	v_mfma_f32_16x16x32_bf16 v[18:21], v[202:205], v[194:197], v[18:21]
	v_mfma_f32_16x16x32_bf16 v[42:45], v[206:209], v[190:193], v[42:45]
	v_mfma_f32_16x16x32_bf16 v[10:13], v[206:209], v[194:197], v[10:13]
	v_mfma_f32_16x16x32_bf16 v[34:37], v[210:213], v[190:193], v[34:37]
	v_mfma_f32_16x16x32_bf16 v[2:5], v[210:213], v[194:197], v[2:5]
	ds_read_b128 v[164:167], v214 offset:38912
	ds_read_b128 v[190:193], v214 offset:40960
	ds_read_b128 v[194:197], v214 offset:43008
	ds_read_b128 v[198:201], v215 offset:16384
	ds_read_b128 v[202:205], v215 offset:18432
	ds_read_b128 v[206:209], v215 offset:20480
	ds_read_b128 v[210:213], v215 offset:22528
	s_waitcnt lgkmcnt(3)
	v_mfma_f32_16x16x32_bf16 v[152:155], v[198:201], v[164:167], v[152:155]
	v_mfma_f32_16x16x32_bf16 v[62:65], v[198:201], v[190:193], v[62:65]
	v_mfma_f32_16x16x32_bf16 v[30:33], v[198:201], v[194:197], v[30:33]
	s_waitcnt lgkmcnt(2)
	v_mfma_f32_16x16x32_bf16 v[120:123], v[202:205], v[164:167], v[120:123]
	v_mfma_f32_16x16x32_bf16 v[54:57], v[202:205], v[190:193], v[54:57]
	v_mfma_f32_16x16x32_bf16 v[22:25], v[202:205], v[194:197], v[22:25]
	s_waitcnt lgkmcnt(1)
	v_mfma_f32_16x16x32_bf16 v[112:115], v[206:209], v[164:167], v[112:115]
	v_mfma_f32_16x16x32_bf16 v[46:49], v[206:209], v[190:193], v[46:49]
	v_mfma_f32_16x16x32_bf16 v[14:17], v[206:209], v[194:197], v[14:17]
	s_waitcnt lgkmcnt(0)
	v_mfma_f32_16x16x32_bf16 v[70:73], v[210:213], v[164:167], v[70:73]
	v_mfma_f32_16x16x32_bf16 v[38:41], v[210:213], v[190:193], v[38:41]
	v_mfma_f32_16x16x32_bf16 v[6:9], v[210:213], v[194:197], v[6:9]
	ds_read_b128 v[198:201], v215 offset:24576
	ds_read_b128 v[202:205], v215 offset:26624
	ds_read_b128 v[206:209], v215 offset:28672
	ds_read_b128 v[210:213], v215 offset:30720
	s_waitcnt lgkmcnt(3)
	v_mfma_f32_16x16x32_bf16 v[148:151], v[198:201], v[164:167], v[148:151]
	v_mfma_f32_16x16x32_bf16 v[58:61], v[198:201], v[190:193], v[58:61]
	v_mfma_f32_16x16x32_bf16 v[26:29], v[198:201], v[194:197], v[26:29]
	s_waitcnt lgkmcnt(2)
	v_mfma_f32_16x16x32_bf16 v[116:119], v[202:205], v[164:167], v[116:119]
	v_mfma_f32_16x16x32_bf16 v[50:53], v[202:205], v[190:193], v[50:53]
	v_mfma_f32_16x16x32_bf16 v[18:21], v[202:205], v[194:197], v[18:21]
	s_waitcnt lgkmcnt(1)
	v_mfma_f32_16x16x32_bf16 v[92:95], v[206:209], v[164:167], v[92:95]
	v_mfma_f32_16x16x32_bf16 v[42:45], v[206:209], v[190:193], v[42:45]
	v_mfma_f32_16x16x32_bf16 v[10:13], v[206:209], v[194:197], v[10:13]
	s_waitcnt lgkmcnt(0)
	v_mfma_f32_16x16x32_bf16 v[66:69], v[210:213], v[164:167], v[66:69]
	v_mfma_f32_16x16x32_bf16 v[34:37], v[210:213], v[190:193], v[34:37]
	v_mfma_f32_16x16x32_bf16 v[2:5], v[210:213], v[194:197], v[2:5]
	ds_read_b128 v[164:167], v216 offset:38912
	ds_read_b128 v[190:193], v216 offset:40960
	ds_read_b128 v[194:197], v216 offset:43008
	ds_read_b128 v[198:201], v217 offset:16384
	ds_read_b128 v[202:205], v217 offset:18432
	ds_read_b128 v[206:209], v217 offset:20480
	ds_read_b128 v[210:213], v217 offset:22528
	s_waitcnt lgkmcnt(3)
	v_mfma_f32_16x16x32_bf16 v[152:155], v[198:201], v[164:167], v[152:155]
	v_mfma_f32_16x16x32_bf16 v[62:65], v[198:201], v[190:193], v[62:65]
	v_mfma_f32_16x16x32_bf16 v[30:33], v[198:201], v[194:197], v[30:33]
	s_waitcnt lgkmcnt(2)
	v_mfma_f32_16x16x32_bf16 v[120:123], v[202:205], v[164:167], v[120:123]
	v_mfma_f32_16x16x32_bf16 v[54:57], v[202:205], v[190:193], v[54:57]
	v_mfma_f32_16x16x32_bf16 v[22:25], v[202:205], v[194:197], v[22:25]
	s_waitcnt lgkmcnt(1)
	v_mfma_f32_16x16x32_bf16 v[112:115], v[206:209], v[164:167], v[112:115]
	v_mfma_f32_16x16x32_bf16 v[46:49], v[206:209], v[190:193], v[46:49]
	v_mfma_f32_16x16x32_bf16 v[14:17], v[206:209], v[194:197], v[14:17]
	s_waitcnt lgkmcnt(0)
	v_mfma_f32_16x16x32_bf16 v[70:73], v[210:213], v[164:167], v[70:73]
	v_mfma_f32_16x16x32_bf16 v[38:41], v[210:213], v[190:193], v[38:41]
	v_mfma_f32_16x16x32_bf16 v[6:9], v[210:213], v[194:197], v[6:9]
	ds_read_b128 v[198:201], v217 offset:24576
	ds_read_b128 v[202:205], v217 offset:26624
	ds_read_b128 v[206:209], v217 offset:28672
	ds_read_b128 v[210:213], v217 offset:30720
	s_lshl_b32 s1, s1, 7
	s_waitcnt vmcnt(9)
	ds_write_b128 v189, v[124:127] offset:32768
	s_waitcnt vmcnt(8)
	ds_write_b128 v181, v[128:131] offset:33792
	s_waitcnt vmcnt(7)
	ds_write_b128 v189, v[132:135] offset:34816
	s_waitcnt vmcnt(6)
	ds_write_b128 v181, v[136:139] offset:35840
	s_waitcnt vmcnt(5)
	ds_write_b128 v189, v[140:143] offset:36864
	s_waitcnt vmcnt(4)
	ds_write_b128 v181, v[144:147] offset:37888
	s_addk_i32 s1, 0x180
	buffer_load_dwordx4 v[132:135], v182, s[4:7], s1 offen
	buffer_load_dwordx4 v[124:127], v183, s[4:7], s1 offen
	buffer_load_dwordx4 v[140:143], v184, s[4:7], s1 offen
	buffer_load_dwordx4 v[144:147], v185, s[4:7], s1 offen
	buffer_load_dwordx4 v[128:131], v186, s[4:7], s1 offen
	buffer_load_dwordx4 v[136:139], v187, s[4:7], s1 offen
	s_waitcnt lgkmcnt(9)
	v_mfma_f32_16x16x32_bf16 v[148:151], v[198:201], v[164:167], v[148:151]
	s_cmp_gt_u32 s0, 29
	s_waitcnt lgkmcnt(0)
	s_barrier
	v_mfma_f32_16x16x32_bf16 v[58:61], v[198:201], v[190:193], v[58:61]
	v_mfma_f32_16x16x32_bf16 v[26:29], v[198:201], v[194:197], v[26:29]
	v_mfma_f32_16x16x32_bf16 v[116:119], v[202:205], v[164:167], v[116:119]
	v_mfma_f32_16x16x32_bf16 v[50:53], v[202:205], v[190:193], v[50:53]
	v_mfma_f32_16x16x32_bf16 v[18:21], v[202:205], v[194:197], v[18:21]
	v_mfma_f32_16x16x32_bf16 v[92:95], v[206:209], v[164:167], v[92:95]
	v_mfma_f32_16x16x32_bf16 v[42:45], v[206:209], v[190:193], v[42:45]
	v_mfma_f32_16x16x32_bf16 v[10:13], v[206:209], v[194:197], v[10:13]
	v_mfma_f32_16x16x32_bf16 v[66:69], v[210:213], v[164:167], v[66:69]
	v_mfma_f32_16x16x32_bf16 v[34:37], v[210:213], v[190:193], v[34:37]
	v_mfma_f32_16x16x32_bf16 v[2:5], v[210:213], v[194:197], v[2:5]
	s_cbranch_scc0 .LBB0_1720
	s_branch .Lmoe_k_done
; #define LAS __attribute__((address_space(3)))
; #define MS_WLOAD(set, t) do { _Pragma("unroll") for (int r_ = 0; r_ < 4; ++r_) wr[set][r_] = __builtin_bit_cast(f32x4, __builtin_amdgcn_raw_buffer_load_b128(wrs, (int)wvo + r_ * LDW * 4, MS_CL(t) * (64 * LDW * 4), 0)); } while (0)
; #define MS_WCOMMIT(set, bufi) do { LAS unsigned char* wb_ = lds + (bufi) * MS_TILE; _Pragma("unroll") for (int i_ = 0; i_ < 4; ++i_) { \
;             u32x2 p_; p_.x = pk2(wr[set][0][i_], wr[set][1][i_]); p_.y = pk2(wr[set][2][i_], wr[set][3][i_]); \
;             *(LAS u32x2*)(wb_ + ((i_ < 2) ? lw0 : lw1) + i_ * 128) = p_; } } while (0)
; #define MS_XSLOAD(t) do { _Pragma("unroll") for (int i_ = 0; i_ < 6; ++i_) xs[i_] = __builtin_bit_cast(bf16x8, __builtin_amdgcn_raw_buffer_load_b128(xrs, (int)xso[i_], MS_CL(t) * 128, 0)); } while (0)
; #define MS_XSWRITE(bufi) do { _Pragma("unroll") for (int i_ = 0; i_ < 6; ++i_) *(LAS bf16x8*)(xw + (bufi) * MS_XBUF + i_ * 1024 + ((i_ & 1) ? (xwo ^ 64) : xwo)) = xs[i_]; } while (0)
; #define MS_STEP(I, J, t) do { MS_WCOMMIT(J, J); MS_WLOAD(J, (t) + 3); MS_COMPUTE(I); MS_XSWRITE(J); MS_XSLOAD((t) + 2); __syncthreads(); } while (0)
;     ...
;             const LAS unsigned char* xr1 = lds + MS_XOFF + wave * MS_XWAVE + tk * 128 + (((4 + q) ^ rd_g) << 4);
;             __syncthreads();
;             MS_XSLOAD(0); MS_WLOAD(0, 0); MS_WLOAD(1, 1);
;             MS_WCOMMIT(0, 0); MS_WLOAD(0, 2);
;             MS_XSWRITE(0); MS_XSLOAD(1);
;             __syncthreads();
; #pragma unroll 1
;             for (int t = 0; t < NT; t += 2) { MS_STEP(0, 1, t); MS_STEP(1, 0, t + 1); }
.Lmoe_k_b:
	s_add_i32 s0, s0, 2
	s_min_u32 s1, s0, 28
	s_lshl_b32 s12, s1, 17
	s_add_i32 s12, s12, 0x60000
	s_waitcnt vmcnt(12)
	v_cvt_pk_bf16_f32 v164, v74, v78
	s_waitcnt vmcnt(10)
	v_cvt_pk_bf16_f32 v165, v82, v86
	v_cvt_pk_bf16_f32 v166, v75, v79
	v_cvt_pk_bf16_f32 v167, v83, v87
	v_cvt_pk_bf16_f32 v190, v76, v80
	v_cvt_pk_bf16_f32 v191, v84, v88
	v_cvt_pk_bf16_f32 v192, v77, v81
	v_cvt_pk_bf16_f32 v193, v85, v89
	buffer_load_dwordx4 v[74:77], v160, s[8:11], s12 offen
	buffer_load_dwordx4 v[78:81], v90, s[8:11], s12 offen
	buffer_load_dwordx4 v[82:85], v178, s[8:11], s12 offen
	buffer_load_dwordx4 v[86:89], v179, s[8:11], s12 offen
	v_add_u32_e32 v194, 0x4000, v188
	v_add_u32_e32 v195, 0x4000, v180
	v_add_u32_e32 v214, v173, v174
	ds_write2_b64 v194, v[164:165], v[166:167] offset1:16
	ds_write2_b64 v195, v[190:191], v[192:193] offset0:32 offset1:48
	v_add_u32_e32 v215, v176, v174
	ds_read_b128 v[164:167], v214 offset:32768
	ds_read_b128 v[190:193], v214 offset:34816
	ds_read_b128 v[198:201], v215
	ds_read_b128 v[202:205], v215 offset:2048
	ds_read_b128 v[206:209], v215 offset:4096
	ds_read_b128 v[210:213], v215 offset:6144
	s_waitcnt lgkmcnt(3)
	v_mfma_f32_16x16x32_bf16 v[152:155], v[198:201], v[164:167], v[152:155]
	v_mfma_f32_16x16x32_bf16 v[62:65], v[198:201], v[190:193], v[62:65]
	s_waitcnt lgkmcnt(2)
	v_mfma_f32_16x16x32_bf16 v[120:123], v[202:205], v[164:167], v[120:123]
	v_mfma_f32_16x16x32_bf16 v[54:57], v[202:205], v[190:193], v[54:57]
	s_waitcnt lgkmcnt(1)
	v_mfma_f32_16x16x32_bf16 v[112:115], v[206:209], v[164:167], v[112:115]
	v_mfma_f32_16x16x32_bf16 v[46:49], v[206:209], v[190:193], v[46:49]
	s_waitcnt lgkmcnt(0)
	v_mfma_f32_16x16x32_bf16 v[70:73], v[210:213], v[164:167], v[70:73]
	v_mfma_f32_16x16x32_bf16 v[38:41], v[210:213], v[190:193], v[38:41]
	ds_read_b128 v[198:201], v215 offset:8192
	ds_read_b128 v[202:205], v215 offset:10240
	ds_read_b128 v[206:209], v215 offset:12288
	ds_read_b128 v[210:213], v215 offset:14336
	s_waitcnt lgkmcnt(3)
	v_mfma_f32_16x16x32_bf16 v[148:151], v[198:201], v[164:167], v[148:151]
	v_mfma_f32_16x16x32_bf16 v[58:61], v[198:201], v[190:193], v[58:61]
	s_waitcnt lgkmcnt(2)
	v_mfma_f32_16x16x32_bf16 v[116:119], v[202:205], v[164:167], v[116:119]
	v_mfma_f32_16x16x32_bf16 v[50:53], v[202:205], v[190:193], v[50:53]
	s_waitcnt lgkmcnt(1)
	v_mfma_f32_16x16x32_bf16 v[92:95], v[206:209], v[164:167], v[92:95]
	v_mfma_f32_16x16x32_bf16 v[42:45], v[206:209], v[190:193], v[42:45]
	s_waitcnt lgkmcnt(0)
	v_mfma_f32_16x16x32_bf16 v[66:69], v[210:213], v[164:167], v[66:69]
	v_mfma_f32_16x16x32_bf16 v[34:37], v[210:213], v[190:193], v[34:37]
	v_add_u32_e32 v216, v173, v175
	ds_read_b128 v[164:167], v216 offset:32768
	ds_read_b128 v[190:193], v216 offset:34816
	v_add_u32_e32 v217, v176, v175
	ds_read_b128 v[198:201], v217
	ds_read_b128 v[202:205], v217 offset:2048
	ds_read_b128 v[206:209], v217 offset:4096
	ds_read_b128 v[210:213], v217 offset:6144
	s_waitcnt lgkmcnt(3)
	v_mfma_f32_16x16x32_bf16 v[152:155], v[198:201], v[164:167], v[152:155]
	v_mfma_f32_16x16x32_bf16 v[62:65], v[198:201], v[190:193], v[62:65]
	s_waitcnt lgkmcnt(2)
	v_mfma_f32_16x16x32_bf16 v[120:123], v[202:205], v[164:167], v[120:123]
	v_mfma_f32_16x16x32_bf16 v[54:57], v[202:205], v[190:193], v[54:57]
	s_waitcnt lgkmcnt(1)
	v_mfma_f32_16x16x32_bf16 v[112:115], v[206:209], v[164:167], v[112:115]
	v_mfma_f32_16x16x32_bf16 v[46:49], v[206:209], v[190:193], v[46:49]
	s_waitcnt lgkmcnt(0)
	v_mfma_f32_16x16x32_bf16 v[70:73], v[210:213], v[164:167], v[70:73]
	v_mfma_f32_16x16x32_bf16 v[38:41], v[210:213], v[190:193], v[38:41]
	ds_read_b128 v[198:201], v217 offset:8192
	ds_read_b128 v[202:205], v217 offset:10240
	ds_read_b128 v[206:209], v217 offset:12288
	ds_read_b128 v[210:213], v217 offset:14336
	s_min_u32 s12, s0, 29
	s_lshl_b32 s12, s12, 7
	s_waitcnt vmcnt(9)
	ds_write_b128 v189, v[132:135] offset:38912
	s_waitcnt vmcnt(8)
	ds_write_b128 v181, v[124:127] offset:39936
	s_waitcnt vmcnt(7)
	ds_write_b128 v189, v[140:143] offset:40960
	s_waitcnt vmcnt(6)
	ds_write_b128 v181, v[144:147] offset:41984
	s_waitcnt vmcnt(5)
	ds_write_b128 v189, v[128:131] offset:43008
	s_waitcnt vmcnt(4)
	ds_write_b128 v181, v[136:139] offset:44032
	s_addk_i32 s12, 0x100
	s_waitcnt lgkmcnt(9)
	v_mfma_f32_16x16x32_bf16 v[148:151], v[198:201], v[164:167], v[148:151]
	buffer_load_dwordx4 v[124:127], v182, s[4:7], s12 offen
	buffer_load_dwordx4 v[128:131], v183, s[4:7], s12 offen
	buffer_load_dwordx4 v[132:135], v184, s[4:7], s12 offen
	buffer_load_dwordx4 v[136:139], v185, s[4:7], s12 offen
	buffer_load_dwordx4 v[140:143], v186, s[4:7], s12 offen
	buffer_load_dwordx4 v[144:147], v187, s[4:7], s12 offen
	s_min_u32 s12, s0, 27
	s_waitcnt lgkmcnt(0)
	v_mfma_f32_16x16x32_bf16 v[116:119], v[202:205], v[164:167], v[116:119]
	s_barrier
; #define LAS __attribute__((address_space(3)))
; #define MS_WLOAD(set, t) do { _Pragma("unroll") for (int r_ = 0; r_ < 4; ++r_) wr[set][r_] = __builtin_bit_cast(f32x4, __builtin_amdgcn_raw_buffer_load_b128(wrs, (int)wvo + r_ * LDW * 4, MS_CL(t) * (64 * LDW * 4), 0)); } while (0)
; #define MS_WCOMMIT(set, bufi) do { LAS unsigned char* wb_ = lds + (bufi) * MS_TILE; _Pragma("unroll") for (int i_ = 0; i_ < 4; ++i_) { \
;             u32x2 p_; p_.x = pk2(wr[set][0][i_], wr[set][1][i_]); p_.y = pk2(wr[set][2][i_], wr[set][3][i_]); \
;             *(LAS u32x2*)(wb_ + ((i_ < 2) ? lw0 : lw1) + i_ * 128) = p_; } } while (0)
; #define MS_XSLOAD(t) do { _Pragma("unroll") for (int i_ = 0; i_ < 6; ++i_) xs[i_] = __builtin_bit_cast(bf16x8, __builtin_amdgcn_raw_buffer_load_b128(xrs, (int)xso[i_], MS_CL(t) * 128, 0)); } while (0)
; #define MS_XSWRITE(bufi) do { _Pragma("unroll") for (int i_ = 0; i_ < 6; ++i_) *(LAS bf16x8*)(xw + (bufi) * MS_XBUF + i_ * 1024 + ((i_ & 1) ? (xwo ^ 64) : xwo)) = xs[i_]; } while (0)
; #define MS_STEP(I, J, t) do { MS_WCOMMIT(J, J); MS_WLOAD(J, (t) + 3); MS_COMPUTE(I); MS_XSWRITE(J); MS_XSLOAD((t) + 2); __syncthreads(); } while (0)
;     ...
;             const LAS unsigned char* xr1 = lds + MS_XOFF + wave * MS_XWAVE + tk * 128 + (((4 + q) ^ rd_g) << 4);
;             __syncthreads();
;             MS_XSLOAD(0); MS_WLOAD(0, 0); MS_WLOAD(1, 1);
;             MS_WCOMMIT(0, 0); MS_WLOAD(0, 2);
;             MS_XSWRITE(0); MS_XSLOAD(1);
;             __syncthreads();
; #pragma unroll 1
;             for (int t = 0; t < NT; t += 2) { MS_STEP(0, 1, t); MS_STEP(1, 0, t + 1); }
	s_lshl_b32 s12, s12, 17
	v_mfma_f32_16x16x32_bf16 v[92:95], v[206:209], v[164:167], v[92:95]
	s_add_i32 s12, s12, 0x80000
	v_mfma_f32_16x16x32_bf16 v[66:69], v[210:213], v[164:167], v[66:69]
	v_cvt_pk_bf16_f32 v164, v96, v100
	v_cvt_pk_bf16_f32 v165, v104, v108
	v_cvt_pk_bf16_f32 v96, v97, v101
	v_cvt_pk_bf16_f32 v97, v105, v109
	ds_write2_b64 v188, v[164:165], v[96:97] offset1:16
	v_cvt_pk_bf16_f32 v96, v98, v102
	v_cvt_pk_bf16_f32 v97, v106, v110
	v_cvt_pk_bf16_f32 v98, v99, v103
	v_cvt_pk_bf16_f32 v99, v107, v111
	ds_write2_b64 v180, v[96:97], v[98:99] offset0:32 offset1:48
	buffer_load_dwordx4 v[96:99], v160, s[8:11], s12 offen
	buffer_load_dwordx4 v[100:103], v90, s[8:11], s12 offen
	buffer_load_dwordx4 v[104:107], v178, s[8:11], s12 offen
	buffer_load_dwordx4 v[108:111], v179, s[8:11], s12 offen
	v_mfma_f32_16x16x32_bf16 v[58:61], v[198:201], v[190:193], v[58:61]
	v_mfma_f32_16x16x32_bf16 v[50:53], v[202:205], v[190:193], v[50:53]
	v_mfma_f32_16x16x32_bf16 v[42:45], v[206:209], v[190:193], v[42:45]
	v_mfma_f32_16x16x32_bf16 v[34:37], v[210:213], v[190:193], v[34:37]
	ds_read_b128 v[164:167], v214 offset:38912
	ds_read_b128 v[190:193], v214 offset:40960
	ds_read_b128 v[198:201], v215 offset:16384
	ds_read_b128 v[202:205], v215 offset:18432
	ds_read_b128 v[206:209], v215 offset:20480
	ds_read_b128 v[210:213], v215 offset:22528
	s_waitcnt lgkmcnt(3)
	v_mfma_f32_16x16x32_bf16 v[152:155], v[198:201], v[164:167], v[152:155]
	v_mfma_f32_16x16x32_bf16 v[62:65], v[198:201], v[190:193], v[62:65]
	s_waitcnt lgkmcnt(2)
	v_mfma_f32_16x16x32_bf16 v[120:123], v[202:205], v[164:167], v[120:123]
	v_mfma_f32_16x16x32_bf16 v[54:57], v[202:205], v[190:193], v[54:57]
	s_waitcnt lgkmcnt(1)
	v_mfma_f32_16x16x32_bf16 v[112:115], v[206:209], v[164:167], v[112:115]
	v_mfma_f32_16x16x32_bf16 v[46:49], v[206:209], v[190:193], v[46:49]
	s_waitcnt lgkmcnt(0)
	v_mfma_f32_16x16x32_bf16 v[70:73], v[210:213], v[164:167], v[70:73]
	v_mfma_f32_16x16x32_bf16 v[38:41], v[210:213], v[190:193], v[38:41]
	ds_read_b128 v[198:201], v215 offset:24576
	ds_read_b128 v[202:205], v215 offset:26624
	ds_read_b128 v[206:209], v215 offset:28672
	ds_read_b128 v[210:213], v215 offset:30720
	s_waitcnt lgkmcnt(3)
	v_mfma_f32_16x16x32_bf16 v[148:151], v[198:201], v[164:167], v[148:151]
	v_mfma_f32_16x16x32_bf16 v[58:61], v[198:201], v[190:193], v[58:61]
	s_waitcnt lgkmcnt(2)
	v_mfma_f32_16x16x32_bf16 v[116:119], v[202:205], v[164:167], v[116:119]
	v_mfma_f32_16x16x32_bf16 v[50:53], v[202:205], v[190:193], v[50:53]
	s_waitcnt lgkmcnt(1)
	v_mfma_f32_16x16x32_bf16 v[92:95], v[206:209], v[164:167], v[92:95]
	v_mfma_f32_16x16x32_bf16 v[42:45], v[206:209], v[190:193], v[42:45]
	s_waitcnt lgkmcnt(0)
	v_mfma_f32_16x16x32_bf16 v[66:69], v[210:213], v[164:167], v[66:69]
	v_mfma_f32_16x16x32_bf16 v[34:37], v[210:213], v[190:193], v[34:37]
	ds_read_b128 v[164:167], v216 offset:38912
	ds_read_b128 v[190:193], v216 offset:40960
	ds_read_b128 v[198:201], v217 offset:16384
	ds_read_b128 v[202:205], v217 offset:18432
	ds_read_b128 v[206:209], v217 offset:20480
	ds_read_b128 v[210:213], v217 offset:22528
	s_waitcnt lgkmcnt(3)
	v_mfma_f32_16x16x32_bf16 v[152:155], v[198:201], v[164:167], v[152:155]
	v_mfma_f32_16x16x32_bf16 v[62:65], v[198:201], v[190:193], v[62:65]
	s_waitcnt lgkmcnt(2)
	v_mfma_f32_16x16x32_bf16 v[120:123], v[202:205], v[164:167], v[120:123]
	v_mfma_f32_16x16x32_bf16 v[54:57], v[202:205], v[190:193], v[54:57]
	s_waitcnt lgkmcnt(1)
	v_mfma_f32_16x16x32_bf16 v[112:115], v[206:209], v[164:167], v[112:115]
	v_mfma_f32_16x16x32_bf16 v[46:49], v[206:209], v[190:193], v[46:49]
	s_waitcnt lgkmcnt(0)
	v_mfma_f32_16x16x32_bf16 v[70:73], v[210:213], v[164:167], v[70:73]
	v_mfma_f32_16x16x32_bf16 v[38:41], v[210:213], v[190:193], v[38:41]
	ds_read_b128 v[198:201], v217 offset:24576
	ds_read_b128 v[202:205], v217 offset:26624
	ds_read_b128 v[206:209], v217 offset:28672
	ds_read_b128 v[210:213], v217 offset:30720
	s_lshl_b32 s1, s1, 7
	s_waitcnt vmcnt(9)
	ds_write_b128 v189, v[124:127] offset:32768
	s_waitcnt vmcnt(8)
	ds_write_b128 v181, v[128:131] offset:33792
	s_waitcnt vmcnt(7)
	ds_write_b128 v189, v[132:135] offset:34816
	s_waitcnt vmcnt(6)
	ds_write_b128 v181, v[136:139] offset:35840
	s_waitcnt vmcnt(5)
	ds_write_b128 v189, v[140:143] offset:36864
	s_waitcnt vmcnt(4)
	ds_write_b128 v181, v[144:147] offset:37888
	s_addk_i32 s1, 0x180
	buffer_load_dwordx4 v[132:135], v182, s[4:7], s1 offen
	buffer_load_dwordx4 v[124:127], v183, s[4:7], s1 offen
	buffer_load_dwordx4 v[140:143], v184, s[4:7], s1 offen
	buffer_load_dwordx4 v[144:147], v185, s[4:7], s1 offen
	buffer_load_dwordx4 v[128:131], v186, s[4:7], s1 offen
	buffer_load_dwordx4 v[136:139], v187, s[4:7], s1 offen
	s_waitcnt lgkmcnt(9)
	v_mfma_f32_16x16x32_bf16 v[148:151], v[198:201], v[164:167], v[148:151]
	s_cmp_gt_u32 s0, 29
	s_waitcnt lgkmcnt(0)
	s_barrier
	v_mfma_f32_16x16x32_bf16 v[58:61], v[198:201], v[190:193], v[58:61]
	v_mfma_f32_16x16x32_bf16 v[116:119], v[202:205], v[164:167], v[116:119]
	v_mfma_f32_16x16x32_bf16 v[50:53], v[202:205], v[190:193], v[50:53]
	v_mfma_f32_16x16x32_bf16 v[92:95], v[206:209], v[164:167], v[92:95]
	v_mfma_f32_16x16x32_bf16 v[42:45], v[206:209], v[190:193], v[42:45]
	v_mfma_f32_16x16x32_bf16 v[66:69], v[210:213], v[164:167], v[66:69]
	v_mfma_f32_16x16x32_bf16 v[34:37], v[210:213], v[190:193], v[34:37]
	s_cbranch_scc0 .Lmoe_k_b
; DI unsigned pk2(float a, float b) { f32x2 v = {a, b}; bf16x2_t r = __builtin_convertvector(v, bf16x2_t); return __builtin_bit_cast(unsigned, r); }
; DI float sigmoidf_(float x) { return 1.f / (1.f + __expf(-x)); }
;     ...
; #pragma unroll
;             for (int mt = 0; mt < 3; ++mt) { const int tok = rp + wave * 48 + mt * 16 + tk;
;                 if (tok < M) {
;                     if (MODE == 0) { bf16* o = (bf16*)(ws + o_hid) + (size_t)(row0 + tok) * DEXP + slab * 64 + 4 * q;
; #pragma unroll
;                         for (int j = 0; j < 4; ++j) { float h[4];
; #pragma unroll
;                             for (int i = 0; i < 4; ++i) { const float gt = acc[mt][j][i]; h[i] = gt * sigmoidf_(gt) * acc[mt][j + 4][i]; }
;                             *(u32x2*)(o + 16 * j) = (u32x2){pk2(h[0], h[1]), pk2(h[2], h[3])}; }
.Lmoe_k_done:
	v_add_u32_e32 v76, s31, v177
	v_cmp_gt_i32_e32 vcc, s28, v76
	s_and_saveexec_b64 s[12:13], vcc
	s_cbranch_execz .LBB0_1723
	v_mul_f32_e32 v77, 0xbfb8aa3b, v152
	v_exp_f32_e32 v78, v77
	v_mul_f32_e32 v77, 0xbfb8aa3b, v153
	v_exp_f32_e32 v79, v77
	v_add_u32_e32 v74, s29, v76
	v_ashrrev_i32_e32 v75, 31, v74
	v_lshlrev_b64 v[74:75], 10, v[74:75]
	v_pk_add_f32 v[78:79], v[78:79], 1.0 op_sel_hi:[1,0]
	v_lshl_add_u64 v[74:75], v[158:159], 0, v[74:75]
	v_rcp_f32_e32 v79, v79
	v_rcp_f32_e32 v78, v78
	v_mul_f32_e32 v77, 0xbfb8aa3b, v154
	v_exp_f32_e32 v80, v77
	v_mul_f32_e32 v77, 0xbfb8aa3b, v155
	v_exp_f32_e32 v81, v77
	v_pk_mul_f32 v[78:79], v[152:153], v[78:79]
	v_pk_add_f32 v[80:81], v[80:81], 1.0 op_sel_hi:[1,0]
	s_nop 0
	v_pk_mul_f32 v[78:79], v[78:79], v[148:149]
	v_rcp_f32_e32 v81, v81
	v_cvt_pk_bf16_f32 v78, v78, v79
	v_rcp_f32_e32 v80, v80
	s_nop 0
	v_pk_mul_f32 v[80:81], v[154:155], v[80:81]
	v_mul_f32_e32 v77, 0xbfb8aa3b, v120
	v_pk_mul_f32 v[80:81], v[80:81], v[150:151]
	s_nop 0
	v_cvt_pk_bf16_f32 v79, v80, v81
	global_store_dwordx2 v[74:75], v[78:79], off
	v_exp_f32_e32 v78, v77
	v_mul_f32_e32 v77, 0xbfb8aa3b, v121
	v_exp_f32_e32 v79, v77
	s_nop 0
	v_pk_add_f32 v[78:79], v[78:79], 1.0 op_sel_hi:[1,0]
	s_nop 0
	v_rcp_f32_e32 v79, v79
	v_rcp_f32_e32 v78, v78
	v_mul_f32_e32 v77, 0xbfb8aa3b, v122
	v_exp_f32_e32 v80, v77
	v_mul_f32_e32 v77, 0xbfb8aa3b, v123
	v_exp_f32_e32 v81, v77
	v_pk_mul_f32 v[78:79], v[120:121], v[78:79]
	v_pk_add_f32 v[80:81], v[80:81], 1.0 op_sel_hi:[1,0]
	s_nop 0
	v_pk_mul_f32 v[78:79], v[78:79], v[116:117]
	v_rcp_f32_e32 v81, v81
	v_cvt_pk_bf16_f32 v78, v78, v79
	v_rcp_f32_e32 v80, v80
	s_nop 0
	v_pk_mul_f32 v[80:81], v[122:123], v[80:81]
	v_mul_f32_e32 v77, 0xbfb8aa3b, v112
	v_pk_mul_f32 v[80:81], v[80:81], v[118:119]
	s_nop 0
	v_cvt_pk_bf16_f32 v79, v80, v81
	global_store_dwordx2 v[74:75], v[78:79], off offset:32
	v_exp_f32_e32 v78, v77
	v_mul_f32_e32 v77, 0xbfb8aa3b, v113
	v_exp_f32_e32 v79, v77
	s_nop 0
	v_pk_add_f32 v[78:79], v[78:79], 1.0 op_sel_hi:[1,0]
	s_nop 0
	v_rcp_f32_e32 v79, v79
	v_rcp_f32_e32 v78, v78
	v_mul_f32_e32 v77, 0xbfb8aa3b, v114
	v_exp_f32_e32 v80, v77
	v_mul_f32_e32 v77, 0xbfb8aa3b, v115
	v_exp_f32_e32 v81, v77
	v_pk_mul_f32 v[78:79], v[112:113], v[78:79]
	v_pk_add_f32 v[80:81], v[80:81], 1.0 op_sel_hi:[1,0]
	s_nop 0
	v_pk_mul_f32 v[78:79], v[78:79], v[92:93]
	v_rcp_f32_e32 v81, v81
	v_cvt_pk_bf16_f32 v78, v78, v79
	v_rcp_f32_e32 v80, v80
	s_nop 0
	v_pk_mul_f32 v[80:81], v[114:115], v[80:81]
	v_mul_f32_e32 v77, 0xbfb8aa3b, v70
	v_pk_mul_f32 v[80:81], v[80:81], v[94:95]
	s_nop 0
	v_cvt_pk_bf16_f32 v79, v80, v81
	global_store_dwordx2 v[74:75], v[78:79], off offset:64
	v_exp_f32_e32 v78, v77
	v_mul_f32_e32 v77, 0xbfb8aa3b, v71
	v_exp_f32_e32 v79, v77
	s_nop 0
	v_pk_add_f32 v[78:79], v[78:79], 1.0 op_sel_hi:[1,0]
	s_nop 0
	v_rcp_f32_e32 v79, v79
	v_rcp_f32_e32 v78, v78
	s_nop 0
	v_pk_mul_f32 v[70:71], v[70:71], v[78:79]
	s_nop 0
	v_pk_mul_f32 v[66:67], v[70:71], v[66:67]
	v_mul_f32_e32 v70, 0xbfb8aa3b, v72
	v_mul_f32_e32 v71, 0xbfb8aa3b, v73
	v_exp_f32_e32 v70, v70
	v_exp_f32_e32 v71, v71
	v_cvt_pk_bf16_f32 v66, v66, v67
	v_pk_add_f32 v[70:71], v[70:71], 1.0 op_sel_hi:[1,0]
	s_nop 0
	v_rcp_f32_e32 v71, v71
	v_rcp_f32_e32 v70, v70
	s_nop 0
	v_pk_mul_f32 v[70:71], v[72:73], v[70:71]
	s_nop 0
	v_pk_mul_f32 v[68:69], v[70:71], v[68:69]
	s_nop 0
	v_cvt_pk_bf16_f32 v67, v68, v69
	global_store_dwordx2 v[74:75], v[66:67], off offset:96
.LBB0_1723:
	s_or_b64 exec, exec, s[12:13]
	v_add_u32_e32 v66, 0x80, v76
	v_cmp_gt_i32_e32 vcc, s28, v66
	s_and_saveexec_b64 s[12:13], vcc
	s_cbranch_execz .LBB0_1725
	v_mul_f32_e32 v68, 0xbfb8aa3b, v62
	v_mul_f32_e32 v69, 0xbfb8aa3b, v63
	v_exp_f32_e32 v68, v68
	v_exp_f32_e32 v69, v69
	v_add_u32_e32 v66, s29, v66
	v_ashrrev_i32_e32 v67, 31, v66
	v_lshlrev_b64 v[66:67], 10, v[66:67]
	v_pk_add_f32 v[68:69], v[68:69], 1.0 op_sel_hi:[1,0]
	v_lshl_add_u64 v[66:67], v[158:159], 0, v[66:67]
	v_rcp_f32_e32 v69, v69
	v_rcp_f32_e32 v68, v68
	s_nop 0
	v_pk_mul_f32 v[62:63], v[62:63], v[68:69]
	s_nop 0
	v_pk_mul_f32 v[58:59], v[62:63], v[58:59]
	v_mul_f32_e32 v62, 0xbfb8aa3b, v64
	v_mul_f32_e32 v63, 0xbfb8aa3b, v65
	v_exp_f32_e32 v62, v62
	v_exp_f32_e32 v63, v63
	v_cvt_pk_bf16_f32 v58, v58, v59
	v_pk_add_f32 v[62:63], v[62:63], 1.0 op_sel_hi:[1,0]
	s_nop 0
	v_rcp_f32_e32 v63, v63
	v_rcp_f32_e32 v62, v62
	s_nop 0
	v_pk_mul_f32 v[62:63], v[64:65], v[62:63]
	s_nop 0
	v_pk_mul_f32 v[60:61], v[62:63], v[60:61]
	s_nop 0
	v_cvt_pk_bf16_f32 v59, v60, v61
	global_store_dwordx2 v[66:67], v[58:59], off
	v_mul_f32_e32 v58, 0xbfb8aa3b, v54
	v_mul_f32_e32 v59, 0xbfb8aa3b, v55
	v_exp_f32_e32 v58, v58
	v_exp_f32_e32 v59, v59
	s_nop 0
	v_pk_add_f32 v[58:59], v[58:59], 1.0 op_sel_hi:[1,0]
	s_nop 0
	v_rcp_f32_e32 v59, v59
	v_rcp_f32_e32 v58, v58
	s_nop 0
	v_pk_mul_f32 v[54:55], v[54:55], v[58:59]
	s_nop 0
	v_pk_mul_f32 v[50:51], v[54:55], v[50:51]
	v_mul_f32_e32 v54, 0xbfb8aa3b, v56
	v_mul_f32_e32 v55, 0xbfb8aa3b, v57
	v_exp_f32_e32 v54, v54
	v_exp_f32_e32 v55, v55
	v_cvt_pk_bf16_f32 v50, v50, v51
	v_pk_add_f32 v[54:55], v[54:55], 1.0 op_sel_hi:[1,0]
	s_nop 0
	v_rcp_f32_e32 v55, v55
	v_rcp_f32_e32 v54, v54
	s_nop 0
	v_pk_mul_f32 v[54:55], v[56:57], v[54:55]
	s_nop 0
	v_pk_mul_f32 v[52:53], v[54:55], v[52:53]
	s_nop 0
	v_cvt_pk_bf16_f32 v51, v52, v53
	global_store_dwordx2 v[66:67], v[50:51], off offset:32
	v_mul_f32_e32 v50, 0xbfb8aa3b, v46
	v_mul_f32_e32 v51, 0xbfb8aa3b, v47
	v_exp_f32_e32 v50, v50
	v_exp_f32_e32 v51, v51
	s_nop 0
	v_pk_add_f32 v[50:51], v[50:51], 1.0 op_sel_hi:[1,0]
	s_nop 0
	v_rcp_f32_e32 v51, v51
	v_rcp_f32_e32 v50, v50
	s_nop 0
	v_pk_mul_f32 v[46:47], v[46:47], v[50:51]
	s_nop 0
	v_pk_mul_f32 v[42:43], v[46:47], v[42:43]
	v_mul_f32_e32 v46, 0xbfb8aa3b, v48
	v_mul_f32_e32 v47, 0xbfb8aa3b, v49
	v_exp_f32_e32 v46, v46
	v_exp_f32_e32 v47, v47
	v_cvt_pk_bf16_f32 v42, v42, v43
	v_pk_add_f32 v[46:47], v[46:47], 1.0 op_sel_hi:[1,0]
	s_nop 0
	v_rcp_f32_e32 v47, v47
	v_rcp_f32_e32 v46, v46
	s_nop 0
	v_pk_mul_f32 v[46:47], v[48:49], v[46:47]
	s_nop 0
	v_pk_mul_f32 v[44:45], v[46:47], v[44:45]
	s_nop 0
	v_cvt_pk_bf16_f32 v43, v44, v45
	global_store_dwordx2 v[66:67], v[42:43], off offset:64
	v_mul_f32_e32 v42, 0xbfb8aa3b, v38
	v_mul_f32_e32 v43, 0xbfb8aa3b, v39
	v_exp_f32_e32 v42, v42
	v_exp_f32_e32 v43, v43
	s_nop 0
	v_pk_add_f32 v[42:43], v[42:43], 1.0 op_sel_hi:[1,0]
	s_nop 0
	v_rcp_f32_e32 v43, v43
	v_rcp_f32_e32 v42, v42
	s_nop 0
	v_pk_mul_f32 v[38:39], v[38:39], v[42:43]
	s_nop 0
	v_pk_mul_f32 v[34:35], v[38:39], v[34:35]
	v_mul_f32_e32 v38, 0xbfb8aa3b, v40
	v_mul_f32_e32 v39, 0xbfb8aa3b, v41
	v_exp_f32_e32 v38, v38
	v_exp_f32_e32 v39, v39
	v_cvt_pk_bf16_f32 v34, v34, v35
	v_pk_add_f32 v[38:39], v[38:39], 1.0 op_sel_hi:[1,0]
	s_nop 0
	v_rcp_f32_e32 v39, v39
	v_rcp_f32_e32 v38, v38
	s_nop 0
	v_pk_mul_f32 v[38:39], v[40:41], v[38:39]
	s_nop 0
	v_pk_mul_f32 v[36:37], v[38:39], v[36:37]
	s_nop 0
	v_cvt_pk_bf16_f32 v35, v36, v37
	global_store_dwordx2 v[66:67], v[34:35], off offset:96
; DI unsigned pk2(float a, float b) { f32x2 v = {a, b}; bf16x2_t r = __builtin_convertvector(v, bf16x2_t); return __builtin_bit_cast(unsigned, r); }
; DI float sigmoidf_(float x) { return 1.f / (1.f + __expf(-x)); }
;     ...
; #pragma unroll
;             for (int mt = 0; mt < 3; ++mt) { const int tok = rp + wave * 48 + mt * 16 + tk;
;                 if (tok < M) {
;                     if (MODE == 0) { bf16* o = (bf16*)(ws + o_hid) + (size_t)(row0 + tok) * DEXP + slab * 64 + 4 * q;
; #pragma unroll
;                         for (int j = 0; j < 4; ++j) { float h[4];
; #pragma unroll
;                             for (int i = 0; i < 4; ++i) { const float gt = acc[mt][j][i]; h[i] = gt * sigmoidf_(gt) * acc[mt][j + 4][i]; }
;                             *(u32x2*)(o + 16 * j) = (u32x2){pk2(h[0], h[1]), pk2(h[2], h[3])}; }
.LBB0_1725:
	s_or_b64 exec, exec, s[12:13]
	v_add_u32_e32 v34, 0x100, v76
	v_cmp_gt_i32_e32 vcc, s28, v34
	s_and_saveexec_b64 s[12:13], vcc
	s_cbranch_execz .LBB0_1718
	v_mul_f32_e32 v36, 0xbfb8aa3b, v30
	v_mul_f32_e32 v37, 0xbfb8aa3b, v31
	v_exp_f32_e32 v36, v36
	v_exp_f32_e32 v37, v37
	v_add_u32_e32 v34, s29, v34
	v_ashrrev_i32_e32 v35, 31, v34
	v_lshlrev_b64 v[34:35], 10, v[34:35]
	v_pk_add_f32 v[36:37], v[36:37], 1.0 op_sel_hi:[1,0]
	v_lshl_add_u64 v[34:35], v[158:159], 0, v[34:35]
	v_rcp_f32_e32 v37, v37
	v_rcp_f32_e32 v36, v36
	s_nop 0
	v_pk_mul_f32 v[30:31], v[30:31], v[36:37]
	s_nop 0
	v_pk_mul_f32 v[26:27], v[30:31], v[26:27]
	v_mul_f32_e32 v30, 0xbfb8aa3b, v32
	v_mul_f32_e32 v31, 0xbfb8aa3b, v33
	v_exp_f32_e32 v30, v30
	v_exp_f32_e32 v31, v31
	v_cvt_pk_bf16_f32 v26, v26, v27
	v_pk_add_f32 v[30:31], v[30:31], 1.0 op_sel_hi:[1,0]
	s_nop 0
	v_rcp_f32_e32 v31, v31
	v_rcp_f32_e32 v30, v30
	s_nop 0
	v_pk_mul_f32 v[30:31], v[32:33], v[30:31]
	s_nop 0
	v_pk_mul_f32 v[28:29], v[30:31], v[28:29]
	s_nop 0
	v_cvt_pk_bf16_f32 v27, v28, v29
	global_store_dwordx2 v[34:35], v[26:27], off
	v_mul_f32_e32 v26, 0xbfb8aa3b, v22
	v_mul_f32_e32 v27, 0xbfb8aa3b, v23
	v_exp_f32_e32 v26, v26
	v_exp_f32_e32 v27, v27
	s_nop 0
	v_pk_add_f32 v[26:27], v[26:27], 1.0 op_sel_hi:[1,0]
	s_nop 0
	v_rcp_f32_e32 v27, v27
	v_rcp_f32_e32 v26, v26
	s_nop 0
	v_pk_mul_f32 v[22:23], v[22:23], v[26:27]
	s_nop 0
	v_pk_mul_f32 v[18:19], v[22:23], v[18:19]
	v_mul_f32_e32 v22, 0xbfb8aa3b, v24
	v_mul_f32_e32 v23, 0xbfb8aa3b, v25
	v_exp_f32_e32 v22, v22
	v_exp_f32_e32 v23, v23
	v_cvt_pk_bf16_f32 v18, v18, v19
	v_pk_add_f32 v[22:23], v[22:23], 1.0 op_sel_hi:[1,0]
	s_nop 0
	v_rcp_f32_e32 v23, v23
	v_rcp_f32_e32 v22, v22
	s_nop 0
	v_pk_mul_f32 v[22:23], v[24:25], v[22:23]
	s_nop 0
	v_pk_mul_f32 v[20:21], v[22:23], v[20:21]
	s_nop 0
	v_cvt_pk_bf16_f32 v19, v20, v21
	global_store_dwordx2 v[34:35], v[18:19], off offset:32
	v_mul_f32_e32 v18, 0xbfb8aa3b, v14
	v_mul_f32_e32 v19, 0xbfb8aa3b, v15
	v_exp_f32_e32 v18, v18
	v_exp_f32_e32 v19, v19
	s_nop 0
	v_pk_add_f32 v[18:19], v[18:19], 1.0 op_sel_hi:[1,0]
	s_nop 0
	v_rcp_f32_e32 v19, v19
	v_rcp_f32_e32 v18, v18
	s_nop 0
	v_pk_mul_f32 v[14:15], v[14:15], v[18:19]
	s_nop 0
	v_pk_mul_f32 v[10:11], v[14:15], v[10:11]
	v_mul_f32_e32 v14, 0xbfb8aa3b, v16
	v_mul_f32_e32 v15, 0xbfb8aa3b, v17
	v_exp_f32_e32 v14, v14
	v_exp_f32_e32 v15, v15
	v_cvt_pk_bf16_f32 v10, v10, v11
	v_pk_add_f32 v[14:15], v[14:15], 1.0 op_sel_hi:[1,0]
	s_nop 0
	v_rcp_f32_e32 v15, v15
	v_rcp_f32_e32 v14, v14
	s_nop 0
	v_pk_mul_f32 v[14:15], v[16:17], v[14:15]
	s_nop 0
	v_pk_mul_f32 v[12:13], v[14:15], v[12:13]
	s_nop 0
	v_cvt_pk_bf16_f32 v11, v12, v13
	global_store_dwordx2 v[34:35], v[10:11], off offset:64
	v_mul_f32_e32 v10, 0xbfb8aa3b, v6
	v_mul_f32_e32 v11, 0xbfb8aa3b, v7
	v_exp_f32_e32 v10, v10
	v_exp_f32_e32 v11, v11
	s_nop 0
	v_pk_add_f32 v[10:11], v[10:11], 1.0 op_sel_hi:[1,0]
	s_nop 0
	v_rcp_f32_e32 v11, v11
	v_rcp_f32_e32 v10, v10
	s_nop 0
	v_pk_mul_f32 v[6:7], v[6:7], v[10:11]
	s_nop 0
	v_pk_mul_f32 v[2:3], v[6:7], v[2:3]
	v_mul_f32_e32 v6, 0xbfb8aa3b, v8
	v_mul_f32_e32 v7, 0xbfb8aa3b, v9
	v_exp_f32_e32 v6, v6
	v_exp_f32_e32 v7, v7
	v_cvt_pk_bf16_f32 v2, v2, v3
	v_pk_add_f32 v[6:7], v[6:7], 1.0 op_sel_hi:[1,0]
	s_nop 0
	v_rcp_f32_e32 v7, v7
	v_rcp_f32_e32 v6, v6
	s_nop 0
	v_pk_mul_f32 v[6:7], v[8:9], v[6:7]
	s_nop 0
	v_pk_mul_f32 v[4:5], v[6:7], v[4:5]
	s_nop 0
	v_cvt_pk_bf16_f32 v3, v4, v5
	global_store_dwordx2 v[34:35], v[2:3], off offset:96
	s_branch .LBB0_1718

; #define GAS __attribute__((address_space(1)))
; #define LAS __attribute__((address_space(3)))
;     ...
;     constexpr int KD = (MODE == 0) ? D : DEXP, NT = KD / 64, NSLAB = (MODE == 0) ? 8 : 16, LDW = (MODE == 0) ? DEXP : D, LDX = KD;
;     const int half = wave & 1, nb16 = lane & 15, kb = 4 * (wave >> 1) + (lane >> 4);
;     const int tk = lane & 15, q = lane >> 4;
;     const GAS char* wmat = (const GAS char*)((MODE == 0) ? (half ? a.inp(I_WEU) : a.inp(I_WEG)) : a.inp(I_WED));
;     const unsigned wvo = (unsigned)((4 * kb * LDW + 4 * nb16) * 4);
;     const int lw0 = (64 * half + 4 * nb16) * 128 + (((kb >> 1) ^ ((2 * nb16) & 7)) << 4) + (kb & 1) * 8, lw1 = lw0 ^ 16;
;     const int rd_g = (tk >> 1) & 7;
;     for (int vb = bid; vb < NEXP * NSLAB; vb += G) {
;         const int xcd = vb & 7, idx = vb >> 3; const int e = xcd * 8 + idx / NSLAB, slab = idx % NSLAB;
;         const int M = __builtin_amdgcn_readfirstlane(lc[LC_CNT / 4 + e]), row0 = __builtin_amdgcn_readfirstlane(lc[LC_PSTART / 4 + e]);
;         const size_t wuo = (MODE == 0) ? ((size_t)(l * NEXP + e) * D * DEXP + slab * 64) * 4 : ((size_t)(l * NEXP + e) * DEXP * D + slab * 128 + 64 * half) * 4;
;         const __amdgpu_buffer_rsrc_t wrs = __builtin_amdgcn_make_buffer_rsrc((void*)(wmat + wuo), 0, KD * LDW * 4, 0x00020000);
;         const __amdgpu_buffer_rsrc_t xrs = __builtin_amdgcn_make_buffer_rsrc((MODE == 0) ? (void*)(ws + WS_U) : (void*)((const GAS char*)(ws + WS_HID) + (size_t)row0 * LDX * 2), 0, 0x7fffffff, 0x00020000);
;         const int* el = (const int*)(ws + WS_ELIST) + (size_t)e * T;
;         for (int rp = 0; rp < M; rp += 384) {
;             unsigned xso[6];
; #pragma unroll
;             for (int i = 0; i < 6; ++i) { int tok = rp + wave * 48 + 8 * i + (lane >> 3); tok = min(tok, M - 1); if (VAR == 5) tok &= 15; if (MODE == 0) tok = el[tok]; xso[i] = (unsigned)(tok * LDX * 2 + (lane & 7) * 16); }
;             LAS unsigned char* xw = lds + MS_XOFF + wave * MS_XWAVE; const int xwo = (lane >> 3) * 128 + (((lane & 7) ^ ((lane >> 4) & 3)) << 4);
;             const LAS unsigned char* xr = lds + MS_XOFF + wave * MS_XWAVE + tk * 128 + ((q ^ rd_g) << 4);
.LBB0_1778:
	s_waitcnt vmcnt(7)
	v_mov_b32_e32 v2, v0
	s_load_dwordx4 s[0:3], s[74:75], 0x108
	s_mov_b64 s[4:5], s[74:75]
	s_waitcnt lgkmcnt(0)
	s_load_dword s0, s[78:79], 0x0
	s_mov_b32 s1, s72
	s_waitcnt lgkmcnt(0)
	s_cmpk_gt_i32 s1, 0x3ff
	v_readfirstlane_b32 s7, v2
	s_cbranch_scc1 .LBB0_1792
	s_ashr_i32 s8, s7, 6
	s_load_dwordx2 s[12:13], s[4:5], 0xf8
	v_and_b32_e32 v3, 15, v2
	s_lshl_b32 s4, s8, 1
	v_bfe_u32 v4, v2, 4, 2
	v_and_or_b32 v5, s4, -4, v4
	s_waitcnt vmcnt(0)
	v_lshlrev_b32_e32 v6, 4, v3
	s_and_b32 s94, s7, 64
	v_lshlrev_b32_e32 v90, 3, v4
	v_lshl_or_b32 v160, v5, 15, v6
	v_lshlrev_b32_e32 v6, 9, v3
	s_lshl_b32 s4, s94, 7
	v_and_b32_e32 v7, 8, v90
	v_or3_b32 v6, s4, v6, v7
	v_readlane_b32 s4, v255, 30
	s_lshl_b32 s26, s4, 6
	s_mul_i32 s4, s8, 16
	s_mul_i32 s80, s8, 16
	v_bfe_u32 v8, v2, 3, 3
	v_lshrrev_b32_e32 v5, 1, v5
	v_lshlrev_b32_e32 v7, 1, v2
	v_or_b32_e32 v162, s4, v8
	v_lshlrev_b32_e32 v8, 4, v2
	v_bitop3_b32 v5, v5, v7, 6 bitop3:0x78
	v_and_b32_e32 v163, 0x70, v8
	v_bitop3_b32 v8, v4, v2, 7 bitop3:0x78
	v_lshl_add_u32 v161, v5, 4, v6
	v_lshrrev_b32_e32 v6, 1, v2
	v_bfe_u32 v7, v2, 1, 3
	s_add_u32 s27, s2, 0x2fe31000
	s_mulk_i32 s8, 0x3000
	v_and_or_b32 v2, v2, 56, v8
	s_addc_u32 s28, s3, 0
	s_add_i32 s29, s8, 0
	v_lshlrev_b32_e32 v172, 4, v2
	v_lshlrev_b32_e32 v2, 7, v3
	v_add_u32_e32 v173, s29, v2
	v_add_u32_e32 v176, 0, v2
	v_or_b32_e32 v177, s4, v3
	v_lshl_add_u64 v[2:3], s[2:3], 0, v[90:91]
	s_mov_b64 s[2:3], 0x31e31000
	v_xor_b32_e32 v5, 16, v161
	v_bitop3_b32 v6, v6, v4, 7 bitop3:0x6c
	v_bitop3_b32 v4, v4, v7, 4 bitop3:0x36
	v_lshl_add_u64 v[156:157], v[2:3], 0, s[2:3]
	v_xor_b32_e32 v2, 64, v172
	v_lshlrev_b32_e32 v174, 4, v6
	v_lshlrev_b32_e32 v175, 4, v4
	v_or_b32_e32 v90, 0x2000, v160
	v_or_b32_e32 v178, 0x4000, v160
	v_or_b32_e32 v179, 0x6000, v160
	v_add_u32_e32 v180, 0, v5
	v_add_u32_e32 v181, s29, v2
	v_readlane_b32 s5, v255, 31
	s_branch .LBB0_1781

; #define LAS __attribute__((address_space(3)))
; #define MS_WLOAD(set, t) do { _Pragma("unroll") for (int r_ = 0; r_ < 4; ++r_) wr[set][r_] = __builtin_bit_cast(f32x4, __builtin_amdgcn_raw_buffer_load_b128(wrs, (int)wvo + r_ * LDW * 4, MS_CL(t) * (64 * LDW * 4), 0)); } while (0)
; #define MS_WCOMMIT(set, bufi) do { LAS unsigned char* wb_ = lds + (bufi) * MS_TILE; _Pragma("unroll") for (int i_ = 0; i_ < 4; ++i_) { \
;             u32x2 p_; p_.x = pk2(wr[set][0][i_], wr[set][1][i_]); p_.y = pk2(wr[set][2][i_], wr[set][3][i_]); \
;             *(LAS u32x2*)(wb_ + ((i_ < 2) ? lw0 : lw1) + i_ * 128) = p_; } } while (0)
; #define MS_XSLOAD(t) do { _Pragma("unroll") for (int i_ = 0; i_ < 6; ++i_) xs[i_] = __builtin_bit_cast(bf16x8, __builtin_amdgcn_raw_buffer_load_b128(xrs, (int)xso[i_], MS_CL(t) * 128, 0)); } while (0)
; #define MS_XSWRITE(bufi) do { _Pragma("unroll") for (int i_ = 0; i_ < 6; ++i_) *(LAS bf16x8*)(xw + (bufi) * MS_XBUF + i_ * 1024 + ((i_ & 1) ? (xwo ^ 64) : xwo)) = xs[i_]; } while (0)
;     ...
;         for (int rp = 0; rp < M; rp += 384) {
;             unsigned xso[6];
; #pragma unroll
;             for (int i = 0; i < 6; ++i) { int tok = rp + wave * 48 + 8 * i + (lane >> 3); tok = min(tok, M - 1); if (VAR == 5) tok &= 15; if (MODE == 0) tok = el[tok]; xso[i] = (unsigned)(tok * LDX * 2 + (lane & 7) * 16); }
;             LAS unsigned char* xw = lds + MS_XOFF + wave * MS_XWAVE; const int xwo = (lane >> 3) * 128 + (((lane & 7) ^ ((lane >> 4) & 3)) << 4);
;             const LAS unsigned char* xr = lds + MS_XOFF + wave * MS_XWAVE + tk * 128 + ((q ^ rd_g) << 4);
;             f32x4 acc[3][8];
; #pragma unroll
;             for (int mt = 0; mt < 3; ++mt)
; #pragma unroll
;                 for (int j = 0; j < 8; ++j) acc[mt][j] = (f32x4){0.f, 0.f, 0.f, 0.f};
;             f32x4 wr[2][4];
;             bf16x8 xs[6];
;     ...
;             const LAS unsigned char* xr1 = lds + MS_XOFF + wave * MS_XWAVE + tk * 128 + (((4 + q) ^ rd_g) << 4);
;             __syncthreads();
;             MS_XSLOAD(0); MS_WLOAD(0, 0); MS_WLOAD(1, 1);
;             MS_WCOMMIT(0, 0); MS_WLOAD(0, 2);
;             MS_XSWRITE(0); MS_XSLOAD(1);
;             __syncthreads();
.LBB0_1784:
	v_add_u32_e32 v2, s31, v162
	v_min_i32_e32 v3, s25, v2
	v_lshl_or_b32 v182, v3, 10, v163
	v_or_b32_e32 v3, 8, v2
	v_min_i32_e32 v3, s25, v3
	v_lshl_or_b32 v183, v3, 10, v163
	v_add_u32_e32 v3, 0x80, v2
	v_min_i32_e32 v3, s25, v3
	v_lshl_or_b32 v184, v3, 10, v163
	v_add_u32_e32 v3, 0x88, v2
	v_min_i32_e32 v3, s25, v3
	v_lshl_or_b32 v185, v3, 10, v163
	v_add_u32_e32 v3, 0x100, v2
	v_add_u32_e32 v2, 0x108, v2
	v_min_i32_e32 v3, s25, v3
	v_min_i32_e32 v2, s25, v2
	s_barrier
	buffer_load_dwordx4 v[52:55], v160, s[8:11], 0 offen
	buffer_load_dwordx4 v[56:59], v90, s[8:11], 0 offen
	buffer_load_dwordx4 v[60:63], v178, s[8:11], 0 offen
	buffer_load_dwordx4 v[64:67], v179, s[8:11], 0 offen
	v_lshl_or_b32 v186, v3, 10, v163
	v_lshl_or_b32 v187, v2, 10, v163
	buffer_load_dwordx4 v[68:71], v182, s[4:7], 0 offen
	buffer_load_dwordx4 v[72:75], v183, s[4:7], 0 offen
	buffer_load_dwordx4 v[76:79], v184, s[4:7], 0 offen
	buffer_load_dwordx4 v[80:83], v185, s[4:7], 0 offen
	buffer_load_dwordx4 v[84:87], v186, s[4:7], 0 offen
	buffer_load_dwordx4 v[96:99], v187, s[4:7], 0 offen
	buffer_load_dwordx4 v[2:5], v160, s[8:11], s23 offen
	buffer_load_dwordx4 v[6:9], v178, s[8:11], s23 offen
	buffer_load_dwordx4 v[18:21], v160, s[8:11], s93 offen
	buffer_load_dwordx4 v[10:13], v90, s[8:11], s23 offen
	buffer_load_dwordx4 v[22:25], v90, s[8:11], s93 offen
	buffer_load_dwordx4 v[26:29], v178, s[8:11], s93 offen
	buffer_load_dwordx4 v[14:17], v179, s[8:11], s23 offen
	buffer_load_dwordx4 v[30:33], v179, s[8:11], s93 offen
	buffer_load_dwordx4 v[104:107], v182, s[4:7], s92 offen
	buffer_load_dwordx4 v[92:95], v183, s[4:7], s92 offen
	buffer_load_dwordx4 v[112:115], v184, s[4:7], s92 offen
	buffer_load_dwordx4 v[116:119], v185, s[4:7], s92 offen
	buffer_load_dwordx4 v[100:103], v186, s[4:7], s92 offen
	buffer_load_dwordx4 v[108:111], v187, s[4:7], s92 offen
	v_add_u32_e32 v188, 0, v161
	v_mov_b32_e32 v34, 0
	v_add_u32_e32 v189, s29, v172
	s_mov_b32 s2, -2
	v_mov_b32_e32 v35, v34
	v_mov_b32_e32 v36, v34
	v_mov_b32_e32 v37, v34
	v_mov_b32_e32 v38, v34
	v_mov_b32_e32 v39, v34
	v_mov_b32_e32 v40, v34
	v_mov_b32_e32 v41, v34
	v_mov_b32_e32 v42, v34
	v_mov_b32_e32 v43, v34
	v_mov_b32_e32 v44, v34
	v_mov_b32_e32 v45, v34
	v_mov_b32_e32 v46, v34
	v_mov_b32_e32 v47, v34
	v_mov_b32_e32 v48, v34
	v_mov_b32_e32 v49, v34
	v_mov_b32_e32 v50, v34
	v_mov_b32_e32 v51, v34
	v_mov_b32_e32 v120, v34
	v_mov_b32_e32 v121, v34
	v_mov_b32_e32 v122, v34
	v_mov_b32_e32 v123, v34
	v_mov_b32_e32 v124, v34
	v_mov_b32_e32 v125, v34
	v_mov_b32_e32 v126, v34
	v_mov_b32_e32 v127, v34
	v_mov_b32_e32 v128, v34
	v_mov_b32_e32 v129, v34
	v_mov_b32_e32 v130, v34
	v_mov_b32_e32 v131, v34
	v_mov_b32_e32 v132, v34
	v_mov_b32_e32 v133, v34
	v_mov_b32_e32 v134, v34
	v_mov_b32_e32 v135, v34
	v_mov_b32_e32 v136, v34
	v_mov_b32_e32 v137, v34
	v_mov_b32_e32 v138, v34
	v_mov_b32_e32 v139, v34
	v_mov_b32_e32 v140, v34
	v_mov_b32_e32 v141, v34
	v_mov_b32_e32 v142, v34
	v_mov_b32_e32 v143, v34
	v_mov_b32_e32 v144, v34
	v_mov_b32_e32 v145, v34
	v_mov_b32_e32 v146, v34
	v_mov_b32_e32 v147, v34
	v_mov_b32_e32 v148, v34
	v_mov_b32_e32 v149, v34
	v_mov_b32_e32 v150, v34
	v_mov_b32_e32 v151, v34
	v_mov_b32_e32 v152, v34
	v_mov_b32_e32 v153, v34
	v_mov_b32_e32 v154, v34
	v_mov_b32_e32 v155, v34
	s_waitcnt vmcnt(22)
	v_cvt_pk_bf16_f32 v88, v52, v56
	v_cvt_pk_bf16_f32 v52, v53, v57
	s_waitcnt vmcnt(20)
	v_cvt_pk_bf16_f32 v89, v60, v64
	v_cvt_pk_bf16_f32 v53, v61, v65
	v_cvt_pk_bf16_f32 v56, v54, v58
	v_cvt_pk_bf16_f32 v57, v62, v66
	v_cvt_pk_bf16_f32 v54, v55, v59
	v_cvt_pk_bf16_f32 v55, v63, v67
	ds_write2_b64 v188, v[88:89], v[52:53] offset1:16
	ds_write2_b64 v180, v[56:57], v[54:55] offset0:32 offset1:48
	s_waitcnt vmcnt(19)
	ds_write_b128 v189, v[68:71] offset:32768
	s_waitcnt vmcnt(18)
	ds_write_b128 v181, v[72:75] offset:33792
	s_waitcnt vmcnt(17)
	ds_write_b128 v189, v[76:79] offset:34816
	s_waitcnt vmcnt(16)
	ds_write_b128 v181, v[80:83] offset:35840
	s_waitcnt vmcnt(15)
	ds_write_b128 v189, v[84:87] offset:36864
	s_waitcnt vmcnt(14)
	ds_write_b128 v181, v[96:99] offset:37888
	v_mov_b32_e32 v52, v34
	v_mov_b32_e32 v53, v34
	v_mov_b32_e32 v54, v34
	v_mov_b32_e32 v55, v34
	v_mov_b32_e32 v56, v34
	v_mov_b32_e32 v57, v34
	v_mov_b32_e32 v58, v34
	v_mov_b32_e32 v59, v34
	v_mov_b32_e32 v60, v34
	v_mov_b32_e32 v61, v34
	v_mov_b32_e32 v62, v34
	v_mov_b32_e32 v63, v34
	v_mov_b32_e32 v64, v34
	v_mov_b32_e32 v65, v34
	v_mov_b32_e32 v66, v34
	v_mov_b32_e32 v67, v34
	v_mov_b32_e32 v68, v34
	v_mov_b32_e32 v69, v34
	v_mov_b32_e32 v70, v34
	v_mov_b32_e32 v71, v34
	v_mov_b32_e32 v72, v34
	v_mov_b32_e32 v73, v34
	v_mov_b32_e32 v74, v34
	v_mov_b32_e32 v75, v34
	v_mov_b32_e32 v76, v34
	v_mov_b32_e32 v77, v34
	v_mov_b32_e32 v78, v34
	v_mov_b32_e32 v79, v34
	v_mov_b32_e32 v80, v34
	v_mov_b32_e32 v81, v34
	v_mov_b32_e32 v82, v34
	v_mov_b32_e32 v83, v34
	v_mov_b32_e32 v84, v34
	v_mov_b32_e32 v85, v34
	v_mov_b32_e32 v86, v34
	v_mov_b32_e32 v87, v34
	v_mov_b32_e32 v88, v34
	v_mov_b32_e32 v89, v34
	v_mov_b32_e32 v96, v34
	v_mov_b32_e32 v97, v34
	v_mov_b32_e32 v98, v34
	v_mov_b32_e32 v99, v34
	s_waitcnt lgkmcnt(0)
	s_barrier
	s_sub_i32 s81, s30, s31
	s_add_i32 s82, s80, 0x100
	s_cmp_le_i32 s81, s82
	s_cbranch_scc1 .Lmoe_l_b
; #define LAS __attribute__((address_space(3)))
; #define MS_WLOAD(set, t) do { _Pragma("unroll") for (int r_ = 0; r_ < 4; ++r_) wr[set][r_] = __builtin_bit_cast(f32x4, __builtin_amdgcn_raw_buffer_load_b128(wrs, (int)wvo + r_ * LDW * 4, MS_CL(t) * (64 * LDW * 4), 0)); } while (0)
; #define MS_WCOMMIT(set, bufi) do { LAS unsigned char* wb_ = lds + (bufi) * MS_TILE; _Pragma("unroll") for (int i_ = 0; i_ < 4; ++i_) { \
;             u32x2 p_; p_.x = pk2(wr[set][0][i_], wr[set][1][i_]); p_.y = pk2(wr[set][2][i_], wr[set][3][i_]); \
;             *(LAS u32x2*)(wb_ + ((i_ < 2) ? lw0 : lw1) + i_ * 128) = p_; } } while (0)
; #define MS_XSLOAD(t) do { _Pragma("unroll") for (int i_ = 0; i_ < 6; ++i_) xs[i_] = __builtin_bit_cast(bf16x8, __builtin_amdgcn_raw_buffer_load_b128(xrs, (int)xso[i_], MS_CL(t) * 128, 0)); } while (0)
; #define MS_XSWRITE(bufi) do { _Pragma("unroll") for (int i_ = 0; i_ < 6; ++i_) *(LAS bf16x8*)(xw + (bufi) * MS_XBUF + i_ * 1024 + ((i_ & 1) ? (xwo ^ 64) : xwo)) = xs[i_]; } while (0)
; #define MS_STEP(I, J, t) do { MS_WCOMMIT(J, J); MS_WLOAD(J, (t) + 3); MS_COMPUTE(I); MS_XSWRITE(J); MS_XSLOAD((t) + 2); __syncthreads(); } while (0)
;     ...
;             const LAS unsigned char* xr1 = lds + MS_XOFF + wave * MS_XWAVE + tk * 128 + (((4 + q) ^ rd_g) << 4);
;             __syncthreads();
;             MS_XSLOAD(0); MS_WLOAD(0, 0); MS_WLOAD(1, 1);
;             MS_WCOMMIT(0, 0); MS_WLOAD(0, 2);
;             MS_XSWRITE(0); MS_XSLOAD(1);
;             __syncthreads();
; #pragma unroll 1
;             for (int t = 0; t < NT; t += 2) { MS_STEP(0, 1, t); MS_STEP(1, 0, t + 1); }
.LBB0_1785:
	s_add_i32 s2, s2, 2
	s_min_u32 s3, s2, 4
	s_lshl_b32 s33, s3, 19
	s_add_i32 s33, s33, 0x180000
	s_waitcnt vmcnt(10)
	v_cvt_pk_bf16_f32 v164, v2, v10
	s_waitcnt vmcnt(7)
	v_cvt_pk_bf16_f32 v165, v6, v14
	v_cvt_pk_bf16_f32 v166, v3, v11
	v_cvt_pk_bf16_f32 v167, v7, v15
	v_cvt_pk_bf16_f32 v190, v4, v12
	v_cvt_pk_bf16_f32 v191, v8, v16
	v_cvt_pk_bf16_f32 v192, v5, v13
	v_cvt_pk_bf16_f32 v193, v9, v17
	buffer_load_dwordx4 v[2:5], v160, s[8:11], s33 offen
	buffer_load_dwordx4 v[10:13], v90, s[8:11], s33 offen
	buffer_load_dwordx4 v[6:9], v178, s[8:11], s33 offen
	buffer_load_dwordx4 v[14:17], v179, s[8:11], s33 offen
	v_add_u32_e32 v194, 0x4000, v188
	v_add_u32_e32 v195, 0x4000, v180
	v_add_u32_e32 v214, v173, v174
	ds_write2_b64 v194, v[164:165], v[166:167] offset1:16
	ds_write2_b64 v195, v[190:191], v[192:193] offset0:32 offset1:48
	v_add_u32_e32 v215, v176, v174
	ds_read_b128 v[164:167], v214 offset:32768
	ds_read_b128 v[190:193], v214 offset:34816
	ds_read_b128 v[194:197], v214 offset:36864
	ds_read_b128 v[198:201], v215
	ds_read_b128 v[202:205], v215 offset:2048
	ds_read_b128 v[206:209], v215 offset:4096
	ds_read_b128 v[210:213], v215 offset:6144
	s_waitcnt lgkmcnt(3)
	v_mfma_f32_16x16x32_bf16 v[152:155], v[198:201], v[164:167], v[152:155]
	v_mfma_f32_16x16x32_bf16 v[120:123], v[198:201], v[190:193], v[120:123]
	v_mfma_f32_16x16x32_bf16 v[62:65], v[198:201], v[194:197], v[62:65]
	s_waitcnt lgkmcnt(2)
	v_mfma_f32_16x16x32_bf16 v[148:151], v[202:205], v[164:167], v[148:151]
	v_mfma_f32_16x16x32_bf16 v[96:99], v[202:205], v[190:193], v[96:99]
	v_mfma_f32_16x16x32_bf16 v[58:61], v[202:205], v[194:197], v[58:61]
	s_waitcnt lgkmcnt(1)
	v_mfma_f32_16x16x32_bf16 v[144:147], v[206:209], v[164:167], v[144:147]
	v_mfma_f32_16x16x32_bf16 v[86:89], v[206:209], v[190:193], v[86:89]
	v_mfma_f32_16x16x32_bf16 v[54:57], v[206:209], v[194:197], v[54:57]
	s_waitcnt lgkmcnt(0)
	v_mfma_f32_16x16x32_bf16 v[140:143], v[210:213], v[164:167], v[140:143]
	v_mfma_f32_16x16x32_bf16 v[82:85], v[210:213], v[190:193], v[82:85]
	v_mfma_f32_16x16x32_bf16 v[50:53], v[210:213], v[194:197], v[50:53]
	ds_read_b128 v[198:201], v215 offset:8192
	ds_read_b128 v[202:205], v215 offset:10240
	ds_read_b128 v[206:209], v215 offset:12288
	ds_read_b128 v[210:213], v215 offset:14336
	s_waitcnt lgkmcnt(3)
	v_mfma_f32_16x16x32_bf16 v[136:139], v[198:201], v[164:167], v[136:139]
	v_mfma_f32_16x16x32_bf16 v[78:81], v[198:201], v[190:193], v[78:81]
	v_mfma_f32_16x16x32_bf16 v[46:49], v[198:201], v[194:197], v[46:49]
	s_waitcnt lgkmcnt(2)
	v_mfma_f32_16x16x32_bf16 v[132:135], v[202:205], v[164:167], v[132:135]
	v_mfma_f32_16x16x32_bf16 v[74:77], v[202:205], v[190:193], v[74:77]
	v_mfma_f32_16x16x32_bf16 v[42:45], v[202:205], v[194:197], v[42:45]
	s_waitcnt lgkmcnt(1)
	v_mfma_f32_16x16x32_bf16 v[128:131], v[206:209], v[164:167], v[128:131]
	v_mfma_f32_16x16x32_bf16 v[70:73], v[206:209], v[190:193], v[70:73]
	v_mfma_f32_16x16x32_bf16 v[38:41], v[206:209], v[194:197], v[38:41]
	s_waitcnt lgkmcnt(0)
	v_mfma_f32_16x16x32_bf16 v[124:127], v[210:213], v[164:167], v[124:127]
	v_mfma_f32_16x16x32_bf16 v[66:69], v[210:213], v[190:193], v[66:69]
	v_mfma_f32_16x16x32_bf16 v[34:37], v[210:213], v[194:197], v[34:37]
	v_add_u32_e32 v216, v173, v175
	ds_read_b128 v[164:167], v216 offset:32768
	ds_read_b128 v[190:193], v216 offset:34816
	v_add_u32_e32 v217, v176, v175
	ds_read_b128 v[194:197], v216 offset:36864
	ds_read_b128 v[198:201], v217
	ds_read_b128 v[202:205], v217 offset:2048
	ds_read_b128 v[206:209], v217 offset:4096
	ds_read_b128 v[210:213], v217 offset:6144
	s_waitcnt lgkmcnt(3)
	v_mfma_f32_16x16x32_bf16 v[152:155], v[198:201], v[164:167], v[152:155]
	v_mfma_f32_16x16x32_bf16 v[120:123], v[198:201], v[190:193], v[120:123]
	v_mfma_f32_16x16x32_bf16 v[62:65], v[198:201], v[194:197], v[62:65]
	s_waitcnt lgkmcnt(2)
	v_mfma_f32_16x16x32_bf16 v[148:151], v[202:205], v[164:167], v[148:151]
	v_mfma_f32_16x16x32_bf16 v[96:99], v[202:205], v[190:193], v[96:99]
	v_mfma_f32_16x16x32_bf16 v[58:61], v[202:205], v[194:197], v[58:61]
	s_waitcnt lgkmcnt(1)
	v_mfma_f32_16x16x32_bf16 v[144:147], v[206:209], v[164:167], v[144:147]
	v_mfma_f32_16x16x32_bf16 v[86:89], v[206:209], v[190:193], v[86:89]
	v_mfma_f32_16x16x32_bf16 v[54:57], v[206:209], v[194:197], v[54:57]
	s_waitcnt lgkmcnt(0)
	v_mfma_f32_16x16x32_bf16 v[140:143], v[210:213], v[164:167], v[140:143]
	v_mfma_f32_16x16x32_bf16 v[82:85], v[210:213], v[190:193], v[82:85]
	v_mfma_f32_16x16x32_bf16 v[50:53], v[210:213], v[194:197], v[50:53]
	ds_read_b128 v[198:201], v217 offset:8192
	ds_read_b128 v[202:205], v217 offset:10240
	ds_read_b128 v[206:209], v217 offset:12288
	ds_read_b128 v[210:213], v217 offset:14336
	s_min_u32 s33, s2, 5
	s_lshl_b32 s33, s33, 7
	s_waitcnt vmcnt(9)
	ds_write_b128 v189, v[104:107] offset:38912
	s_waitcnt vmcnt(8)
	ds_write_b128 v181, v[92:95] offset:39936
	s_waitcnt vmcnt(7)
	ds_write_b128 v189, v[112:115] offset:40960
	s_waitcnt vmcnt(6)
	ds_write_b128 v181, v[116:119] offset:41984
	s_waitcnt vmcnt(5)
	ds_write_b128 v189, v[100:103] offset:43008
	s_waitcnt vmcnt(4)
	ds_write_b128 v181, v[108:111] offset:44032
	s_addk_i32 s33, 0x100
	s_waitcnt lgkmcnt(9)
	v_mfma_f32_16x16x32_bf16 v[136:139], v[198:201], v[164:167], v[136:139]
	buffer_load_dwordx4 v[92:95], v182, s[4:7], s33 offen
	buffer_load_dwordx4 v[100:103], v183, s[4:7], s33 offen
	buffer_load_dwordx4 v[104:107], v184, s[4:7], s33 offen
	buffer_load_dwordx4 v[108:111], v185, s[4:7], s33 offen
	buffer_load_dwordx4 v[112:115], v186, s[4:7], s33 offen
	buffer_load_dwordx4 v[116:119], v187, s[4:7], s33 offen
	s_min_u32 s33, s2, 3
	s_waitcnt lgkmcnt(0)
	v_mfma_f32_16x16x32_bf16 v[132:135], v[202:205], v[164:167], v[132:135]
	s_barrier
; #define LAS __attribute__((address_space(3)))
; #define MS_WLOAD(set, t) do { _Pragma("unroll") for (int r_ = 0; r_ < 4; ++r_) wr[set][r_] = __builtin_bit_cast(f32x4, __builtin_amdgcn_raw_buffer_load_b128(wrs, (int)wvo + r_ * LDW * 4, MS_CL(t) * (64 * LDW * 4), 0)); } while (0)
; #define MS_WCOMMIT(set, bufi) do { LAS unsigned char* wb_ = lds + (bufi) * MS_TILE; _Pragma("unroll") for (int i_ = 0; i_ < 4; ++i_) { \
;             u32x2 p_; p_.x = pk2(wr[set][0][i_], wr[set][1][i_]); p_.y = pk2(wr[set][2][i_], wr[set][3][i_]); \
;             *(LAS u32x2*)(wb_ + ((i_ < 2) ? lw0 : lw1) + i_ * 128) = p_; } } while (0)
; #define MS_XSLOAD(t) do { _Pragma("unroll") for (int i_ = 0; i_ < 6; ++i_) xs[i_] = __builtin_bit_cast(bf16x8, __builtin_amdgcn_raw_buffer_load_b128(xrs, (int)xso[i_], MS_CL(t) * 128, 0)); } while (0)
; #define MS_XSWRITE(bufi) do { _Pragma("unroll") for (int i_ = 0; i_ < 6; ++i_) *(LAS bf16x8*)(xw + (bufi) * MS_XBUF + i_ * 1024 + ((i_ & 1) ? (xwo ^ 64) : xwo)) = xs[i_]; } while (0)
; #define MS_STEP(I, J, t) do { MS_WCOMMIT(J, J); MS_WLOAD(J, (t) + 3); MS_COMPUTE(I); MS_XSWRITE(J); MS_XSLOAD((t) + 2); __syncthreads(); } while (0)
;     ...
;             const LAS unsigned char* xr1 = lds + MS_XOFF + wave * MS_XWAVE + tk * 128 + (((4 + q) ^ rd_g) << 4);
;             __syncthreads();
;             MS_XSLOAD(0); MS_WLOAD(0, 0); MS_WLOAD(1, 1);
;             MS_WCOMMIT(0, 0); MS_WLOAD(0, 2);
;             MS_XSWRITE(0); MS_XSLOAD(1);
;             __syncthreads();
; #pragma unroll 1
;             for (int t = 0; t < NT; t += 2) { MS_STEP(0, 1, t); MS_STEP(1, 0, t + 1); }
	s_lshl_b32 s33, s33, 19
	v_mfma_f32_16x16x32_bf16 v[128:131], v[206:209], v[164:167], v[128:131]
	s_bitset1_b32 s33, 21
	v_mfma_f32_16x16x32_bf16 v[124:127], v[210:213], v[164:167], v[124:127]
	v_cvt_pk_bf16_f32 v164, v18, v22
	v_cvt_pk_bf16_f32 v165, v26, v30
	v_cvt_pk_bf16_f32 v18, v19, v23
	v_cvt_pk_bf16_f32 v19, v27, v31
	ds_write2_b64 v188, v[164:165], v[18:19] offset1:16
	v_cvt_pk_bf16_f32 v18, v20, v24
	v_cvt_pk_bf16_f32 v19, v28, v32
	v_cvt_pk_bf16_f32 v20, v21, v25
	v_cvt_pk_bf16_f32 v21, v29, v33
	ds_write2_b64 v180, v[18:19], v[20:21] offset0:32 offset1:48
	buffer_load_dwordx4 v[18:21], v160, s[8:11], s33 offen
	buffer_load_dwordx4 v[22:25], v90, s[8:11], s33 offen
	buffer_load_dwordx4 v[26:29], v178, s[8:11], s33 offen
	buffer_load_dwordx4 v[30:33], v179, s[8:11], s33 offen
	v_mfma_f32_16x16x32_bf16 v[78:81], v[198:201], v[190:193], v[78:81]
	v_mfma_f32_16x16x32_bf16 v[46:49], v[198:201], v[194:197], v[46:49]
	v_mfma_f32_16x16x32_bf16 v[74:77], v[202:205], v[190:193], v[74:77]
	v_mfma_f32_16x16x32_bf16 v[42:45], v[202:205], v[194:197], v[42:45]
	v_mfma_f32_16x16x32_bf16 v[70:73], v[206:209], v[190:193], v[70:73]
	v_mfma_f32_16x16x32_bf16 v[38:41], v[206:209], v[194:197], v[38:41]
	v_mfma_f32_16x16x32_bf16 v[66:69], v[210:213], v[190:193], v[66:69]
	v_mfma_f32_16x16x32_bf16 v[34:37], v[210:213], v[194:197], v[34:37]
	ds_read_b128 v[164:167], v214 offset:38912
	ds_read_b128 v[190:193], v214 offset:40960
	ds_read_b128 v[194:197], v214 offset:43008
	ds_read_b128 v[198:201], v215 offset:16384
	ds_read_b128 v[202:205], v215 offset:18432
	ds_read_b128 v[206:209], v215 offset:20480
	ds_read_b128 v[210:213], v215 offset:22528
	s_waitcnt lgkmcnt(3)
	v_mfma_f32_16x16x32_bf16 v[152:155], v[198:201], v[164:167], v[152:155]
	v_mfma_f32_16x16x32_bf16 v[120:123], v[198:201], v[190:193], v[120:123]
	v_mfma_f32_16x16x32_bf16 v[62:65], v[198:201], v[194:197], v[62:65]
	s_waitcnt lgkmcnt(2)
	v_mfma_f32_16x16x32_bf16 v[148:151], v[202:205], v[164:167], v[148:151]
	v_mfma_f32_16x16x32_bf16 v[96:99], v[202:205], v[190:193], v[96:99]
	v_mfma_f32_16x16x32_bf16 v[58:61], v[202:205], v[194:197], v[58:61]
	s_waitcnt lgkmcnt(1)
	v_mfma_f32_16x16x32_bf16 v[144:147], v[206:209], v[164:167], v[144:147]
	v_mfma_f32_16x16x32_bf16 v[86:89], v[206:209], v[190:193], v[86:89]
	v_mfma_f32_16x16x32_bf16 v[54:57], v[206:209], v[194:197], v[54:57]
	s_waitcnt lgkmcnt(0)
	v_mfma_f32_16x16x32_bf16 v[140:143], v[210:213], v[164:167], v[140:143]
	v_mfma_f32_16x16x32_bf16 v[82:85], v[210:213], v[190:193], v[82:85]
	v_mfma_f32_16x16x32_bf16 v[50:53], v[210:213], v[194:197], v[50:53]
	ds_read_b128 v[198:201], v215 offset:24576
	ds_read_b128 v[202:205], v215 offset:26624
	ds_read_b128 v[206:209], v215 offset:28672
	ds_read_b128 v[210:213], v215 offset:30720
	s_waitcnt lgkmcnt(3)
	v_mfma_f32_16x16x32_bf16 v[136:139], v[198:201], v[164:167], v[136:139]
	v_mfma_f32_16x16x32_bf16 v[78:81], v[198:201], v[190:193], v[78:81]
	v_mfma_f32_16x16x32_bf16 v[46:49], v[198:201], v[194:197], v[46:49]
	s_waitcnt lgkmcnt(2)
	v_mfma_f32_16x16x32_bf16 v[132:135], v[202:205], v[164:167], v[132:135]
	v_mfma_f32_16x16x32_bf16 v[74:77], v[202:205], v[190:193], v[74:77]
	v_mfma_f32_16x16x32_bf16 v[42:45], v[202:205], v[194:197], v[42:45]
	s_waitcnt lgkmcnt(1)
	v_mfma_f32_16x16x32_bf16 v[128:131], v[206:209], v[164:167], v[128:131]
	v_mfma_f32_16x16x32_bf16 v[70:73], v[206:209], v[190:193], v[70:73]
	v_mfma_f32_16x16x32_bf16 v[38:41], v[206:209], v[194:197], v[38:41]
	s_waitcnt lgkmcnt(0)
	v_mfma_f32_16x16x32_bf16 v[124:127], v[210:213], v[164:167], v[124:127]
	v_mfma_f32_16x16x32_bf16 v[66:69], v[210:213], v[190:193], v[66:69]
	v_mfma_f32_16x16x32_bf16 v[34:37], v[210:213], v[194:197], v[34:37]
	ds_read_b128 v[164:167], v216 offset:38912
	ds_read_b128 v[190:193], v216 offset:40960
	ds_read_b128 v[194:197], v216 offset:43008
	ds_read_b128 v[198:201], v217 offset:16384
	ds_read_b128 v[202:205], v217 offset:18432
	ds_read_b128 v[206:209], v217 offset:20480
	ds_read_b128 v[210:213], v217 offset:22528
	s_waitcnt lgkmcnt(3)
	v_mfma_f32_16x16x32_bf16 v[152:155], v[198:201], v[164:167], v[152:155]
	v_mfma_f32_16x16x32_bf16 v[120:123], v[198:201], v[190:193], v[120:123]
	v_mfma_f32_16x16x32_bf16 v[62:65], v[198:201], v[194:197], v[62:65]
	s_waitcnt lgkmcnt(2)
	v_mfma_f32_16x16x32_bf16 v[148:151], v[202:205], v[164:167], v[148:151]
	v_mfma_f32_16x16x32_bf16 v[96:99], v[202:205], v[190:193], v[96:99]
	v_mfma_f32_16x16x32_bf16 v[58:61], v[202:205], v[194:197], v[58:61]
	s_waitcnt lgkmcnt(1)
	v_mfma_f32_16x16x32_bf16 v[144:147], v[206:209], v[164:167], v[144:147]
	v_mfma_f32_16x16x32_bf16 v[86:89], v[206:209], v[190:193], v[86:89]
	v_mfma_f32_16x16x32_bf16 v[54:57], v[206:209], v[194:197], v[54:57]
	s_waitcnt lgkmcnt(0)
	v_mfma_f32_16x16x32_bf16 v[140:143], v[210:213], v[164:167], v[140:143]
	v_mfma_f32_16x16x32_bf16 v[82:85], v[210:213], v[190:193], v[82:85]
	v_mfma_f32_16x16x32_bf16 v[50:53], v[210:213], v[194:197], v[50:53]
	ds_read_b128 v[198:201], v217 offset:24576
	ds_read_b128 v[202:205], v217 offset:26624
	ds_read_b128 v[206:209], v217 offset:28672
	ds_read_b128 v[210:213], v217 offset:30720
	s_lshl_b32 s3, s3, 7
	s_waitcnt vmcnt(9)
	ds_write_b128 v189, v[92:95] offset:32768
	s_waitcnt vmcnt(8)
	ds_write_b128 v181, v[100:103] offset:33792
	s_waitcnt vmcnt(7)
	ds_write_b128 v189, v[104:107] offset:34816
	s_waitcnt vmcnt(6)
	ds_write_b128 v181, v[108:111] offset:35840
	s_waitcnt vmcnt(5)
	ds_write_b128 v189, v[112:115] offset:36864
	s_waitcnt vmcnt(4)
	ds_write_b128 v181, v[116:119] offset:37888
	s_addk_i32 s3, 0x180
	buffer_load_dwordx4 v[104:107], v182, s[4:7], s3 offen
	buffer_load_dwordx4 v[92:95], v183, s[4:7], s3 offen
	buffer_load_dwordx4 v[112:115], v184, s[4:7], s3 offen
	buffer_load_dwordx4 v[116:119], v185, s[4:7], s3 offen
	buffer_load_dwordx4 v[100:103], v186, s[4:7], s3 offen
	buffer_load_dwordx4 v[108:111], v187, s[4:7], s3 offen
	s_waitcnt lgkmcnt(9)
	v_mfma_f32_16x16x32_bf16 v[136:139], v[198:201], v[164:167], v[136:139]
	s_cmp_gt_u32 s2, 5
	s_waitcnt lgkmcnt(0)
	s_barrier
	v_mfma_f32_16x16x32_bf16 v[78:81], v[198:201], v[190:193], v[78:81]
	v_mfma_f32_16x16x32_bf16 v[46:49], v[198:201], v[194:197], v[46:49]
	v_mfma_f32_16x16x32_bf16 v[132:135], v[202:205], v[164:167], v[132:135]
	v_mfma_f32_16x16x32_bf16 v[74:77], v[202:205], v[190:193], v[74:77]
	v_mfma_f32_16x16x32_bf16 v[42:45], v[202:205], v[194:197], v[42:45]
	v_mfma_f32_16x16x32_bf16 v[128:131], v[206:209], v[164:167], v[128:131]
	v_mfma_f32_16x16x32_bf16 v[70:73], v[206:209], v[190:193], v[70:73]
	v_mfma_f32_16x16x32_bf16 v[38:41], v[206:209], v[194:197], v[38:41]
	v_mfma_f32_16x16x32_bf16 v[124:127], v[210:213], v[164:167], v[124:127]
	v_mfma_f32_16x16x32_bf16 v[66:69], v[210:213], v[190:193], v[66:69]
	v_mfma_f32_16x16x32_bf16 v[34:37], v[210:213], v[194:197], v[34:37]
	s_cbranch_scc0 .LBB0_1785
	s_branch .Lmoe_l_done
; #define LAS __attribute__((address_space(3)))
; #define MS_WLOAD(set, t) do { _Pragma("unroll") for (int r_ = 0; r_ < 4; ++r_) wr[set][r_] = __builtin_bit_cast(f32x4, __builtin_amdgcn_raw_buffer_load_b128(wrs, (int)wvo + r_ * LDW * 4, MS_CL(t) * (64 * LDW * 4), 0)); } while (0)
; #define MS_WCOMMIT(set, bufi) do { LAS unsigned char* wb_ = lds + (bufi) * MS_TILE; _Pragma("unroll") for (int i_ = 0; i_ < 4; ++i_) { \
;             u32x2 p_; p_.x = pk2(wr[set][0][i_], wr[set][1][i_]); p_.y = pk2(wr[set][2][i_], wr[set][3][i_]); \
;             *(LAS u32x2*)(wb_ + ((i_ < 2) ? lw0 : lw1) + i_ * 128) = p_; } } while (0)
; #define MS_XSLOAD(t) do { _Pragma("unroll") for (int i_ = 0; i_ < 6; ++i_) xs[i_] = __builtin_bit_cast(bf16x8, __builtin_amdgcn_raw_buffer_load_b128(xrs, (int)xso[i_], MS_CL(t) * 128, 0)); } while (0)
; #define MS_XSWRITE(bufi) do { _Pragma("unroll") for (int i_ = 0; i_ < 6; ++i_) *(LAS bf16x8*)(xw + (bufi) * MS_XBUF + i_ * 1024 + ((i_ & 1) ? (xwo ^ 64) : xwo)) = xs[i_]; } while (0)
; #define MS_STEP(I, J, t) do { MS_WCOMMIT(J, J); MS_WLOAD(J, (t) + 3); MS_COMPUTE(I); MS_XSWRITE(J); MS_XSLOAD((t) + 2); __syncthreads(); } while (0)
;     ...
;             const LAS unsigned char* xr1 = lds + MS_XOFF + wave * MS_XWAVE + tk * 128 + (((4 + q) ^ rd_g) << 4);
;             __syncthreads();
;             MS_XSLOAD(0); MS_WLOAD(0, 0); MS_WLOAD(1, 1);
;             MS_WCOMMIT(0, 0); MS_WLOAD(0, 2);
;             MS_XSWRITE(0); MS_XSLOAD(1);
;             __syncthreads();
; #pragma unroll 1
;             for (int t = 0; t < NT; t += 2) { MS_STEP(0, 1, t); MS_STEP(1, 0, t + 1); }
.Lmoe_l_b:
	s_add_i32 s2, s2, 2
	s_min_u32 s3, s2, 4
	s_lshl_b32 s33, s3, 19
	s_add_i32 s33, s33, 0x180000
	s_waitcnt vmcnt(10)
	v_cvt_pk_bf16_f32 v164, v2, v10
	s_waitcnt vmcnt(7)
	v_cvt_pk_bf16_f32 v165, v6, v14
	v_cvt_pk_bf16_f32 v166, v3, v11
	v_cvt_pk_bf16_f32 v167, v7, v15
	v_cvt_pk_bf16_f32 v190, v4, v12
	v_cvt_pk_bf16_f32 v191, v8, v16
	v_cvt_pk_bf16_f32 v192, v5, v13
	v_cvt_pk_bf16_f32 v193, v9, v17
	buffer_load_dwordx4 v[2:5], v160, s[8:11], s33 offen
	buffer_load_dwordx4 v[10:13], v90, s[8:11], s33 offen
	buffer_load_dwordx4 v[6:9], v178, s[8:11], s33 offen
	buffer_load_dwordx4 v[14:17], v179, s[8:11], s33 offen
	v_add_u32_e32 v194, 0x4000, v188
	v_add_u32_e32 v195, 0x4000, v180
	v_add_u32_e32 v214, v173, v174
	ds_write2_b64 v194, v[164:165], v[166:167] offset1:16
	ds_write2_b64 v195, v[190:191], v[192:193] offset0:32 offset1:48
	v_add_u32_e32 v215, v176, v174
	ds_read_b128 v[164:167], v214 offset:32768
	ds_read_b128 v[190:193], v214 offset:34816
	ds_read_b128 v[198:201], v215
	ds_read_b128 v[202:205], v215 offset:2048
	ds_read_b128 v[206:209], v215 offset:4096
	ds_read_b128 v[210:213], v215 offset:6144
	s_waitcnt lgkmcnt(3)
	v_mfma_f32_16x16x32_bf16 v[152:155], v[198:201], v[164:167], v[152:155]
	v_mfma_f32_16x16x32_bf16 v[120:123], v[198:201], v[190:193], v[120:123]
	s_waitcnt lgkmcnt(2)
	v_mfma_f32_16x16x32_bf16 v[148:151], v[202:205], v[164:167], v[148:151]
	v_mfma_f32_16x16x32_bf16 v[96:99], v[202:205], v[190:193], v[96:99]
	s_waitcnt lgkmcnt(1)
	v_mfma_f32_16x16x32_bf16 v[144:147], v[206:209], v[164:167], v[144:147]
	v_mfma_f32_16x16x32_bf16 v[86:89], v[206:209], v[190:193], v[86:89]
	s_waitcnt lgkmcnt(0)
	v_mfma_f32_16x16x32_bf16 v[140:143], v[210:213], v[164:167], v[140:143]
	v_mfma_f32_16x16x32_bf16 v[82:85], v[210:213], v[190:193], v[82:85]
	ds_read_b128 v[198:201], v215 offset:8192
	ds_read_b128 v[202:205], v215 offset:10240
	ds_read_b128 v[206:209], v215 offset:12288
	ds_read_b128 v[210:213], v215 offset:14336
	s_waitcnt lgkmcnt(3)
	v_mfma_f32_16x16x32_bf16 v[136:139], v[198:201], v[164:167], v[136:139]
	v_mfma_f32_16x16x32_bf16 v[78:81], v[198:201], v[190:193], v[78:81]
	s_waitcnt lgkmcnt(2)
	v_mfma_f32_16x16x32_bf16 v[132:135], v[202:205], v[164:167], v[132:135]
	v_mfma_f32_16x16x32_bf16 v[74:77], v[202:205], v[190:193], v[74:77]
	s_waitcnt lgkmcnt(1)
	v_mfma_f32_16x16x32_bf16 v[128:131], v[206:209], v[164:167], v[128:131]
	v_mfma_f32_16x16x32_bf16 v[70:73], v[206:209], v[190:193], v[70:73]
	s_waitcnt lgkmcnt(0)
	v_mfma_f32_16x16x32_bf16 v[124:127], v[210:213], v[164:167], v[124:127]
	v_mfma_f32_16x16x32_bf16 v[66:69], v[210:213], v[190:193], v[66:69]
	v_add_u32_e32 v216, v173, v175
	ds_read_b128 v[164:167], v216 offset:32768
	ds_read_b128 v[190:193], v216 offset:34816
	v_add_u32_e32 v217, v176, v175
	ds_read_b128 v[198:201], v217
	ds_read_b128 v[202:205], v217 offset:2048
	ds_read_b128 v[206:209], v217 offset:4096
	ds_read_b128 v[210:213], v217 offset:6144
	s_waitcnt lgkmcnt(3)
	v_mfma_f32_16x16x32_bf16 v[152:155], v[198:201], v[164:167], v[152:155]
	v_mfma_f32_16x16x32_bf16 v[120:123], v[198:201], v[190:193], v[120:123]
	s_waitcnt lgkmcnt(2)
	v_mfma_f32_16x16x32_bf16 v[148:151], v[202:205], v[164:167], v[148:151]
	v_mfma_f32_16x16x32_bf16 v[96:99], v[202:205], v[190:193], v[96:99]
	s_waitcnt lgkmcnt(1)
	v_mfma_f32_16x16x32_bf16 v[144:147], v[206:209], v[164:167], v[144:147]
	v_mfma_f32_16x16x32_bf16 v[86:89], v[206:209], v[190:193], v[86:89]
	s_waitcnt lgkmcnt(0)
	v_mfma_f32_16x16x32_bf16 v[140:143], v[210:213], v[164:167], v[140:143]
	v_mfma_f32_16x16x32_bf16 v[82:85], v[210:213], v[190:193], v[82:85]
	ds_read_b128 v[198:201], v217 offset:8192
	ds_read_b128 v[202:205], v217 offset:10240
	ds_read_b128 v[206:209], v217 offset:12288
	ds_read_b128 v[210:213], v217 offset:14336
	s_min_u32 s33, s2, 5
	s_lshl_b32 s33, s33, 7
	s_waitcnt vmcnt(9)
	ds_write_b128 v189, v[104:107] offset:38912
	s_waitcnt vmcnt(8)
	ds_write_b128 v181, v[92:95] offset:39936
	s_waitcnt vmcnt(7)
	ds_write_b128 v189, v[112:115] offset:40960
	s_waitcnt vmcnt(6)
	ds_write_b128 v181, v[116:119] offset:41984
	s_waitcnt vmcnt(5)
	ds_write_b128 v189, v[100:103] offset:43008
	s_waitcnt vmcnt(4)
	ds_write_b128 v181, v[108:111] offset:44032
	s_addk_i32 s33, 0x100
	s_waitcnt lgkmcnt(9)
	v_mfma_f32_16x16x32_bf16 v[136:139], v[198:201], v[164:167], v[136:139]
	buffer_load_dwordx4 v[92:95], v182, s[4:7], s33 offen
	buffer_load_dwordx4 v[100:103], v183, s[4:7], s33 offen
	buffer_load_dwordx4 v[104:107], v184, s[4:7], s33 offen
	buffer_load_dwordx4 v[108:111], v185, s[4:7], s33 offen
	buffer_load_dwordx4 v[112:115], v186, s[4:7], s33 offen
	buffer_load_dwordx4 v[116:119], v187, s[4:7], s33 offen
	s_min_u32 s33, s2, 3
	s_waitcnt lgkmcnt(0)
	v_mfma_f32_16x16x32_bf16 v[132:135], v[202:205], v[164:167], v[132:135]
	s_barrier
; #define LAS __attribute__((address_space(3)))
; #define MS_WLOAD(set, t) do { _Pragma("unroll") for (int r_ = 0; r_ < 4; ++r_) wr[set][r_] = __builtin_bit_cast(f32x4, __builtin_amdgcn_raw_buffer_load_b128(wrs, (int)wvo + r_ * LDW * 4, MS_CL(t) * (64 * LDW * 4), 0)); } while (0)
; #define MS_WCOMMIT(set, bufi) do { LAS unsigned char* wb_ = lds + (bufi) * MS_TILE; _Pragma("unroll") for (int i_ = 0; i_ < 4; ++i_) { \
;             u32x2 p_; p_.x = pk2(wr[set][0][i_], wr[set][1][i_]); p_.y = pk2(wr[set][2][i_], wr[set][3][i_]); \
;             *(LAS u32x2*)(wb_ + ((i_ < 2) ? lw0 : lw1) + i_ * 128) = p_; } } while (0)
; #define MS_XSLOAD(t) do { _Pragma("unroll") for (int i_ = 0; i_ < 6; ++i_) xs[i_] = __builtin_bit_cast(bf16x8, __builtin_amdgcn_raw_buffer_load_b128(xrs, (int)xso[i_], MS_CL(t) * 128, 0)); } while (0)
; #define MS_XSWRITE(bufi) do { _Pragma("unroll") for (int i_ = 0; i_ < 6; ++i_) *(LAS bf16x8*)(xw + (bufi) * MS_XBUF + i_ * 1024 + ((i_ & 1) ? (xwo ^ 64) : xwo)) = xs[i_]; } while (0)
; #define MS_STEP(I, J, t) do { MS_WCOMMIT(J, J); MS_WLOAD(J, (t) + 3); MS_COMPUTE(I); MS_XSWRITE(J); MS_XSLOAD((t) + 2); __syncthreads(); } while (0)
;     ...
;             const LAS unsigned char* xr1 = lds + MS_XOFF + wave * MS_XWAVE + tk * 128 + (((4 + q) ^ rd_g) << 4);
;             __syncthreads();
;             MS_XSLOAD(0); MS_WLOAD(0, 0); MS_WLOAD(1, 1);
;             MS_WCOMMIT(0, 0); MS_WLOAD(0, 2);
;             MS_XSWRITE(0); MS_XSLOAD(1);
;             __syncthreads();
; #pragma unroll 1
;             for (int t = 0; t < NT; t += 2) { MS_STEP(0, 1, t); MS_STEP(1, 0, t + 1); }
	s_lshl_b32 s33, s33, 19
	v_mfma_f32_16x16x32_bf16 v[128:131], v[206:209], v[164:167], v[128:131]
	s_bitset1_b32 s33, 21
	v_mfma_f32_16x16x32_bf16 v[124:127], v[210:213], v[164:167], v[124:127]
	v_cvt_pk_bf16_f32 v164, v18, v22
	v_cvt_pk_bf16_f32 v165, v26, v30
	v_cvt_pk_bf16_f32 v18, v19, v23
	v_cvt_pk_bf16_f32 v19, v27, v31
	ds_write2_b64 v188, v[164:165], v[18:19] offset1:16
	v_cvt_pk_bf16_f32 v18, v20, v24
	v_cvt_pk_bf16_f32 v19, v28, v32
	v_cvt_pk_bf16_f32 v20, v21, v25
	v_cvt_pk_bf16_f32 v21, v29, v33
	ds_write2_b64 v180, v[18:19], v[20:21] offset0:32 offset1:48
	buffer_load_dwordx4 v[18:21], v160, s[8:11], s33 offen
	buffer_load_dwordx4 v[22:25], v90, s[8:11], s33 offen
	buffer_load_dwordx4 v[26:29], v178, s[8:11], s33 offen
	buffer_load_dwordx4 v[30:33], v179, s[8:11], s33 offen
	v_mfma_f32_16x16x32_bf16 v[78:81], v[198:201], v[190:193], v[78:81]
	v_mfma_f32_16x16x32_bf16 v[74:77], v[202:205], v[190:193], v[74:77]
	v_mfma_f32_16x16x32_bf16 v[70:73], v[206:209], v[190:193], v[70:73]
	v_mfma_f32_16x16x32_bf16 v[66:69], v[210:213], v[190:193], v[66:69]
	ds_read_b128 v[164:167], v214 offset:38912
	ds_read_b128 v[190:193], v214 offset:40960
	ds_read_b128 v[198:201], v215 offset:16384
	ds_read_b128 v[202:205], v215 offset:18432
	ds_read_b128 v[206:209], v215 offset:20480
	ds_read_b128 v[210:213], v215 offset:22528
	s_waitcnt lgkmcnt(3)
	v_mfma_f32_16x16x32_bf16 v[152:155], v[198:201], v[164:167], v[152:155]
	v_mfma_f32_16x16x32_bf16 v[120:123], v[198:201], v[190:193], v[120:123]
	s_waitcnt lgkmcnt(2)
	v_mfma_f32_16x16x32_bf16 v[148:151], v[202:205], v[164:167], v[148:151]
	v_mfma_f32_16x16x32_bf16 v[96:99], v[202:205], v[190:193], v[96:99]
	s_waitcnt lgkmcnt(1)
	v_mfma_f32_16x16x32_bf16 v[144:147], v[206:209], v[164:167], v[144:147]
	v_mfma_f32_16x16x32_bf16 v[86:89], v[206:209], v[190:193], v[86:89]
	s_waitcnt lgkmcnt(0)
	v_mfma_f32_16x16x32_bf16 v[140:143], v[210:213], v[164:167], v[140:143]
	v_mfma_f32_16x16x32_bf16 v[82:85], v[210:213], v[190:193], v[82:85]
	ds_read_b128 v[198:201], v215 offset:24576
	ds_read_b128 v[202:205], v215 offset:26624
	ds_read_b128 v[206:209], v215 offset:28672
	ds_read_b128 v[210:213], v215 offset:30720
	s_waitcnt lgkmcnt(3)
	v_mfma_f32_16x16x32_bf16 v[136:139], v[198:201], v[164:167], v[136:139]
	v_mfma_f32_16x16x32_bf16 v[78:81], v[198:201], v[190:193], v[78:81]
	s_waitcnt lgkmcnt(2)
	v_mfma_f32_16x16x32_bf16 v[132:135], v[202:205], v[164:167], v[132:135]
	v_mfma_f32_16x16x32_bf16 v[74:77], v[202:205], v[190:193], v[74:77]
	s_waitcnt lgkmcnt(1)
	v_mfma_f32_16x16x32_bf16 v[128:131], v[206:209], v[164:167], v[128:131]
	v_mfma_f32_16x16x32_bf16 v[70:73], v[206:209], v[190:193], v[70:73]
	s_waitcnt lgkmcnt(0)
	v_mfma_f32_16x16x32_bf16 v[124:127], v[210:213], v[164:167], v[124:127]
	v_mfma_f32_16x16x32_bf16 v[66:69], v[210:213], v[190:193], v[66:69]
	ds_read_b128 v[164:167], v216 offset:38912
	ds_read_b128 v[190:193], v216 offset:40960
	ds_read_b128 v[198:201], v217 offset:16384
	ds_read_b128 v[202:205], v217 offset:18432
	ds_read_b128 v[206:209], v217 offset:20480
	ds_read_b128 v[210:213], v217 offset:22528
	s_waitcnt lgkmcnt(3)
	v_mfma_f32_16x16x32_bf16 v[152:155], v[198:201], v[164:167], v[152:155]
	v_mfma_f32_16x16x32_bf16 v[120:123], v[198:201], v[190:193], v[120:123]
	s_waitcnt lgkmcnt(2)
	v_mfma_f32_16x16x32_bf16 v[148:151], v[202:205], v[164:167], v[148:151]
	v_mfma_f32_16x16x32_bf16 v[96:99], v[202:205], v[190:193], v[96:99]
	s_waitcnt lgkmcnt(1)
	v_mfma_f32_16x16x32_bf16 v[144:147], v[206:209], v[164:167], v[144:147]
	v_mfma_f32_16x16x32_bf16 v[86:89], v[206:209], v[190:193], v[86:89]
	s_waitcnt lgkmcnt(0)
	v_mfma_f32_16x16x32_bf16 v[140:143], v[210:213], v[164:167], v[140:143]
	v_mfma_f32_16x16x32_bf16 v[82:85], v[210:213], v[190:193], v[82:85]
	ds_read_b128 v[198:201], v217 offset:24576
	ds_read_b128 v[202:205], v217 offset:26624
	ds_read_b128 v[206:209], v217 offset:28672
	ds_read_b128 v[210:213], v217 offset:30720
	s_lshl_b32 s3, s3, 7
	s_waitcnt vmcnt(9)
	ds_write_b128 v189, v[92:95] offset:32768
	s_waitcnt vmcnt(8)
	ds_write_b128 v181, v[100:103] offset:33792
	s_waitcnt vmcnt(7)
	ds_write_b128 v189, v[104:107] offset:34816
	s_waitcnt vmcnt(6)
	ds_write_b128 v181, v[108:111] offset:35840
	s_waitcnt vmcnt(5)
	ds_write_b128 v189, v[112:115] offset:36864
	s_waitcnt vmcnt(4)
	ds_write_b128 v181, v[116:119] offset:37888
	s_addk_i32 s3, 0x180
	buffer_load_dwordx4 v[104:107], v182, s[4:7], s3 offen
	buffer_load_dwordx4 v[92:95], v183, s[4:7], s3 offen
	buffer_load_dwordx4 v[112:115], v184, s[4:7], s3 offen
	buffer_load_dwordx4 v[116:119], v185, s[4:7], s3 offen
	buffer_load_dwordx4 v[100:103], v186, s[4:7], s3 offen
	buffer_load_dwordx4 v[108:111], v187, s[4:7], s3 offen
	s_waitcnt lgkmcnt(9)
	v_mfma_f32_16x16x32_bf16 v[136:139], v[198:201], v[164:167], v[136:139]
	s_cmp_gt_u32 s2, 5
	s_waitcnt lgkmcnt(0)
	s_barrier
	v_mfma_f32_16x16x32_bf16 v[78:81], v[198:201], v[190:193], v[78:81]
	v_mfma_f32_16x16x32_bf16 v[132:135], v[202:205], v[164:167], v[132:135]
	v_mfma_f32_16x16x32_bf16 v[74:77], v[202:205], v[190:193], v[74:77]
	v_mfma_f32_16x16x32_bf16 v[128:131], v[206:209], v[164:167], v[128:131]
	v_mfma_f32_16x16x32_bf16 v[70:73], v[206:209], v[190:193], v[70:73]
	v_mfma_f32_16x16x32_bf16 v[124:127], v[210:213], v[164:167], v[124:127]
	v_mfma_f32_16x16x32_bf16 v[66:69], v[210:213], v[190:193], v[66:69]
	s_cbranch_scc0 .Lmoe_l_b
; DI unsigned pk2(float a, float b) { f32x2 v = {a, b}; bf16x2_t r = __builtin_convertvector(v, bf16x2_t); return __builtin_bit_cast(unsigned, r); }
; DI float sigmoidf_(float x) { return 1.f / (1.f + __expf(-x)); }
;     ...
; #pragma unroll
;             for (int mt = 0; mt < 3; ++mt) { const int tok = rp + wave * 48 + mt * 16 + tk;
;                 if (tok < M) {
;                     if (MODE == 0) { bf16* o = (bf16*)(ws + o_hid) + (size_t)(row0 + tok) * DEXP + slab * 64 + 4 * q;
; #pragma unroll
;                         for (int j = 0; j < 4; ++j) { float h[4];
; #pragma unroll
;                             for (int i = 0; i < 4; ++i) { const float gt = acc[mt][j][i]; h[i] = gt * sigmoidf_(gt) * acc[mt][j + 4][i]; }
;                             *(u32x2*)(o + 16 * j) = (u32x2){pk2(h[0], h[1]), pk2(h[2], h[3])}; }
;                     } else { bf16* o = (bf16*)(ws + o_yr) + (size_t)(row0 + tok) * D + slab * 128 + 4 * q;
; #pragma unroll
;                         for (int j = 0; j < 8; ++j) *(u32x2*)(o + 16 * j) = (u32x2){pk2(acc[mt][j][0], acc[mt][j][1]), pk2(acc[mt][j][2], acc[mt][j][3])}; } } }
.Lmoe_l_done:
	v_add_u32_e32 v2, s31, v177
	v_cmp_gt_i32_e32 vcc, s30, v2
	s_and_saveexec_b64 s[2:3], vcc
	s_cbranch_execz .LBB0_1788
	v_add_u32_e32 v4, s24, v2
	v_ashrrev_i32_e32 v5, 31, v4
	v_lshlrev_b64 v[4:5], 12, v[4:5]
	v_lshl_add_u64 v[4:5], v[158:159], 0, v[4:5]
	v_cvt_pk_bf16_f32 v6, v152, v153
	v_cvt_pk_bf16_f32 v7, v154, v155
	global_store_dwordx2 v[4:5], v[6:7], off
	v_cvt_pk_bf16_f32 v6, v148, v149
	v_cvt_pk_bf16_f32 v7, v150, v151
	global_store_dwordx2 v[4:5], v[6:7], off offset:32
	v_cvt_pk_bf16_f32 v6, v144, v145
	v_cvt_pk_bf16_f32 v7, v146, v147
	global_store_dwordx2 v[4:5], v[6:7], off offset:64
	v_cvt_pk_bf16_f32 v6, v140, v141
	v_cvt_pk_bf16_f32 v7, v142, v143
	global_store_dwordx2 v[4:5], v[6:7], off offset:96
	v_cvt_pk_bf16_f32 v6, v136, v137
	v_cvt_pk_bf16_f32 v7, v138, v139
	global_store_dwordx2 v[4:5], v[6:7], off offset:128
	v_cvt_pk_bf16_f32 v6, v132, v133
	v_cvt_pk_bf16_f32 v7, v134, v135
	global_store_dwordx2 v[4:5], v[6:7], off offset:160
	v_cvt_pk_bf16_f32 v6, v128, v129
	v_cvt_pk_bf16_f32 v7, v130, v131
	global_store_dwordx2 v[4:5], v[6:7], off offset:192
	v_cvt_pk_bf16_f32 v6, v124, v125
	v_cvt_pk_bf16_f32 v7, v126, v127
	global_store_dwordx2 v[4:5], v[6:7], off offset:224
.LBB0_1788:
	s_or_b64 exec, exec, s[2:3]
	v_add_u32_e32 v3, 0x80, v2
	v_cmp_gt_i32_e32 vcc, s30, v3
	s_and_saveexec_b64 s[2:3], vcc
	s_cbranch_execz .LBB0_1790
	v_add_u32_e32 v4, s24, v3
	v_ashrrev_i32_e32 v5, 31, v4
	v_lshlrev_b64 v[4:5], 12, v[4:5]
	v_lshl_add_u64 v[4:5], v[158:159], 0, v[4:5]
	v_cvt_pk_bf16_f32 v6, v120, v121
	v_cvt_pk_bf16_f32 v7, v122, v123
	global_store_dwordx2 v[4:5], v[6:7], off
	v_cvt_pk_bf16_f32 v6, v96, v97
	v_cvt_pk_bf16_f32 v7, v98, v99
	global_store_dwordx2 v[4:5], v[6:7], off offset:32
	v_cvt_pk_bf16_f32 v6, v86, v87
	v_cvt_pk_bf16_f32 v7, v88, v89
	global_store_dwordx2 v[4:5], v[6:7], off offset:64
	v_cvt_pk_bf16_f32 v6, v82, v83
	v_cvt_pk_bf16_f32 v7, v84, v85
	global_store_dwordx2 v[4:5], v[6:7], off offset:96
	v_cvt_pk_bf16_f32 v6, v78, v79
	v_cvt_pk_bf16_f32 v7, v80, v81
	global_store_dwordx2 v[4:5], v[6:7], off offset:128
	v_cvt_pk_bf16_f32 v6, v74, v75
	v_cvt_pk_bf16_f32 v7, v76, v77
	global_store_dwordx2 v[4:5], v[6:7], off offset:160
	v_cvt_pk_bf16_f32 v6, v70, v71
	v_cvt_pk_bf16_f32 v7, v72, v73
	global_store_dwordx2 v[4:5], v[6:7], off offset:192
	v_cvt_pk_bf16_f32 v6, v66, v67
	v_cvt_pk_bf16_f32 v7, v68, v69
	global_store_dwordx2 v[4:5], v[6:7], off offset:224
.LBB0_1790:
	s_or_b64 exec, exec, s[2:3]
	v_add_u32_e32 v2, 0x100, v2
	v_cmp_gt_i32_e32 vcc, s30, v2
	s_and_saveexec_b64 s[2:3], vcc
	s_cbranch_execz .LBB0_1783
	v_add_u32_e32 v2, s24, v2
	v_ashrrev_i32_e32 v3, 31, v2
	v_lshlrev_b64 v[2:3], 12, v[2:3]
	v_lshl_add_u64 v[2:3], v[158:159], 0, v[2:3]
	v_cvt_pk_bf16_f32 v4, v62, v63
	v_cvt_pk_bf16_f32 v5, v64, v65
	global_store_dwordx2 v[2:3], v[4:5], off
	v_cvt_pk_bf16_f32 v4, v58, v59
	v_cvt_pk_bf16_f32 v5, v60, v61
	global_store_dwordx2 v[2:3], v[4:5], off offset:32
	v_cvt_pk_bf16_f32 v4, v54, v55
	v_cvt_pk_bf16_f32 v5, v56, v57
	global_store_dwordx2 v[2:3], v[4:5], off offset:64
	v_cvt_pk_bf16_f32 v4, v50, v51
	v_cvt_pk_bf16_f32 v5, v52, v53
	global_store_dwordx2 v[2:3], v[4:5], off offset:96
	v_cvt_pk_bf16_f32 v4, v46, v47
	v_cvt_pk_bf16_f32 v5, v48, v49
	global_store_dwordx2 v[2:3], v[4:5], off offset:128
	v_cvt_pk_bf16_f32 v4, v42, v43
	v_cvt_pk_bf16_f32 v5, v44, v45
	global_store_dwordx2 v[2:3], v[4:5], off offset:160
	v_cvt_pk_bf16_f32 v4, v38, v39
	v_cvt_pk_bf16_f32 v5, v40, v41
	global_store_dwordx2 v[2:3], v[4:5], off offset:192
	v_cvt_pk_bf16_f32 v4, v34, v35
	v_cvt_pk_bf16_f32 v5, v36, v37
	global_store_dwordx2 v[2:3], v[4:5], off offset:224
	s_branch .LBB0_1783
